# retention q/k projection tiles written by the in-proj epilogue in MFMA-fragment order to the unused 64 MiB workspace slot; P3 query/key fragment loads and the scan key pieces read that copy (lane-cont
# speedup vs baseline: 1.0130x; 1.0074x over previous
;     __device__ __forceinline__ void operator()(const f32x4 (&acc)[2][2][4][2], const Unit& u, int wr, int wc, int fr, int fq) const {
;     ...
;                 const int row = row0 + ai * HALF + m * 16, pos = row & (MS - 1);
;                 const float rs = rstd[row];
; #pragma unroll
;                 for (int bj = 0; bj < 2; ++bj) {
;                     const int c0 = u.pn * BM + bj * HALF + wc * 32 + 8 * fq;
;                     f32x4 v0 = acc[ai][bj][m][0] * rs, v1 = acc[ai][bj][m][1] * rs;
;                     if (kind <= 1) {
;                         float s = (v0[0] * v0[0] + v0[1] * v0[1]) + (v0[2] * v0[2] + v0[3] * v0[3]) + (v1[0] * v1[0] + v1[1] * v1[1]) + (v1[2] * v1[2] + v1[3] * v1[3]);
;                         s += __shfl_xor(s, 16); s += __shfl_xor(s, 32);
;                         const int head = (u.pn & 3) * 2 + bj;
;                         if (fq == 0) ssq[(size_t)((kind * 8 + head) * 4 + wc) * MT + row] = s;
;                     } else if (kind <= 3) {
;                         const int i0 = (c0 & 127) >> 1;
;                         const f32x4 csa = *(const f32x4*)(cs + (size_t)pos * 64 + i0), csb = *(const f32x4*)(cs + (size_t)pos * 64 + i0 + 2);
;                         const float sc = (kind == 3) ? KSCALE : 1.0f;
;                         f32x4 w0, w1;
;                         w0[0] = (v0[0] * csa[0] - v0[1] * csa[1]) * sc; w0[1] = (v0[1] * csa[0] + v0[0] * csa[1]) * sc;
;                         w0[2] = (v0[2] * csa[2] - v0[3] * csa[3]) * sc; w0[3] = (v0[3] * csa[2] + v0[2] * csa[3]) * sc;
;                         w1[0] = (v1[0] * csb[0] - v1[1] * csb[1]) * sc; w1[1] = (v1[1] * csb[0] + v1[0] * csb[1]) * sc;
;                         w1[2] = (v1[2] * csb[2] - v1[3] * csb[3]) * sc; w1[3] = (v1[3] * csb[2] + v1[2] * csb[3]) * sc;
;                         v0 = w0; v1 = w1;
;                     } else {
; #pragma unroll
;                         for (int j = 0; j < 4; ++j) { v0[j] = v0[j] * __builtin_amdgcn_rcpf(1.0f + __builtin_amdgcn_exp2f(-1.4426950408889634f * v0[j]));
;                                                       v1[j] = v1[j] * __builtin_amdgcn_rcpf(1.0f + __builtin_amdgcn_exp2f(-1.4426950408889634f * v1[j])); }
.LBB0_226:
	s_add_i32 s100, s66, -8
	v_mov_b32_e32 v240, s100
	s_cmp_lt_u32 s100, 8
	s_cselect_b32 s100, -1, 0
	s_mov_b32 s101, s100
	v_lshlrev_b32_e32 v240, 13, v240
	v_lshl_add_u32 v240, v161, 5, v240
	v_and_b32_e32 v241, 15, v159
	v_lshl_add_u32 v240, v241, 4, v240
	v_add_u32_e32 v240, 0xe000000, v240
	v_mov_b32_e32 v241, 0
	v_mov_b32_e32 v238, s62
	v_mov_b32_e32 v239, s63
	v_lshl_add_u64 v[238:239], v[238:239], 0, v[240:241]
	v_mov_b32_e32 v242, 0x100
	v_mov_b32_e32 v244, 0x1000
	v_cndmask_b32_e64 v242, v242, v244, s[100:101]
	v_mov_b32_e32 v243, 0
	v_lshl_add_u32 v142, s38, 8, v159
	v_readlane_b32 s56, v250, 22
	v_ashrrev_i32_e32 v143, 31, v142
	v_readlane_b32 s57, v250, 23
	s_ashr_i32 s4, s66, 2
	s_cmp_gt_i32 s4, 1
	v_lshl_add_u64 v[146:147], v[142:143], 2, s[56:57]
	global_load_dword v148, v[146:147], off
	global_load_dword v226, v[146:147], off offset:64
	global_load_dword v227, v[146:147], off offset:128
	global_load_dword v228, v[146:147], off offset:192
	global_load_dword v229, v[146:147], off offset:512
	global_load_dword v230, v[146:147], off offset:576
	global_load_dword v231, v[146:147], off offset:640
	global_load_dword v232, v[146:147], off offset:704
	s_cselect_b64 s[0:1], -1, 0
	s_cmp_gt_u32 s4, 3
	s_cselect_b64 s[8:9], -1, 0
	s_cmp_eq_u32 s4, 3
	v_lshlrev_b32_e32 v149, 6, v142
	s_cselect_b64 vcc, -1, 0
	v_and_b32_e32 v163, 0x1f3c0, v149
	v_cndmask_b32_e32 v144, 1.0, v220, vcc
	s_mov_b64 s[2:3], -1
	s_and_b64 vcc, exec, s[0:1]
	s_waitcnt vmcnt(0)
	v_pk_mul_f32 v[126:127], v[126:127], v[148:149] op_sel_hi:[1,0]
	v_pk_mul_f32 v[124:125], v[124:125], v[148:149] op_sel_hi:[1,0]
	v_pk_mul_f32 v[122:123], v[122:123], v[148:149] op_sel_hi:[1,0]
	v_pk_mul_f32 v[120:121], v[120:121], v[148:149] op_sel_hi:[1,0]
	v_cndmask_b32_e64 v149, 0, 1, s[8:9]
	v_cmp_ne_u32_e64 s[38:39], 1, v149
	s_cbranch_vccz .LBB0_232
	s_and_b64 vcc, exec, s[38:39]
	s_cbranch_vccnz .LBB0_229
	v_mul_f32_e32 v149, 0xbfb8aa3b, v124
	v_exp_f32_e32 v149, v149
	v_mul_f32_e32 v150, 0xbfb8aa3b, v120
	v_mul_f32_e32 v151, 0xbfb8aa3b, v125
	v_exp_f32_e32 v152, v150
	v_exp_f32_e32 v151, v151
	v_add_f32_e32 v149, 1.0, v149
	v_rcp_f32_e32 v150, v149
	v_add_f32_e32 v149, 1.0, v152
	v_rcp_f32_e32 v154, v149
	v_add_f32_e32 v149, 1.0, v151
	v_mul_f32_e32 v153, 0xbfb8aa3b, v122
	v_rcp_f32_e32 v151, v149
	v_mul_f32_e32 v149, 0xbfb8aa3b, v121
	v_mul_f32_e32 v152, 0xbfb8aa3b, v126
	v_exp_f32_e32 v153, v153
	v_mul_f32_e32 v155, 0xbfb8aa3b, v127
	v_mul_f32_e32 v156, 0xbfb8aa3b, v123
	v_exp_f32_e32 v149, v149
	v_exp_f32_e32 v152, v152
	v_exp_f32_e32 v155, v155
	v_exp_f32_e32 v157, v156
	v_add_f32_e32 v153, 1.0, v153
	v_add_f32_e32 v149, 1.0, v149
	v_add_f32_e32 v152, 1.0, v152
	v_rcp_f32_e32 v156, v153
	v_add_f32_e32 v153, 1.0, v155
	v_add_f32_e32 v155, 1.0, v157
	v_rcp_f32_e32 v152, v152
	v_rcp_f32_e32 v153, v153
	v_rcp_f32_e32 v157, v155
	v_rcp_f32_e32 v155, v149
	v_pk_mul_f32 v[150:151], v[124:125], v[150:151]
	v_pk_mul_f32 v[152:153], v[126:127], v[152:153]
	v_pk_mul_f32 v[156:157], v[122:123], v[156:157]
	v_pk_mul_f32 v[154:155], v[120:121], v[154:155]
	s_mov_b64 s[2:3], 0
.LBB0_229:
	s_andn2_b64 vcc, exec, s[2:3]
	s_cbranch_vccnz .LBB0_231
	v_lshlrev_b32_e32 v184, 3, v163
	v_lshl_add_u64 v[150:151], v[136:137], 0, v[184:185]
	v_mov_b32_e32 v236, v150
	v_mov_b32_e32 v237, v151
	global_load_dwordx4 v[168:171], v[236:237], off
	global_load_dwordx4 v[172:175], v[236:237], off offset:16
	v_add_co_u32_e32 v234, vcc, 0x2000, v236
	s_nop 1
	v_addc_co_u32_e32 v235, vcc, 0, v237, vcc
	global_load_dwordx4 v[176:179], v[234:235], off
	global_load_dwordx4 v[180:183], v[234:235], off offset:16
	v_add_co_u32_e32 v234, vcc, 0x4000, v236
	s_nop 1
	v_addc_co_u32_e32 v235, vcc, 0, v237, vcc
	global_load_dwordx4 v[194:197], v[234:235], off
	global_load_dwordx4 v[198:201], v[234:235], off offset:16
	v_add_co_u32_e32 v234, vcc, 0x6000, v236
	s_nop 1
	v_addc_co_u32_e32 v235, vcc, 0, v237, vcc
	global_load_dwordx4 v[202:205], v[234:235], off
	global_load_dwordx4 v[206:209], v[234:235], off offset:16
	s_waitcnt vmcnt(6)
	v_mov_b32_e32 v154, v172
	v_mov_b32_e32 v155, v173
	v_mov_b32_e32 v156, v174
	v_mov_b32_e32 v157, v175
	v_mov_b32_e32 v150, v168
	v_mov_b32_e32 v151, v169
	v_mov_b32_e32 v152, v170
	v_mov_b32_e32 v153, v171
	v_pk_mul_f32 v[164:165], v[124:125], v[150:151] op_sel:[1,1] op_sel_hi:[0,1]
	v_pk_fma_f32 v[166:167], v[124:125], v[150:151], v[164:165] neg_lo:[0,0,1] neg_hi:[0,0,1]
	v_pk_fma_f32 v[150:151], v[124:125], v[150:151], v[164:165] op_sel_hi:[1,0,1]
	v_mul_f32_e32 v164, v127, v153
	v_mov_b32_e32 v167, v151
	v_pk_mul_f32 v[150:151], v[144:145], v[166:167] op_sel_hi:[0,1]
	v_mul_f32_e32 v166, v127, v152
	v_pk_fma_f32 v[164:165], v[126:127], v[152:153], v[164:165] op_sel_hi:[1,1,0] neg_lo:[0,0,1] neg_hi:[0,0,1]
	v_pk_fma_f32 v[152:153], v[126:127], v[152:153], v[166:167] op_sel:[1,0,0] op_sel_hi:[0,1,0]
	v_mov_b32_e32 v165, v153
	v_pk_mul_f32 v[152:153], v[144:145], v[164:165] op_sel_hi:[0,1]
	v_pk_mul_f32 v[164:165], v[120:121], v[154:155] op_sel:[1,1] op_sel_hi:[0,1]
	v_pk_fma_f32 v[166:167], v[120:121], v[154:155], v[164:165] neg_lo:[0,0,1] neg_hi:[0,0,1]
	v_pk_fma_f32 v[154:155], v[120:121], v[154:155], v[164:165] op_sel_hi:[1,0,1]
	v_mul_f32_e32 v164, v123, v157
	v_mov_b32_e32 v167, v155
	v_pk_mul_f32 v[154:155], v[144:145], v[166:167] op_sel_hi:[0,1]
	v_mul_f32_e32 v166, v123, v156
	v_pk_fma_f32 v[164:165], v[122:123], v[156:157], v[164:165] op_sel_hi:[1,1,0] neg_lo:[0,0,1] neg_hi:[0,0,1]
	v_pk_fma_f32 v[156:157], v[122:123], v[156:157], v[166:167] op_sel:[1,0,0] op_sel_hi:[0,1,0]
	v_mov_b32_e32 v165, v157
	v_pk_mul_f32 v[156:157], v[144:145], v[164:165] op_sel_hi:[0,1]

; __device__ __forceinline__ unsigned cvt_pk_bf16(float lo, float hi) { unsigned r; asm volatile("v_cvt_pk_bf16_f32 %0, %1, %2" : "=v"(r) : "v"(lo), "v"(hi)); return r; }
;     __device__ __forceinline__ void operator()(const f32x4 (&acc)[2][2][4][2], const Unit& u, int wr, int wc, int fr, int fq) const {
;     ...
;                     f32x4 v0 = acc[ai][bj][m][0] * rs, v1 = acc[ai][bj][m][1] * rs;
;                     if (kind <= 1) {
;                         float s = (v0[0] * v0[0] + v0[1] * v0[1]) + (v0[2] * v0[2] + v0[3] * v0[3]) + (v1[0] * v1[0] + v1[1] * v1[1]) + (v1[2] * v1[2] + v1[3] * v1[3]);
;                         s += __shfl_xor(s, 16); s += __shfl_xor(s, 32);
;                         const int head = (u.pn & 3) * 2 + bj;
;                         if (fq == 0) ssq[(size_t)((kind * 8 + head) * 4 + wc) * MT + row] = s;
;                     } else if (kind <= 3) {
;                         const int i0 = (c0 & 127) >> 1;
;                         const f32x4 csa = *(const f32x4*)(cs + (size_t)pos * 64 + i0), csb = *(const f32x4*)(cs + (size_t)pos * 64 + i0 + 2);
;                         const float sc = (kind == 3) ? KSCALE : 1.0f;
;                         f32x4 w0, w1;
;                         w0[0] = (v0[0] * csa[0] - v0[1] * csa[1]) * sc; w0[1] = (v0[1] * csa[0] + v0[0] * csa[1]) * sc;
;                         w0[2] = (v0[2] * csa[2] - v0[3] * csa[3]) * sc; w0[3] = (v0[3] * csa[2] + v0[2] * csa[3]) * sc;
;                         w1[0] = (v1[0] * csb[0] - v1[1] * csb[1]) * sc; w1[1] = (v1[1] * csb[0] + v1[0] * csb[1]) * sc;
;                         w1[2] = (v1[2] * csb[2] - v1[3] * csb[3]) * sc; w1[3] = (v1[3] * csb[2] + v1[2] * csb[3]) * sc;
;                         v0 = w0; v1 = w1;
;                     } else {
; #pragma unroll
;                         for (int j = 0; j < 4; ++j) { v0[j] = v0[j] * __builtin_amdgcn_rcpf(1.0f + __builtin_amdgcn_exp2f(-1.4426950408889634f * v0[j]));
;                                                       v1[j] = v1[j] * __builtin_amdgcn_rcpf(1.0f + __builtin_amdgcn_exp2f(-1.4426950408889634f * v1[j])); }
;                     }
;                     u32x4 w; w.x = cvt_pk_bf16(v0[0], v0[1]); w.y = cvt_pk_bf16(v0[2], v0[3]); w.z = cvt_pk_bf16(v1[0], v1[1]); w.w = cvt_pk_bf16(v1[2], v1[3]);
;                     *(u32x4*)(O + (size_t)row * TOKP + c0) = w;
.LBB0_236:
	v_lshl_or_b32 v120, s66, 8, v161
	v_mov_b64_e32 v[122:123], s[80:81]
	s_movk_i32 s2, 0x2900
	v_mad_i64_i32 v[122:123], s[2:3], v142, s2, v[122:123]
	v_ashrrev_i32_e32 v121, 31, v120
	v_cvt_pk_bf16_f32 v124, v150, v151
	v_cvt_pk_bf16_f32 v125, v152, v153
	v_lshl_add_u64 v[122:123], v[120:121], 1, v[122:123]
	v_cvt_pk_bf16_f32 v126, v154, v155
	v_cvt_pk_bf16_f32 v127, v156, v157
	v_and_b32_e32 v244, -16, v142
	v_lshlrev_b32_e32 v244, 12, v244
	v_mov_b32_e32 v245, 0
	v_lshl_add_u64 v[246:247], v[244:245], 0, v[238:239]
	v_cndmask_b32_e64 v246, v122, v246, s[100:101]
	v_cndmask_b32_e64 v247, v123, v247, s[100:101]
	v_lshl_add_u64 v[248:249], v[246:247], 0, v[242:243]
	global_store_dwordx4 v[246:247], v[124:127], off
	v_mov_b32_e32 v149, v148
	v_pk_mul_f32 v[116:117], v[116:117], v[148:149]
	v_mov_b32_e32 v124, v148
	v_mov_b32_e32 v125, v148
	v_pk_mul_f32 v[118:119], v[118:119], v[124:125]
	v_pk_mul_f32 v[114:115], v[114:115], v[124:125]
	v_cndmask_b32_e64 v124, 0, 1, s[0:1]
	v_pk_mul_f32 v[112:113], v[112:113], v[148:149]
	v_cmp_ne_u32_e64 s[40:41], 1, v124
	s_andn2_b64 vcc, exec, s[0:1]
	s_mov_b64 s[0:1], -1
	s_cbranch_vccnz .LBB0_242
	s_and_b64 vcc, exec, s[38:39]
	s_cbranch_vccnz .LBB0_239
	v_mul_f32_e32 v125, 0xbfb8aa3b, v112
	v_mul_f32_e32 v126, 0xbfb8aa3b, v117
	v_exp_f32_e32 v125, v125
	v_exp_f32_e32 v126, v126
	v_mul_f32_e32 v127, 0xbfb8aa3b, v118
	v_mul_f32_e32 v149, 0xbfb8aa3b, v114
	v_add_f32_e32 v125, 1.0, v125
	v_rcp_f32_e32 v148, v125
	v_add_f32_e32 v125, 1.0, v126
	v_mul_f32_e32 v126, 0xbfb8aa3b, v113
	v_exp_f32_e32 v126, v126
	v_exp_f32_e32 v127, v127
	v_exp_f32_e32 v149, v149
	v_mul_f32_e32 v124, 0xbfb8aa3b, v116
	v_add_f32_e32 v152, 1.0, v126
	v_add_f32_e32 v126, 1.0, v127
	v_add_f32_e32 v127, 1.0, v149
	v_mul_f32_e32 v149, 0xbfb8aa3b, v119
	v_mul_f32_e32 v150, 0xbfb8aa3b, v115
	v_exp_f32_e32 v124, v124
	v_exp_f32_e32 v149, v149
	v_exp_f32_e32 v151, v150
	v_rcp_f32_e32 v150, v127
	v_add_f32_e32 v124, 1.0, v124
	v_add_f32_e32 v127, 1.0, v149
	v_add_f32_e32 v149, 1.0, v151
	v_rcp_f32_e32 v124, v124
	v_rcp_f32_e32 v125, v125
	v_rcp_f32_e32 v126, v126
	v_rcp_f32_e32 v127, v127
	v_rcp_f32_e32 v151, v149
	v_rcp_f32_e32 v149, v152
	v_pk_mul_f32 v[124:125], v[116:117], v[124:125]
	v_pk_mul_f32 v[126:127], v[118:119], v[126:127]
	v_pk_mul_f32 v[150:151], v[114:115], v[150:151]
	v_pk_mul_f32 v[148:149], v[112:113], v[148:149]
	s_mov_b64 s[0:1], 0

;     __device__ __forceinline__ void operator()(const f32x4 (&acc)[2][2][4][2], const Unit& u, int wr, int wc, int fr, int fq) const {
;     ...
;                 const int row = row0 + ai * HALF + m * 16, pos = row & (MS - 1);
;                 const float rs = rstd[row];
; #pragma unroll
;                 for (int bj = 0; bj < 2; ++bj) {
;                     const int c0 = u.pn * BM + bj * HALF + wc * 32 + 8 * fq;
;                     f32x4 v0 = acc[ai][bj][m][0] * rs, v1 = acc[ai][bj][m][1] * rs;
;                     if (kind <= 1) {
;                         float s = (v0[0] * v0[0] + v0[1] * v0[1]) + (v0[2] * v0[2] + v0[3] * v0[3]) + (v1[0] * v1[0] + v1[1] * v1[1]) + (v1[2] * v1[2] + v1[3] * v1[3]);
;                         s += __shfl_xor(s, 16); s += __shfl_xor(s, 32);
;                         const int head = (u.pn & 3) * 2 + bj;
;                         if (fq == 0) ssq[(size_t)((kind * 8 + head) * 4 + wc) * MT + row] = s;
;                     } else if (kind <= 3) {
;                         const int i0 = (c0 & 127) >> 1;
;                         const f32x4 csa = *(const f32x4*)(cs + (size_t)pos * 64 + i0), csb = *(const f32x4*)(cs + (size_t)pos * 64 + i0 + 2);
;                         const float sc = (kind == 3) ? KSCALE : 1.0f;
;                         f32x4 w0, w1;
;                         w0[0] = (v0[0] * csa[0] - v0[1] * csa[1]) * sc; w0[1] = (v0[1] * csa[0] + v0[0] * csa[1]) * sc;
;                         w0[2] = (v0[2] * csa[2] - v0[3] * csa[3]) * sc; w0[3] = (v0[3] * csa[2] + v0[2] * csa[3]) * sc;
;                         w1[0] = (v1[0] * csb[0] - v1[1] * csb[1]) * sc; w1[1] = (v1[1] * csb[0] + v1[0] * csb[1]) * sc;
;                         w1[2] = (v1[2] * csb[2] - v1[3] * csb[3]) * sc; w1[3] = (v1[3] * csb[2] + v1[2] * csb[3]) * sc;
;                         v0 = w0; v1 = w1;
;                     } else {
; #pragma unroll
;                         for (int j = 0; j < 4; ++j) { v0[j] = v0[j] * __builtin_amdgcn_rcpf(1.0f + __builtin_amdgcn_exp2f(-1.4426950408889634f * v0[j]));
;                                                       v1[j] = v1[j] * __builtin_amdgcn_rcpf(1.0f + __builtin_amdgcn_exp2f(-1.4426950408889634f * v1[j])); }
;                     }
;                     u32x4 w; w.x = cvt_pk_bf16(v0[0], v0[1]); w.y = cvt_pk_bf16(v0[2], v0[3]); w.z = cvt_pk_bf16(v1[0], v1[1]); w.w = cvt_pk_bf16(v1[2], v1[3]);
.LBB0_246:
	v_cvt_pk_bf16_f32 v112, v124, v125
	v_cvt_pk_bf16_f32 v113, v126, v127
	v_cvt_pk_bf16_f32 v114, v148, v149
	v_cvt_pk_bf16_f32 v115, v150, v151
	global_store_dwordx4 v[248:249], v[112:115], off
	s_and_b64 vcc, exec, s[40:41]
	s_mov_b64 s[0:1], -1
	v_or_b32_e32 v114, 16, v142
	v_ashrrev_i32_e32 v115, 31, v114
	v_lshl_add_u64 v[112:113], v[114:115], 2, s[56:57]
	s_nop 1
	v_mov_b32_e32 v112, v226
	v_lshlrev_b32_e32 v113, 6, v114
	v_and_b32_e32 v115, 0x1f7c0, v113
	v_pk_mul_f32 v[110:111], v[110:111], v[112:113] op_sel_hi:[1,0]
	v_pk_mul_f32 v[108:109], v[108:109], v[112:113] op_sel_hi:[1,0]
	v_pk_mul_f32 v[106:107], v[106:107], v[112:113] op_sel_hi:[1,0]
	v_pk_mul_f32 v[104:105], v[104:105], v[112:113] op_sel_hi:[1,0]
	s_cbranch_vccnz .LBB0_252
	s_and_b64 vcc, exec, s[38:39]
	s_cbranch_vccnz .LBB0_249
	v_mul_f32_e32 v113, 0xbfb8aa3b, v108
	v_exp_f32_e32 v113, v113
	v_mul_f32_e32 v116, 0xbfb8aa3b, v104
	v_mul_f32_e32 v117, 0xbfb8aa3b, v109
	v_exp_f32_e32 v118, v116
	v_exp_f32_e32 v117, v117
	v_add_f32_e32 v113, 1.0, v113
	v_rcp_f32_e32 v116, v113
	v_add_f32_e32 v113, 1.0, v118
	v_rcp_f32_e32 v122, v113
	v_add_f32_e32 v113, 1.0, v117
	v_mul_f32_e32 v119, 0xbfb8aa3b, v106
	v_rcp_f32_e32 v117, v113
	v_mul_f32_e32 v113, 0xbfb8aa3b, v105
	v_mul_f32_e32 v118, 0xbfb8aa3b, v110
	v_exp_f32_e32 v119, v119
	v_mul_f32_e32 v123, 0xbfb8aa3b, v111
	v_mul_f32_e32 v124, 0xbfb8aa3b, v107
	v_exp_f32_e32 v113, v113
	v_exp_f32_e32 v118, v118
	v_exp_f32_e32 v123, v123
	v_exp_f32_e32 v125, v124
	v_add_f32_e32 v119, 1.0, v119
	v_add_f32_e32 v113, 1.0, v113
	v_add_f32_e32 v118, 1.0, v118
	v_rcp_f32_e32 v124, v119
	v_add_f32_e32 v119, 1.0, v123
	v_add_f32_e32 v123, 1.0, v125
	v_rcp_f32_e32 v118, v118
	v_rcp_f32_e32 v119, v119
	v_rcp_f32_e32 v125, v123
	v_rcp_f32_e32 v123, v113
	v_pk_mul_f32 v[116:117], v[108:109], v[116:117]
	v_pk_mul_f32 v[118:119], v[110:111], v[118:119]
	v_pk_mul_f32 v[124:125], v[106:107], v[124:125]
	v_pk_mul_f32 v[122:123], v[104:105], v[122:123]
	s_mov_b64 s[0:1], 0
.LBB0_249:
	s_andn2_b64 vcc, exec, s[0:1]
	s_cbranch_vccnz .LBB0_251
	v_lshlrev_b32_e32 v184, 3, v115
	v_lshl_add_u64 v[116:117], v[136:137], 0, v[184:185]
	v_add_co_u32_e32 v234, vcc, 0x10000, v236
	s_nop 1
	v_addc_co_u32_e32 v235, vcc, 0, v237, vcc
	global_load_dwordx4 v[168:171], v[234:235], off
	global_load_dwordx4 v[172:175], v[234:235], off offset:16
	s_waitcnt vmcnt(8)
	v_mov_b32_e32 v122, v180
	v_mov_b32_e32 v123, v181
	v_mov_b32_e32 v124, v182
	v_mov_b32_e32 v125, v183
	v_mov_b32_e32 v116, v176
	v_mov_b32_e32 v117, v177
	v_mov_b32_e32 v118, v178
	v_mov_b32_e32 v119, v179
	v_pk_mul_f32 v[126:127], v[108:109], v[116:117] op_sel:[1,1] op_sel_hi:[0,1]
	v_pk_fma_f32 v[148:149], v[108:109], v[116:117], v[126:127] neg_lo:[0,0,1] neg_hi:[0,0,1]
	v_pk_fma_f32 v[116:117], v[108:109], v[116:117], v[126:127] op_sel_hi:[1,0,1]
	v_mul_f32_e32 v126, v111, v119
	v_mov_b32_e32 v149, v117
	v_pk_mul_f32 v[116:117], v[144:145], v[148:149] op_sel_hi:[0,1]
	v_mul_f32_e32 v148, v111, v118
	v_pk_fma_f32 v[126:127], v[110:111], v[118:119], v[126:127] op_sel_hi:[1,1,0] neg_lo:[0,0,1] neg_hi:[0,0,1]
	v_pk_fma_f32 v[118:119], v[110:111], v[118:119], v[148:149] op_sel:[1,0,0] op_sel_hi:[0,1,0]
	v_mov_b32_e32 v127, v119
	v_pk_mul_f32 v[118:119], v[144:145], v[126:127] op_sel_hi:[0,1]
	v_pk_mul_f32 v[126:127], v[104:105], v[122:123] op_sel:[1,1] op_sel_hi:[0,1]
	v_pk_fma_f32 v[148:149], v[104:105], v[122:123], v[126:127] neg_lo:[0,0,1] neg_hi:[0,0,1]
	v_pk_fma_f32 v[122:123], v[104:105], v[122:123], v[126:127] op_sel_hi:[1,0,1]
	v_mul_f32_e32 v126, v107, v125
	v_mov_b32_e32 v149, v123
	v_pk_mul_f32 v[122:123], v[144:145], v[148:149] op_sel_hi:[0,1]
	v_mul_f32_e32 v148, v107, v124
	v_pk_fma_f32 v[126:127], v[106:107], v[124:125], v[126:127] op_sel_hi:[1,1,0] neg_lo:[0,0,1] neg_hi:[0,0,1]
	v_pk_fma_f32 v[124:125], v[106:107], v[124:125], v[148:149] op_sel:[1,0,0] op_sel_hi:[0,1,0]
	v_mov_b32_e32 v127, v125
	v_pk_mul_f32 v[124:125], v[144:145], v[126:127] op_sel_hi:[0,1]

; __device__ __forceinline__ unsigned cvt_pk_bf16(float lo, float hi) { unsigned r; asm volatile("v_cvt_pk_bf16_f32 %0, %1, %2" : "=v"(r) : "v"(lo), "v"(hi)); return r; }
;     __device__ __forceinline__ void operator()(const f32x4 (&acc)[2][2][4][2], const Unit& u, int wr, int wc, int fr, int fq) const {
;     ...
;                     f32x4 v0 = acc[ai][bj][m][0] * rs, v1 = acc[ai][bj][m][1] * rs;
;                     if (kind <= 1) {
;                         float s = (v0[0] * v0[0] + v0[1] * v0[1]) + (v0[2] * v0[2] + v0[3] * v0[3]) + (v1[0] * v1[0] + v1[1] * v1[1]) + (v1[2] * v1[2] + v1[3] * v1[3]);
;                         s += __shfl_xor(s, 16); s += __shfl_xor(s, 32);
;                         const int head = (u.pn & 3) * 2 + bj;
;                         if (fq == 0) ssq[(size_t)((kind * 8 + head) * 4 + wc) * MT + row] = s;
;                     } else if (kind <= 3) {
;                         const int i0 = (c0 & 127) >> 1;
;                         const f32x4 csa = *(const f32x4*)(cs + (size_t)pos * 64 + i0), csb = *(const f32x4*)(cs + (size_t)pos * 64 + i0 + 2);
;                         const float sc = (kind == 3) ? KSCALE : 1.0f;
;                         f32x4 w0, w1;
;                         w0[0] = (v0[0] * csa[0] - v0[1] * csa[1]) * sc; w0[1] = (v0[1] * csa[0] + v0[0] * csa[1]) * sc;
;                         w0[2] = (v0[2] * csa[2] - v0[3] * csa[3]) * sc; w0[3] = (v0[3] * csa[2] + v0[2] * csa[3]) * sc;
;                         w1[0] = (v1[0] * csb[0] - v1[1] * csb[1]) * sc; w1[1] = (v1[1] * csb[0] + v1[0] * csb[1]) * sc;
;                         w1[2] = (v1[2] * csb[2] - v1[3] * csb[3]) * sc; w1[3] = (v1[3] * csb[2] + v1[2] * csb[3]) * sc;
;                         v0 = w0; v1 = w1;
;                     } else {
; #pragma unroll
;                         for (int j = 0; j < 4; ++j) { v0[j] = v0[j] * __builtin_amdgcn_rcpf(1.0f + __builtin_amdgcn_exp2f(-1.4426950408889634f * v0[j]));
;                                                       v1[j] = v1[j] * __builtin_amdgcn_rcpf(1.0f + __builtin_amdgcn_exp2f(-1.4426950408889634f * v1[j])); }
;                     }
;                     u32x4 w; w.x = cvt_pk_bf16(v0[0], v0[1]); w.y = cvt_pk_bf16(v0[2], v0[3]); w.z = cvt_pk_bf16(v1[0], v1[1]); w.w = cvt_pk_bf16(v1[2], v1[3]);
;                     *(u32x4*)(O + (size_t)row * TOKP + c0) = w;
.LBB0_256:
	v_mov_b64_e32 v[104:105], s[80:81]
	s_movk_i32 s0, 0x2900
	v_mad_i64_i32 v[104:105], s[0:1], v114, s0, v[104:105]
	v_cvt_pk_bf16_f32 v106, v116, v117
	v_cvt_pk_bf16_f32 v107, v118, v119
	v_lshl_add_u64 v[104:105], v[120:121], 1, v[104:105]
	v_mov_b32_e32 v113, v112
	v_cvt_pk_bf16_f32 v108, v122, v123
	v_cvt_pk_bf16_f32 v109, v124, v125
	v_and_b32_e32 v244, -16, v114
	v_lshlrev_b32_e32 v244, 12, v244
	v_mov_b32_e32 v245, 0
	v_lshl_add_u64 v[246:247], v[244:245], 0, v[238:239]
	v_cndmask_b32_e64 v246, v104, v246, s[100:101]
	v_cndmask_b32_e64 v247, v105, v247, s[100:101]
	v_lshl_add_u64 v[248:249], v[246:247], 0, v[242:243]
	global_store_dwordx4 v[246:247], v[106:109], off
	v_pk_mul_f32 v[100:101], v[100:101], v[112:113]
	v_pk_mul_f32 v[96:97], v[96:97], v[112:113]
	v_mov_b32_e32 v106, v112
	v_mov_b32_e32 v107, v112
	v_pk_mul_f32 v[102:103], v[102:103], v[106:107]
	v_pk_mul_f32 v[98:99], v[98:99], v[106:107]
	s_and_b64 vcc, exec, s[40:41]
	s_mov_b64 s[0:1], -1
	s_cbranch_vccnz .LBB0_262
	s_and_b64 vcc, exec, s[38:39]
	s_cbranch_vccnz .LBB0_259
	v_mul_f32_e32 v107, 0xbfb8aa3b, v96
	v_mul_f32_e32 v108, 0xbfb8aa3b, v101
	v_exp_f32_e32 v107, v107
	v_exp_f32_e32 v108, v108
	v_mul_f32_e32 v109, 0xbfb8aa3b, v102
	v_mul_f32_e32 v111, 0xbfb8aa3b, v98
	v_add_f32_e32 v107, 1.0, v107
	v_rcp_f32_e32 v110, v107
	v_add_f32_e32 v107, 1.0, v108
	v_mul_f32_e32 v108, 0xbfb8aa3b, v97
	v_exp_f32_e32 v108, v108
	v_exp_f32_e32 v109, v109
	v_exp_f32_e32 v111, v111
	v_mul_f32_e32 v106, 0xbfb8aa3b, v100
	v_add_f32_e32 v114, 1.0, v108
	v_add_f32_e32 v108, 1.0, v109
	v_add_f32_e32 v109, 1.0, v111
	v_mul_f32_e32 v111, 0xbfb8aa3b, v103
	v_mul_f32_e32 v112, 0xbfb8aa3b, v99
	v_exp_f32_e32 v106, v106
	v_exp_f32_e32 v111, v111
	v_exp_f32_e32 v113, v112
	v_rcp_f32_e32 v112, v109
	v_add_f32_e32 v106, 1.0, v106
	v_add_f32_e32 v109, 1.0, v111
	v_add_f32_e32 v111, 1.0, v113
	v_rcp_f32_e32 v106, v106
	v_rcp_f32_e32 v107, v107
	v_rcp_f32_e32 v108, v108
	v_rcp_f32_e32 v109, v109
	v_rcp_f32_e32 v113, v111
	v_rcp_f32_e32 v111, v114
	v_pk_mul_f32 v[106:107], v[100:101], v[106:107]
	v_pk_mul_f32 v[108:109], v[102:103], v[108:109]
	v_pk_mul_f32 v[112:113], v[98:99], v[112:113]
	v_pk_mul_f32 v[110:111], v[96:97], v[110:111]
	s_mov_b64 s[0:1], 0

;     __device__ __forceinline__ void operator()(const f32x4 (&acc)[2][2][4][2], const Unit& u, int wr, int wc, int fr, int fq) const {
;     ...
;                 const int row = row0 + ai * HALF + m * 16, pos = row & (MS - 1);
;                 const float rs = rstd[row];
; #pragma unroll
;                 for (int bj = 0; bj < 2; ++bj) {
;                     const int c0 = u.pn * BM + bj * HALF + wc * 32 + 8 * fq;
;                     f32x4 v0 = acc[ai][bj][m][0] * rs, v1 = acc[ai][bj][m][1] * rs;
;                     if (kind <= 1) {
;                         float s = (v0[0] * v0[0] + v0[1] * v0[1]) + (v0[2] * v0[2] + v0[3] * v0[3]) + (v1[0] * v1[0] + v1[1] * v1[1]) + (v1[2] * v1[2] + v1[3] * v1[3]);
;                         s += __shfl_xor(s, 16); s += __shfl_xor(s, 32);
;                         const int head = (u.pn & 3) * 2 + bj;
;                         if (fq == 0) ssq[(size_t)((kind * 8 + head) * 4 + wc) * MT + row] = s;
;                     } else if (kind <= 3) {
;                         const int i0 = (c0 & 127) >> 1;
;                         const f32x4 csa = *(const f32x4*)(cs + (size_t)pos * 64 + i0), csb = *(const f32x4*)(cs + (size_t)pos * 64 + i0 + 2);
;                         const float sc = (kind == 3) ? KSCALE : 1.0f;
;                         f32x4 w0, w1;
;                         w0[0] = (v0[0] * csa[0] - v0[1] * csa[1]) * sc; w0[1] = (v0[1] * csa[0] + v0[0] * csa[1]) * sc;
;                         w0[2] = (v0[2] * csa[2] - v0[3] * csa[3]) * sc; w0[3] = (v0[3] * csa[2] + v0[2] * csa[3]) * sc;
;                         w1[0] = (v1[0] * csb[0] - v1[1] * csb[1]) * sc; w1[1] = (v1[1] * csb[0] + v1[0] * csb[1]) * sc;
;                         w1[2] = (v1[2] * csb[2] - v1[3] * csb[3]) * sc; w1[3] = (v1[3] * csb[2] + v1[2] * csb[3]) * sc;
;                         v0 = w0; v1 = w1;
;                     } else {
; #pragma unroll
;                         for (int j = 0; j < 4; ++j) { v0[j] = v0[j] * __builtin_amdgcn_rcpf(1.0f + __builtin_amdgcn_exp2f(-1.4426950408889634f * v0[j]));
;                                                       v1[j] = v1[j] * __builtin_amdgcn_rcpf(1.0f + __builtin_amdgcn_exp2f(-1.4426950408889634f * v1[j])); }
;                     }
;                     u32x4 w; w.x = cvt_pk_bf16(v0[0], v0[1]); w.y = cvt_pk_bf16(v0[2], v0[3]); w.z = cvt_pk_bf16(v1[0], v1[1]); w.w = cvt_pk_bf16(v1[2], v1[3]);
.LBB0_266:
	v_cvt_pk_bf16_f32 v96, v106, v107
	v_cvt_pk_bf16_f32 v97, v108, v109
	v_cvt_pk_bf16_f32 v98, v110, v111
	v_cvt_pk_bf16_f32 v99, v112, v113
	global_store_dwordx4 v[248:249], v[96:99], off
	s_and_b64 vcc, exec, s[40:41]
	s_mov_b64 s[0:1], -1
	v_or_b32_e32 v98, 32, v142
	v_ashrrev_i32_e32 v99, 31, v98
	v_lshl_add_u64 v[96:97], v[98:99], 2, s[56:57]
	s_nop 1
	v_mov_b32_e32 v96, v227
	v_lshlrev_b32_e32 v97, 6, v98
	v_and_b32_e32 v99, 0x1fbc0, v97
	v_pk_mul_f32 v[94:95], v[94:95], v[96:97] op_sel_hi:[1,0]
	v_pk_mul_f32 v[92:93], v[92:93], v[96:97] op_sel_hi:[1,0]
	v_pk_mul_f32 v[90:91], v[90:91], v[96:97] op_sel_hi:[1,0]
	v_pk_mul_f32 v[88:89], v[88:89], v[96:97] op_sel_hi:[1,0]
	s_cbranch_vccnz .LBB0_272
	s_and_b64 vcc, exec, s[38:39]
	s_cbranch_vccnz .LBB0_269
	v_mul_f32_e32 v97, 0xbfb8aa3b, v92
	v_exp_f32_e32 v97, v97
	v_mul_f32_e32 v100, 0xbfb8aa3b, v88
	v_mul_f32_e32 v101, 0xbfb8aa3b, v93
	v_exp_f32_e32 v102, v100
	v_exp_f32_e32 v101, v101
	v_add_f32_e32 v97, 1.0, v97
	v_rcp_f32_e32 v100, v97
	v_add_f32_e32 v97, 1.0, v102
	v_rcp_f32_e32 v104, v97
	v_add_f32_e32 v97, 1.0, v101
	v_mul_f32_e32 v103, 0xbfb8aa3b, v90
	v_rcp_f32_e32 v101, v97
	v_mul_f32_e32 v97, 0xbfb8aa3b, v89
	v_mul_f32_e32 v102, 0xbfb8aa3b, v94
	v_exp_f32_e32 v103, v103
	v_mul_f32_e32 v105, 0xbfb8aa3b, v95
	v_mul_f32_e32 v106, 0xbfb8aa3b, v91
	v_exp_f32_e32 v97, v97
	v_exp_f32_e32 v102, v102
	v_exp_f32_e32 v105, v105
	v_exp_f32_e32 v107, v106
	v_add_f32_e32 v103, 1.0, v103
	v_add_f32_e32 v97, 1.0, v97
	v_add_f32_e32 v102, 1.0, v102
	v_rcp_f32_e32 v106, v103
	v_add_f32_e32 v103, 1.0, v105
	v_add_f32_e32 v105, 1.0, v107
	v_rcp_f32_e32 v102, v102
	v_rcp_f32_e32 v103, v103
	v_rcp_f32_e32 v107, v105
	v_rcp_f32_e32 v105, v97
	v_pk_mul_f32 v[100:101], v[92:93], v[100:101]
	v_pk_mul_f32 v[102:103], v[94:95], v[102:103]
	v_pk_mul_f32 v[106:107], v[90:91], v[106:107]
	v_pk_mul_f32 v[104:105], v[88:89], v[104:105]
	s_mov_b64 s[0:1], 0
.LBB0_269:
	s_andn2_b64 vcc, exec, s[0:1]
	s_cbranch_vccnz .LBB0_271
	v_lshlrev_b32_e32 v184, 3, v99
	v_lshl_add_u64 v[100:101], v[136:137], 0, v[184:185]
	v_add_co_u32_e32 v234, vcc, 0x12000, v236
	s_nop 1
	v_addc_co_u32_e32 v235, vcc, 0, v237, vcc
	global_load_dwordx4 v[176:179], v[234:235], off
	global_load_dwordx4 v[180:183], v[234:235], off offset:16
	s_waitcnt vmcnt(10)
	v_mov_b32_e32 v104, v198
	v_mov_b32_e32 v105, v199
	v_mov_b32_e32 v106, v200
	v_mov_b32_e32 v107, v201
	v_mov_b32_e32 v100, v194
	v_mov_b32_e32 v101, v195
	v_mov_b32_e32 v102, v196
	v_mov_b32_e32 v103, v197
	v_pk_mul_f32 v[108:109], v[92:93], v[100:101] op_sel:[1,1] op_sel_hi:[0,1]
	v_pk_fma_f32 v[110:111], v[92:93], v[100:101], v[108:109] neg_lo:[0,0,1] neg_hi:[0,0,1]
	v_pk_fma_f32 v[100:101], v[92:93], v[100:101], v[108:109] op_sel_hi:[1,0,1]
	v_mul_f32_e32 v108, v95, v103
	v_mov_b32_e32 v111, v101
	v_pk_mul_f32 v[100:101], v[144:145], v[110:111] op_sel_hi:[0,1]
	v_mul_f32_e32 v110, v95, v102
	v_pk_fma_f32 v[108:109], v[94:95], v[102:103], v[108:109] op_sel_hi:[1,1,0] neg_lo:[0,0,1] neg_hi:[0,0,1]
	v_pk_fma_f32 v[102:103], v[94:95], v[102:103], v[110:111] op_sel:[1,0,0] op_sel_hi:[0,1,0]
	v_mov_b32_e32 v109, v103
	v_pk_mul_f32 v[102:103], v[144:145], v[108:109] op_sel_hi:[0,1]
	v_pk_mul_f32 v[108:109], v[88:89], v[104:105] op_sel:[1,1] op_sel_hi:[0,1]
	v_pk_fma_f32 v[110:111], v[88:89], v[104:105], v[108:109] neg_lo:[0,0,1] neg_hi:[0,0,1]
	v_pk_fma_f32 v[104:105], v[88:89], v[104:105], v[108:109] op_sel_hi:[1,0,1]
	v_mul_f32_e32 v108, v91, v107
	v_mov_b32_e32 v111, v105
	v_pk_mul_f32 v[104:105], v[144:145], v[110:111] op_sel_hi:[0,1]
	v_mul_f32_e32 v110, v91, v106
	v_pk_fma_f32 v[108:109], v[90:91], v[106:107], v[108:109] op_sel_hi:[1,1,0] neg_lo:[0,0,1] neg_hi:[0,0,1]
	v_pk_fma_f32 v[106:107], v[90:91], v[106:107], v[110:111] op_sel:[1,0,0] op_sel_hi:[0,1,0]
	v_mov_b32_e32 v109, v107
	v_pk_mul_f32 v[106:107], v[144:145], v[108:109] op_sel_hi:[0,1]

; __device__ __forceinline__ unsigned cvt_pk_bf16(float lo, float hi) { unsigned r; asm volatile("v_cvt_pk_bf16_f32 %0, %1, %2" : "=v"(r) : "v"(lo), "v"(hi)); return r; }
;     __device__ __forceinline__ void operator()(const f32x4 (&acc)[2][2][4][2], const Unit& u, int wr, int wc, int fr, int fq) const {
;     ...
;                     f32x4 v0 = acc[ai][bj][m][0] * rs, v1 = acc[ai][bj][m][1] * rs;
;                     if (kind <= 1) {
;                         float s = (v0[0] * v0[0] + v0[1] * v0[1]) + (v0[2] * v0[2] + v0[3] * v0[3]) + (v1[0] * v1[0] + v1[1] * v1[1]) + (v1[2] * v1[2] + v1[3] * v1[3]);
;                         s += __shfl_xor(s, 16); s += __shfl_xor(s, 32);
;                         const int head = (u.pn & 3) * 2 + bj;
;                         if (fq == 0) ssq[(size_t)((kind * 8 + head) * 4 + wc) * MT + row] = s;
;                     } else if (kind <= 3) {
;                         const int i0 = (c0 & 127) >> 1;
;                         const f32x4 csa = *(const f32x4*)(cs + (size_t)pos * 64 + i0), csb = *(const f32x4*)(cs + (size_t)pos * 64 + i0 + 2);
;                         const float sc = (kind == 3) ? KSCALE : 1.0f;
;                         f32x4 w0, w1;
;                         w0[0] = (v0[0] * csa[0] - v0[1] * csa[1]) * sc; w0[1] = (v0[1] * csa[0] + v0[0] * csa[1]) * sc;
;                         w0[2] = (v0[2] * csa[2] - v0[3] * csa[3]) * sc; w0[3] = (v0[3] * csa[2] + v0[2] * csa[3]) * sc;
;                         w1[0] = (v1[0] * csb[0] - v1[1] * csb[1]) * sc; w1[1] = (v1[1] * csb[0] + v1[0] * csb[1]) * sc;
;                         w1[2] = (v1[2] * csb[2] - v1[3] * csb[3]) * sc; w1[3] = (v1[3] * csb[2] + v1[2] * csb[3]) * sc;
;                         v0 = w0; v1 = w1;
;                     } else {
; #pragma unroll
;                         for (int j = 0; j < 4; ++j) { v0[j] = v0[j] * __builtin_amdgcn_rcpf(1.0f + __builtin_amdgcn_exp2f(-1.4426950408889634f * v0[j]));
;                                                       v1[j] = v1[j] * __builtin_amdgcn_rcpf(1.0f + __builtin_amdgcn_exp2f(-1.4426950408889634f * v1[j])); }
;                     }
;                     u32x4 w; w.x = cvt_pk_bf16(v0[0], v0[1]); w.y = cvt_pk_bf16(v0[2], v0[3]); w.z = cvt_pk_bf16(v1[0], v1[1]); w.w = cvt_pk_bf16(v1[2], v1[3]);
;                     *(u32x4*)(O + (size_t)row * TOKP + c0) = w;
.LBB0_276:
	v_mov_b64_e32 v[88:89], s[80:81]
	s_movk_i32 s0, 0x2900
	v_mad_i64_i32 v[88:89], s[0:1], v98, s0, v[88:89]
	v_cvt_pk_bf16_f32 v90, v100, v101
	v_cvt_pk_bf16_f32 v91, v102, v103
	v_lshl_add_u64 v[88:89], v[120:121], 1, v[88:89]
	v_mov_b32_e32 v97, v96
	v_cvt_pk_bf16_f32 v92, v104, v105
	v_cvt_pk_bf16_f32 v93, v106, v107
	v_and_b32_e32 v244, -16, v98
	v_lshlrev_b32_e32 v244, 12, v244
	v_mov_b32_e32 v245, 0
	v_lshl_add_u64 v[246:247], v[244:245], 0, v[238:239]
	v_cndmask_b32_e64 v246, v88, v246, s[100:101]
	v_cndmask_b32_e64 v247, v89, v247, s[100:101]
	v_lshl_add_u64 v[248:249], v[246:247], 0, v[242:243]
	global_store_dwordx4 v[246:247], v[90:93], off
	v_pk_mul_f32 v[84:85], v[84:85], v[96:97]
	v_pk_mul_f32 v[80:81], v[80:81], v[96:97]
	v_mov_b32_e32 v90, v96
	v_mov_b32_e32 v91, v96
	v_pk_mul_f32 v[86:87], v[86:87], v[90:91]
	v_pk_mul_f32 v[82:83], v[82:83], v[90:91]
	s_and_b64 vcc, exec, s[40:41]
	s_mov_b64 s[0:1], -1
	s_cbranch_vccnz .LBB0_282
	s_and_b64 vcc, exec, s[38:39]
	s_cbranch_vccnz .LBB0_279
	v_mul_f32_e32 v91, 0xbfb8aa3b, v80
	v_mul_f32_e32 v92, 0xbfb8aa3b, v85
	v_exp_f32_e32 v91, v91
	v_exp_f32_e32 v92, v92
	v_mul_f32_e32 v93, 0xbfb8aa3b, v86
	v_mul_f32_e32 v95, 0xbfb8aa3b, v82
	v_add_f32_e32 v91, 1.0, v91
	v_rcp_f32_e32 v94, v91
	v_add_f32_e32 v91, 1.0, v92
	v_mul_f32_e32 v92, 0xbfb8aa3b, v81
	v_exp_f32_e32 v92, v92
	v_exp_f32_e32 v93, v93
	v_exp_f32_e32 v95, v95
	v_mul_f32_e32 v90, 0xbfb8aa3b, v84
	v_add_f32_e32 v98, 1.0, v92
	v_add_f32_e32 v92, 1.0, v93
	v_add_f32_e32 v93, 1.0, v95
	v_mul_f32_e32 v95, 0xbfb8aa3b, v87
	v_mul_f32_e32 v96, 0xbfb8aa3b, v83
	v_exp_f32_e32 v90, v90
	v_exp_f32_e32 v95, v95
	v_exp_f32_e32 v97, v96
	v_rcp_f32_e32 v96, v93
	v_add_f32_e32 v90, 1.0, v90
	v_add_f32_e32 v93, 1.0, v95
	v_add_f32_e32 v95, 1.0, v97
	v_rcp_f32_e32 v90, v90
	v_rcp_f32_e32 v91, v91
	v_rcp_f32_e32 v92, v92
	v_rcp_f32_e32 v93, v93
	v_rcp_f32_e32 v97, v95
	v_rcp_f32_e32 v95, v98
	v_pk_mul_f32 v[90:91], v[84:85], v[90:91]
	v_pk_mul_f32 v[92:93], v[86:87], v[92:93]
	v_pk_mul_f32 v[96:97], v[82:83], v[96:97]
	v_pk_mul_f32 v[94:95], v[80:81], v[94:95]
	s_mov_b64 s[0:1], 0

;     __device__ __forceinline__ void operator()(const f32x4 (&acc)[2][2][4][2], const Unit& u, int wr, int wc, int fr, int fq) const {
;     ...
;                 const int row = row0 + ai * HALF + m * 16, pos = row & (MS - 1);
;                 const float rs = rstd[row];
; #pragma unroll
;                 for (int bj = 0; bj < 2; ++bj) {
;                     const int c0 = u.pn * BM + bj * HALF + wc * 32 + 8 * fq;
;                     f32x4 v0 = acc[ai][bj][m][0] * rs, v1 = acc[ai][bj][m][1] * rs;
;                     if (kind <= 1) {
;                         float s = (v0[0] * v0[0] + v0[1] * v0[1]) + (v0[2] * v0[2] + v0[3] * v0[3]) + (v1[0] * v1[0] + v1[1] * v1[1]) + (v1[2] * v1[2] + v1[3] * v1[3]);
;                         s += __shfl_xor(s, 16); s += __shfl_xor(s, 32);
;                         const int head = (u.pn & 3) * 2 + bj;
;                         if (fq == 0) ssq[(size_t)((kind * 8 + head) * 4 + wc) * MT + row] = s;
;                     } else if (kind <= 3) {
;                         const int i0 = (c0 & 127) >> 1;
;                         const f32x4 csa = *(const f32x4*)(cs + (size_t)pos * 64 + i0), csb = *(const f32x4*)(cs + (size_t)pos * 64 + i0 + 2);
;                         const float sc = (kind == 3) ? KSCALE : 1.0f;
;                         f32x4 w0, w1;
;                         w0[0] = (v0[0] * csa[0] - v0[1] * csa[1]) * sc; w0[1] = (v0[1] * csa[0] + v0[0] * csa[1]) * sc;
;                         w0[2] = (v0[2] * csa[2] - v0[3] * csa[3]) * sc; w0[3] = (v0[3] * csa[2] + v0[2] * csa[3]) * sc;
;                         w1[0] = (v1[0] * csb[0] - v1[1] * csb[1]) * sc; w1[1] = (v1[1] * csb[0] + v1[0] * csb[1]) * sc;
;                         w1[2] = (v1[2] * csb[2] - v1[3] * csb[3]) * sc; w1[3] = (v1[3] * csb[2] + v1[2] * csb[3]) * sc;
;                         v0 = w0; v1 = w1;
;                     } else {
; #pragma unroll
;                         for (int j = 0; j < 4; ++j) { v0[j] = v0[j] * __builtin_amdgcn_rcpf(1.0f + __builtin_amdgcn_exp2f(-1.4426950408889634f * v0[j]));
;                                                       v1[j] = v1[j] * __builtin_amdgcn_rcpf(1.0f + __builtin_amdgcn_exp2f(-1.4426950408889634f * v1[j])); }
;                     }
;                     u32x4 w; w.x = cvt_pk_bf16(v0[0], v0[1]); w.y = cvt_pk_bf16(v0[2], v0[3]); w.z = cvt_pk_bf16(v1[0], v1[1]); w.w = cvt_pk_bf16(v1[2], v1[3]);
.LBB0_286:
	v_cvt_pk_bf16_f32 v80, v90, v91
	v_cvt_pk_bf16_f32 v81, v92, v93
	v_cvt_pk_bf16_f32 v82, v94, v95
	v_cvt_pk_bf16_f32 v83, v96, v97
	global_store_dwordx4 v[248:249], v[80:83], off
	s_and_b64 vcc, exec, s[40:41]
	s_mov_b64 s[0:1], -1
	v_or_b32_e32 v82, 48, v142
	v_ashrrev_i32_e32 v83, 31, v82
	v_lshl_add_u64 v[80:81], v[82:83], 2, s[56:57]
	s_nop 1
	v_mov_b32_e32 v80, v228
	v_lshlrev_b32_e32 v81, 6, v82
	v_and_b32_e32 v83, 0x1ffc0, v81
	v_pk_mul_f32 v[78:79], v[78:79], v[80:81] op_sel_hi:[1,0]
	v_pk_mul_f32 v[76:77], v[76:77], v[80:81] op_sel_hi:[1,0]
	v_pk_mul_f32 v[74:75], v[74:75], v[80:81] op_sel_hi:[1,0]
	v_pk_mul_f32 v[72:73], v[72:73], v[80:81] op_sel_hi:[1,0]
	s_cbranch_vccnz .LBB0_292
	s_and_b64 vcc, exec, s[38:39]
	s_cbranch_vccnz .LBB0_289
	v_mul_f32_e32 v81, 0xbfb8aa3b, v76
	v_exp_f32_e32 v81, v81
	v_mul_f32_e32 v84, 0xbfb8aa3b, v72
	v_mul_f32_e32 v85, 0xbfb8aa3b, v77
	v_exp_f32_e32 v86, v84
	v_exp_f32_e32 v85, v85
	v_add_f32_e32 v81, 1.0, v81
	v_rcp_f32_e32 v84, v81
	v_add_f32_e32 v81, 1.0, v86
	v_rcp_f32_e32 v88, v81
	v_add_f32_e32 v81, 1.0, v85
	v_mul_f32_e32 v87, 0xbfb8aa3b, v74
	v_rcp_f32_e32 v85, v81
	v_mul_f32_e32 v81, 0xbfb8aa3b, v73
	v_mul_f32_e32 v86, 0xbfb8aa3b, v78
	v_exp_f32_e32 v87, v87
	v_mul_f32_e32 v89, 0xbfb8aa3b, v79
	v_mul_f32_e32 v90, 0xbfb8aa3b, v75
	v_exp_f32_e32 v81, v81
	v_exp_f32_e32 v86, v86
	v_exp_f32_e32 v89, v89
	v_exp_f32_e32 v91, v90
	v_add_f32_e32 v87, 1.0, v87
	v_add_f32_e32 v81, 1.0, v81
	v_add_f32_e32 v86, 1.0, v86
	v_rcp_f32_e32 v90, v87
	v_add_f32_e32 v87, 1.0, v89
	v_add_f32_e32 v89, 1.0, v91
	v_rcp_f32_e32 v86, v86
	v_rcp_f32_e32 v87, v87
	v_rcp_f32_e32 v91, v89
	v_rcp_f32_e32 v89, v81
	v_pk_mul_f32 v[84:85], v[76:77], v[84:85]
	v_pk_mul_f32 v[86:87], v[78:79], v[86:87]
	v_pk_mul_f32 v[90:91], v[74:75], v[90:91]
	v_pk_mul_f32 v[88:89], v[72:73], v[88:89]
	s_mov_b64 s[0:1], 0
.LBB0_289:
	s_andn2_b64 vcc, exec, s[0:1]
	s_cbranch_vccnz .LBB0_291
	v_lshlrev_b32_e32 v184, 3, v83
	v_lshl_add_u64 v[84:85], v[136:137], 0, v[184:185]
	v_add_co_u32_e32 v234, vcc, 0x14000, v236
	s_nop 1
	v_addc_co_u32_e32 v235, vcc, 0, v237, vcc
	global_load_dwordx4 v[194:197], v[234:235], off
	global_load_dwordx4 v[198:201], v[234:235], off offset:16
	s_waitcnt vmcnt(12)
	v_mov_b32_e32 v88, v206
	v_mov_b32_e32 v89, v207
	v_mov_b32_e32 v90, v208
	v_mov_b32_e32 v91, v209
	v_mov_b32_e32 v84, v202
	v_mov_b32_e32 v85, v203
	v_mov_b32_e32 v86, v204
	v_mov_b32_e32 v87, v205
	v_pk_mul_f32 v[92:93], v[76:77], v[84:85] op_sel:[1,1] op_sel_hi:[0,1]
	v_pk_fma_f32 v[94:95], v[76:77], v[84:85], v[92:93] neg_lo:[0,0,1] neg_hi:[0,0,1]
	v_pk_fma_f32 v[84:85], v[76:77], v[84:85], v[92:93] op_sel_hi:[1,0,1]
	v_mul_f32_e32 v92, v79, v87
	v_mov_b32_e32 v95, v85
	v_pk_mul_f32 v[84:85], v[144:145], v[94:95] op_sel_hi:[0,1]
	v_mul_f32_e32 v94, v79, v86
	v_pk_fma_f32 v[92:93], v[78:79], v[86:87], v[92:93] op_sel_hi:[1,1,0] neg_lo:[0,0,1] neg_hi:[0,0,1]
	v_pk_fma_f32 v[86:87], v[78:79], v[86:87], v[94:95] op_sel:[1,0,0] op_sel_hi:[0,1,0]
	v_mov_b32_e32 v93, v87
	v_pk_mul_f32 v[86:87], v[144:145], v[92:93] op_sel_hi:[0,1]
	v_pk_mul_f32 v[92:93], v[72:73], v[88:89] op_sel:[1,1] op_sel_hi:[0,1]
	v_pk_fma_f32 v[94:95], v[72:73], v[88:89], v[92:93] neg_lo:[0,0,1] neg_hi:[0,0,1]
	v_pk_fma_f32 v[88:89], v[72:73], v[88:89], v[92:93] op_sel_hi:[1,0,1]
	v_mul_f32_e32 v92, v75, v91
	v_mov_b32_e32 v95, v89
	v_pk_mul_f32 v[88:89], v[144:145], v[94:95] op_sel_hi:[0,1]
	v_mul_f32_e32 v94, v75, v90
	v_pk_fma_f32 v[92:93], v[74:75], v[90:91], v[92:93] op_sel_hi:[1,1,0] neg_lo:[0,0,1] neg_hi:[0,0,1]
	v_pk_fma_f32 v[90:91], v[74:75], v[90:91], v[94:95] op_sel:[1,0,0] op_sel_hi:[0,1,0]
	v_mov_b32_e32 v93, v91
	v_pk_mul_f32 v[90:91], v[144:145], v[92:93] op_sel_hi:[0,1]

; __device__ __forceinline__ unsigned cvt_pk_bf16(float lo, float hi) { unsigned r; asm volatile("v_cvt_pk_bf16_f32 %0, %1, %2" : "=v"(r) : "v"(lo), "v"(hi)); return r; }
;     __device__ __forceinline__ void operator()(const f32x4 (&acc)[2][2][4][2], const Unit& u, int wr, int wc, int fr, int fq) const {
;     ...
;                     f32x4 v0 = acc[ai][bj][m][0] * rs, v1 = acc[ai][bj][m][1] * rs;
;                     if (kind <= 1) {
;                         float s = (v0[0] * v0[0] + v0[1] * v0[1]) + (v0[2] * v0[2] + v0[3] * v0[3]) + (v1[0] * v1[0] + v1[1] * v1[1]) + (v1[2] * v1[2] + v1[3] * v1[3]);
;                         s += __shfl_xor(s, 16); s += __shfl_xor(s, 32);
;                         const int head = (u.pn & 3) * 2 + bj;
;                         if (fq == 0) ssq[(size_t)((kind * 8 + head) * 4 + wc) * MT + row] = s;
;                     } else if (kind <= 3) {
;                         const int i0 = (c0 & 127) >> 1;
;                         const f32x4 csa = *(const f32x4*)(cs + (size_t)pos * 64 + i0), csb = *(const f32x4*)(cs + (size_t)pos * 64 + i0 + 2);
;                         const float sc = (kind == 3) ? KSCALE : 1.0f;
;                         f32x4 w0, w1;
;                         w0[0] = (v0[0] * csa[0] - v0[1] * csa[1]) * sc; w0[1] = (v0[1] * csa[0] + v0[0] * csa[1]) * sc;
;                         w0[2] = (v0[2] * csa[2] - v0[3] * csa[3]) * sc; w0[3] = (v0[3] * csa[2] + v0[2] * csa[3]) * sc;
;                         w1[0] = (v1[0] * csb[0] - v1[1] * csb[1]) * sc; w1[1] = (v1[1] * csb[0] + v1[0] * csb[1]) * sc;
;                         w1[2] = (v1[2] * csb[2] - v1[3] * csb[3]) * sc; w1[3] = (v1[3] * csb[2] + v1[2] * csb[3]) * sc;
;                         v0 = w0; v1 = w1;
;                     } else {
; #pragma unroll
;                         for (int j = 0; j < 4; ++j) { v0[j] = v0[j] * __builtin_amdgcn_rcpf(1.0f + __builtin_amdgcn_exp2f(-1.4426950408889634f * v0[j]));
;                                                       v1[j] = v1[j] * __builtin_amdgcn_rcpf(1.0f + __builtin_amdgcn_exp2f(-1.4426950408889634f * v1[j])); }
;                     }
;                     u32x4 w; w.x = cvt_pk_bf16(v0[0], v0[1]); w.y = cvt_pk_bf16(v0[2], v0[3]); w.z = cvt_pk_bf16(v1[0], v1[1]); w.w = cvt_pk_bf16(v1[2], v1[3]);
;                     *(u32x4*)(O + (size_t)row * TOKP + c0) = w;
.LBB0_296:
	v_mov_b64_e32 v[72:73], s[80:81]
	s_movk_i32 s0, 0x2900
	v_mad_i64_i32 v[72:73], s[0:1], v82, s0, v[72:73]
	v_cvt_pk_bf16_f32 v74, v84, v85
	v_cvt_pk_bf16_f32 v75, v86, v87
	v_lshl_add_u64 v[72:73], v[120:121], 1, v[72:73]
	v_mov_b32_e32 v81, v80
	v_cvt_pk_bf16_f32 v76, v88, v89
	v_cvt_pk_bf16_f32 v77, v90, v91
	v_and_b32_e32 v244, -16, v82
	v_lshlrev_b32_e32 v244, 12, v244
	v_mov_b32_e32 v245, 0
	v_lshl_add_u64 v[246:247], v[244:245], 0, v[238:239]
	v_cndmask_b32_e64 v246, v72, v246, s[100:101]
	v_cndmask_b32_e64 v247, v73, v247, s[100:101]
	v_lshl_add_u64 v[248:249], v[246:247], 0, v[242:243]
	global_store_dwordx4 v[246:247], v[74:77], off
	v_pk_mul_f32 v[68:69], v[68:69], v[80:81]
	v_pk_mul_f32 v[64:65], v[64:65], v[80:81]
	v_mov_b32_e32 v74, v80
	v_mov_b32_e32 v75, v80
	v_pk_mul_f32 v[70:71], v[70:71], v[74:75]
	v_pk_mul_f32 v[66:67], v[66:67], v[74:75]
	s_and_b64 vcc, exec, s[40:41]
	s_mov_b64 s[0:1], -1
	s_cbranch_vccnz .LBB0_302
	s_and_b64 vcc, exec, s[38:39]
	s_cbranch_vccnz .LBB0_299
	v_mul_f32_e32 v75, 0xbfb8aa3b, v64
	v_mul_f32_e32 v76, 0xbfb8aa3b, v69
	v_exp_f32_e32 v75, v75
	v_exp_f32_e32 v76, v76
	v_mul_f32_e32 v77, 0xbfb8aa3b, v70
	v_mul_f32_e32 v79, 0xbfb8aa3b, v66
	v_add_f32_e32 v75, 1.0, v75
	v_rcp_f32_e32 v78, v75
	v_add_f32_e32 v75, 1.0, v76
	v_mul_f32_e32 v76, 0xbfb8aa3b, v65
	v_exp_f32_e32 v76, v76
	v_exp_f32_e32 v77, v77
	v_exp_f32_e32 v79, v79
	v_mul_f32_e32 v74, 0xbfb8aa3b, v68
	v_add_f32_e32 v82, 1.0, v76
	v_add_f32_e32 v76, 1.0, v77
	v_add_f32_e32 v77, 1.0, v79
	v_mul_f32_e32 v79, 0xbfb8aa3b, v71
	v_mul_f32_e32 v80, 0xbfb8aa3b, v67
	v_exp_f32_e32 v74, v74
	v_exp_f32_e32 v79, v79
	v_exp_f32_e32 v81, v80
	v_rcp_f32_e32 v80, v77
	v_add_f32_e32 v74, 1.0, v74
	v_add_f32_e32 v77, 1.0, v79
	v_add_f32_e32 v79, 1.0, v81
	v_rcp_f32_e32 v74, v74
	v_rcp_f32_e32 v75, v75
	v_rcp_f32_e32 v76, v76
	v_rcp_f32_e32 v77, v77
	v_rcp_f32_e32 v81, v79
	v_rcp_f32_e32 v79, v82
	v_pk_mul_f32 v[74:75], v[68:69], v[74:75]
	v_pk_mul_f32 v[76:77], v[70:71], v[76:77]
	v_pk_mul_f32 v[80:81], v[66:67], v[80:81]
	v_pk_mul_f32 v[78:79], v[64:65], v[78:79]
	s_mov_b64 s[0:1], 0

;     __device__ __forceinline__ void operator()(const f32x4 (&acc)[2][2][4][2], const Unit& u, int wr, int wc, int fr, int fq) const {
;     ...
;                 const int row = row0 + ai * HALF + m * 16, pos = row & (MS - 1);
;                 const float rs = rstd[row];
; #pragma unroll
;                 for (int bj = 0; bj < 2; ++bj) {
;                     const int c0 = u.pn * BM + bj * HALF + wc * 32 + 8 * fq;
;                     f32x4 v0 = acc[ai][bj][m][0] * rs, v1 = acc[ai][bj][m][1] * rs;
;                     if (kind <= 1) {
;                         float s = (v0[0] * v0[0] + v0[1] * v0[1]) + (v0[2] * v0[2] + v0[3] * v0[3]) + (v1[0] * v1[0] + v1[1] * v1[1]) + (v1[2] * v1[2] + v1[3] * v1[3]);
;                         s += __shfl_xor(s, 16); s += __shfl_xor(s, 32);
;                         const int head = (u.pn & 3) * 2 + bj;
;                         if (fq == 0) ssq[(size_t)((kind * 8 + head) * 4 + wc) * MT + row] = s;
;                     } else if (kind <= 3) {
;                         const int i0 = (c0 & 127) >> 1;
;                         const f32x4 csa = *(const f32x4*)(cs + (size_t)pos * 64 + i0), csb = *(const f32x4*)(cs + (size_t)pos * 64 + i0 + 2);
;                         const float sc = (kind == 3) ? KSCALE : 1.0f;
;                         f32x4 w0, w1;
;                         w0[0] = (v0[0] * csa[0] - v0[1] * csa[1]) * sc; w0[1] = (v0[1] * csa[0] + v0[0] * csa[1]) * sc;
;                         w0[2] = (v0[2] * csa[2] - v0[3] * csa[3]) * sc; w0[3] = (v0[3] * csa[2] + v0[2] * csa[3]) * sc;
;                         w1[0] = (v1[0] * csb[0] - v1[1] * csb[1]) * sc; w1[1] = (v1[1] * csb[0] + v1[0] * csb[1]) * sc;
;                         w1[2] = (v1[2] * csb[2] - v1[3] * csb[3]) * sc; w1[3] = (v1[3] * csb[2] + v1[2] * csb[3]) * sc;
;                         v0 = w0; v1 = w1;
;                     } else {
; #pragma unroll
;                         for (int j = 0; j < 4; ++j) { v0[j] = v0[j] * __builtin_amdgcn_rcpf(1.0f + __builtin_amdgcn_exp2f(-1.4426950408889634f * v0[j]));
;                                                       v1[j] = v1[j] * __builtin_amdgcn_rcpf(1.0f + __builtin_amdgcn_exp2f(-1.4426950408889634f * v1[j])); }
;                     }
;                     u32x4 w; w.x = cvt_pk_bf16(v0[0], v0[1]); w.y = cvt_pk_bf16(v0[2], v0[3]); w.z = cvt_pk_bf16(v1[0], v1[1]); w.w = cvt_pk_bf16(v1[2], v1[3]);
.LBB0_306:
	v_cvt_pk_bf16_f32 v64, v74, v75
	v_cvt_pk_bf16_f32 v65, v76, v77
	v_cvt_pk_bf16_f32 v66, v78, v79
	v_cvt_pk_bf16_f32 v67, v80, v81
	global_store_dwordx4 v[248:249], v[64:67], off
	s_nop 1
	v_mov_b32_e32 v64, v229
	v_add_u32_e32 v75, 0x80, v142
	v_lshlrev_b32_e32 v65, 6, v75
	s_and_b64 vcc, exec, s[40:41]
	v_and_b32_e32 v74, 0x1f3c0, v65
	s_mov_b64 s[0:1], -1
	v_pk_mul_f32 v[62:63], v[62:63], v[64:65] op_sel_hi:[1,0]
	v_pk_mul_f32 v[60:61], v[60:61], v[64:65] op_sel_hi:[1,0]
	v_pk_mul_f32 v[58:59], v[58:59], v[64:65] op_sel_hi:[1,0]
	v_pk_mul_f32 v[56:57], v[56:57], v[64:65] op_sel_hi:[1,0]
	s_cbranch_vccnz .LBB0_312
	s_and_b64 vcc, exec, s[38:39]
	s_cbranch_vccnz .LBB0_309
	v_mul_f32_e32 v65, 0xbfb8aa3b, v60
	v_exp_f32_e32 v65, v65
	v_mul_f32_e32 v66, 0xbfb8aa3b, v56
	v_mul_f32_e32 v67, 0xbfb8aa3b, v61
	v_exp_f32_e32 v68, v66
	v_exp_f32_e32 v67, v67
	v_add_f32_e32 v65, 1.0, v65
	v_rcp_f32_e32 v66, v65
	v_add_f32_e32 v65, 1.0, v68
	v_rcp_f32_e32 v70, v65
	v_add_f32_e32 v65, 1.0, v67
	v_mul_f32_e32 v69, 0xbfb8aa3b, v58
	v_rcp_f32_e32 v67, v65
	v_mul_f32_e32 v65, 0xbfb8aa3b, v57
	v_mul_f32_e32 v68, 0xbfb8aa3b, v62
	v_exp_f32_e32 v69, v69
	v_mul_f32_e32 v71, 0xbfb8aa3b, v63
	v_mul_f32_e32 v72, 0xbfb8aa3b, v59
	v_exp_f32_e32 v65, v65
	v_exp_f32_e32 v68, v68
	v_exp_f32_e32 v71, v71
	v_exp_f32_e32 v73, v72
	v_add_f32_e32 v69, 1.0, v69
	v_add_f32_e32 v65, 1.0, v65
	v_add_f32_e32 v68, 1.0, v68
	v_rcp_f32_e32 v72, v69
	v_add_f32_e32 v69, 1.0, v71
	v_add_f32_e32 v71, 1.0, v73
	v_rcp_f32_e32 v68, v68
	v_rcp_f32_e32 v69, v69
	v_rcp_f32_e32 v73, v71
	v_rcp_f32_e32 v71, v65
	v_pk_mul_f32 v[66:67], v[60:61], v[66:67]
	v_pk_mul_f32 v[68:69], v[62:63], v[68:69]
	v_pk_mul_f32 v[72:73], v[58:59], v[72:73]
	v_pk_mul_f32 v[70:71], v[56:57], v[70:71]
	s_mov_b64 s[0:1], 0
.LBB0_309:
	s_andn2_b64 vcc, exec, s[0:1]
	s_cbranch_vccnz .LBB0_311
	v_lshlrev_b32_e32 v184, 3, v74
	v_lshl_add_u64 v[66:67], v[136:137], 0, v[184:185]
	v_add_co_u32_e32 v234, vcc, 0x16000, v236
	s_nop 1
	v_addc_co_u32_e32 v235, vcc, 0, v237, vcc
	global_load_dwordx4 v[202:205], v[234:235], off
	global_load_dwordx4 v[206:209], v[234:235], off offset:16
	s_waitcnt vmcnt(12)
	v_mov_b32_e32 v70, v172
	v_mov_b32_e32 v71, v173
	v_mov_b32_e32 v72, v174
	v_mov_b32_e32 v73, v175
	v_mov_b32_e32 v66, v168
	v_mov_b32_e32 v67, v169
	v_mov_b32_e32 v68, v170
	v_mov_b32_e32 v69, v171
	v_pk_mul_f32 v[76:77], v[60:61], v[66:67] op_sel:[1,1] op_sel_hi:[0,1]
	v_pk_fma_f32 v[78:79], v[60:61], v[66:67], v[76:77] neg_lo:[0,0,1] neg_hi:[0,0,1]
	v_pk_fma_f32 v[66:67], v[60:61], v[66:67], v[76:77] op_sel_hi:[1,0,1]
	v_mul_f32_e32 v76, v63, v69
	v_mov_b32_e32 v79, v67
	v_pk_mul_f32 v[66:67], v[144:145], v[78:79] op_sel_hi:[0,1]
	v_mul_f32_e32 v78, v63, v68
	v_pk_fma_f32 v[76:77], v[62:63], v[68:69], v[76:77] op_sel_hi:[1,1,0] neg_lo:[0,0,1] neg_hi:[0,0,1]
	v_pk_fma_f32 v[68:69], v[62:63], v[68:69], v[78:79] op_sel:[1,0,0] op_sel_hi:[0,1,0]
	v_mov_b32_e32 v77, v69
	v_pk_mul_f32 v[68:69], v[144:145], v[76:77] op_sel_hi:[0,1]
	v_pk_mul_f32 v[76:77], v[56:57], v[70:71] op_sel:[1,1] op_sel_hi:[0,1]
	v_pk_fma_f32 v[78:79], v[56:57], v[70:71], v[76:77] neg_lo:[0,0,1] neg_hi:[0,0,1]
	v_pk_fma_f32 v[70:71], v[56:57], v[70:71], v[76:77] op_sel_hi:[1,0,1]
	v_mul_f32_e32 v76, v59, v73
	v_mov_b32_e32 v79, v71
	v_pk_mul_f32 v[70:71], v[144:145], v[78:79] op_sel_hi:[0,1]
	v_mul_f32_e32 v78, v59, v72
	v_pk_fma_f32 v[76:77], v[58:59], v[72:73], v[76:77] op_sel_hi:[1,1,0] neg_lo:[0,0,1] neg_hi:[0,0,1]
	v_pk_fma_f32 v[72:73], v[58:59], v[72:73], v[78:79] op_sel:[1,0,0] op_sel_hi:[0,1,0]
	v_mov_b32_e32 v77, v73
	v_pk_mul_f32 v[72:73], v[144:145], v[76:77] op_sel_hi:[0,1]

; __device__ __forceinline__ unsigned cvt_pk_bf16(float lo, float hi) { unsigned r; asm volatile("v_cvt_pk_bf16_f32 %0, %1, %2" : "=v"(r) : "v"(lo), "v"(hi)); return r; }
;     __device__ __forceinline__ void operator()(const f32x4 (&acc)[2][2][4][2], const Unit& u, int wr, int wc, int fr, int fq) const {
;     ...
;                     f32x4 v0 = acc[ai][bj][m][0] * rs, v1 = acc[ai][bj][m][1] * rs;
;                     if (kind <= 1) {
;                         float s = (v0[0] * v0[0] + v0[1] * v0[1]) + (v0[2] * v0[2] + v0[3] * v0[3]) + (v1[0] * v1[0] + v1[1] * v1[1]) + (v1[2] * v1[2] + v1[3] * v1[3]);
;                         s += __shfl_xor(s, 16); s += __shfl_xor(s, 32);
;                         const int head = (u.pn & 3) * 2 + bj;
;                         if (fq == 0) ssq[(size_t)((kind * 8 + head) * 4 + wc) * MT + row] = s;
;                     } else if (kind <= 3) {
;                         const int i0 = (c0 & 127) >> 1;
;                         const f32x4 csa = *(const f32x4*)(cs + (size_t)pos * 64 + i0), csb = *(const f32x4*)(cs + (size_t)pos * 64 + i0 + 2);
;                         const float sc = (kind == 3) ? KSCALE : 1.0f;
;                         f32x4 w0, w1;
;                         w0[0] = (v0[0] * csa[0] - v0[1] * csa[1]) * sc; w0[1] = (v0[1] * csa[0] + v0[0] * csa[1]) * sc;
;                         w0[2] = (v0[2] * csa[2] - v0[3] * csa[3]) * sc; w0[3] = (v0[3] * csa[2] + v0[2] * csa[3]) * sc;
;                         w1[0] = (v1[0] * csb[0] - v1[1] * csb[1]) * sc; w1[1] = (v1[1] * csb[0] + v1[0] * csb[1]) * sc;
;                         w1[2] = (v1[2] * csb[2] - v1[3] * csb[3]) * sc; w1[3] = (v1[3] * csb[2] + v1[2] * csb[3]) * sc;
;                         v0 = w0; v1 = w1;
;                     } else {
; #pragma unroll
;                         for (int j = 0; j < 4; ++j) { v0[j] = v0[j] * __builtin_amdgcn_rcpf(1.0f + __builtin_amdgcn_exp2f(-1.4426950408889634f * v0[j]));
;                                                       v1[j] = v1[j] * __builtin_amdgcn_rcpf(1.0f + __builtin_amdgcn_exp2f(-1.4426950408889634f * v1[j])); }
;                     }
;                     u32x4 w; w.x = cvt_pk_bf16(v0[0], v0[1]); w.y = cvt_pk_bf16(v0[2], v0[3]); w.z = cvt_pk_bf16(v1[0], v1[1]); w.w = cvt_pk_bf16(v1[2], v1[3]);
;                     *(u32x4*)(O + (size_t)row * TOKP + c0) = w;
.LBB0_316:
	v_mov_b64_e32 v[56:57], s[80:81]
	s_movk_i32 s0, 0x2900
	v_mad_i64_i32 v[56:57], s[0:1], v75, s0, v[56:57]
	v_cvt_pk_bf16_f32 v58, v66, v67
	v_cvt_pk_bf16_f32 v59, v68, v69
	v_lshl_add_u64 v[56:57], v[120:121], 1, v[56:57]
	v_mov_b32_e32 v65, v64
	v_cvt_pk_bf16_f32 v60, v70, v71
	v_cvt_pk_bf16_f32 v61, v72, v73
	v_and_b32_e32 v244, -16, v75
	v_lshlrev_b32_e32 v244, 12, v244
	v_mov_b32_e32 v245, 0
	v_lshl_add_u64 v[246:247], v[244:245], 0, v[238:239]
	v_cndmask_b32_e64 v246, v56, v246, s[100:101]
	v_cndmask_b32_e64 v247, v57, v247, s[100:101]
	v_lshl_add_u64 v[248:249], v[246:247], 0, v[242:243]
	global_store_dwordx4 v[246:247], v[58:61], off
	v_pk_mul_f32 v[52:53], v[52:53], v[64:65]
	v_pk_mul_f32 v[48:49], v[48:49], v[64:65]
	v_mov_b32_e32 v58, v64
	v_mov_b32_e32 v59, v64
	v_pk_mul_f32 v[54:55], v[54:55], v[58:59]
	v_pk_mul_f32 v[50:51], v[50:51], v[58:59]
	s_and_b64 vcc, exec, s[40:41]
	s_mov_b64 s[0:1], -1
	s_cbranch_vccnz .LBB0_322
	s_and_b64 vcc, exec, s[38:39]
	s_cbranch_vccnz .LBB0_319
	v_mul_f32_e32 v59, 0xbfb8aa3b, v48
	v_mul_f32_e32 v60, 0xbfb8aa3b, v53
	v_exp_f32_e32 v59, v59
	v_exp_f32_e32 v60, v60
	v_mul_f32_e32 v61, 0xbfb8aa3b, v54
	v_mul_f32_e32 v63, 0xbfb8aa3b, v50
	v_add_f32_e32 v59, 1.0, v59
	v_rcp_f32_e32 v62, v59
	v_add_f32_e32 v59, 1.0, v60
	v_mul_f32_e32 v60, 0xbfb8aa3b, v49
	v_exp_f32_e32 v60, v60
	v_exp_f32_e32 v61, v61
	v_exp_f32_e32 v63, v63
	v_mul_f32_e32 v58, 0xbfb8aa3b, v52
	v_add_f32_e32 v66, 1.0, v60
	v_add_f32_e32 v60, 1.0, v61
	v_add_f32_e32 v61, 1.0, v63
	v_mul_f32_e32 v63, 0xbfb8aa3b, v55
	v_mul_f32_e32 v64, 0xbfb8aa3b, v51
	v_exp_f32_e32 v58, v58
	v_exp_f32_e32 v63, v63
	v_exp_f32_e32 v65, v64
	v_rcp_f32_e32 v64, v61
	v_add_f32_e32 v58, 1.0, v58
	v_add_f32_e32 v61, 1.0, v63
	v_add_f32_e32 v63, 1.0, v65
	v_rcp_f32_e32 v58, v58
	v_rcp_f32_e32 v59, v59
	v_rcp_f32_e32 v60, v60
	v_rcp_f32_e32 v61, v61
	v_rcp_f32_e32 v65, v63
	v_rcp_f32_e32 v63, v66
	v_pk_mul_f32 v[58:59], v[52:53], v[58:59]
	v_pk_mul_f32 v[60:61], v[54:55], v[60:61]
	v_pk_mul_f32 v[64:65], v[50:51], v[64:65]
	v_pk_mul_f32 v[62:63], v[48:49], v[62:63]
	s_mov_b64 s[0:1], 0

;     __device__ __forceinline__ void operator()(const f32x4 (&acc)[2][2][4][2], const Unit& u, int wr, int wc, int fr, int fq) const {
;     ...
;                 const int row = row0 + ai * HALF + m * 16, pos = row & (MS - 1);
;                 const float rs = rstd[row];
; #pragma unroll
;                 for (int bj = 0; bj < 2; ++bj) {
;                     const int c0 = u.pn * BM + bj * HALF + wc * 32 + 8 * fq;
;                     f32x4 v0 = acc[ai][bj][m][0] * rs, v1 = acc[ai][bj][m][1] * rs;
;                     if (kind <= 1) {
;                         float s = (v0[0] * v0[0] + v0[1] * v0[1]) + (v0[2] * v0[2] + v0[3] * v0[3]) + (v1[0] * v1[0] + v1[1] * v1[1]) + (v1[2] * v1[2] + v1[3] * v1[3]);
;                         s += __shfl_xor(s, 16); s += __shfl_xor(s, 32);
;                         const int head = (u.pn & 3) * 2 + bj;
;                         if (fq == 0) ssq[(size_t)((kind * 8 + head) * 4 + wc) * MT + row] = s;
;                     } else if (kind <= 3) {
;                         const int i0 = (c0 & 127) >> 1;
;                         const f32x4 csa = *(const f32x4*)(cs + (size_t)pos * 64 + i0), csb = *(const f32x4*)(cs + (size_t)pos * 64 + i0 + 2);
;                         const float sc = (kind == 3) ? KSCALE : 1.0f;
;                         f32x4 w0, w1;
;                         w0[0] = (v0[0] * csa[0] - v0[1] * csa[1]) * sc; w0[1] = (v0[1] * csa[0] + v0[0] * csa[1]) * sc;
;                         w0[2] = (v0[2] * csa[2] - v0[3] * csa[3]) * sc; w0[3] = (v0[3] * csa[2] + v0[2] * csa[3]) * sc;
;                         w1[0] = (v1[0] * csb[0] - v1[1] * csb[1]) * sc; w1[1] = (v1[1] * csb[0] + v1[0] * csb[1]) * sc;
;                         w1[2] = (v1[2] * csb[2] - v1[3] * csb[3]) * sc; w1[3] = (v1[3] * csb[2] + v1[2] * csb[3]) * sc;
;                         v0 = w0; v1 = w1;
;                     } else {
; #pragma unroll
;                         for (int j = 0; j < 4; ++j) { v0[j] = v0[j] * __builtin_amdgcn_rcpf(1.0f + __builtin_amdgcn_exp2f(-1.4426950408889634f * v0[j]));
;                                                       v1[j] = v1[j] * __builtin_amdgcn_rcpf(1.0f + __builtin_amdgcn_exp2f(-1.4426950408889634f * v1[j])); }
;                     }
;                     u32x4 w; w.x = cvt_pk_bf16(v0[0], v0[1]); w.y = cvt_pk_bf16(v0[2], v0[3]); w.z = cvt_pk_bf16(v1[0], v1[1]); w.w = cvt_pk_bf16(v1[2], v1[3]);
.LBB0_326:
	v_cvt_pk_bf16_f32 v48, v58, v59
	v_cvt_pk_bf16_f32 v49, v60, v61
	v_cvt_pk_bf16_f32 v50, v62, v63
	v_cvt_pk_bf16_f32 v51, v64, v65
	global_store_dwordx4 v[248:249], v[48:51], off
	s_nop 1
	v_mov_b32_e32 v48, v230
	v_add_u32_e32 v59, 0x90, v142
	v_lshlrev_b32_e32 v49, 6, v59
	s_and_b64 vcc, exec, s[40:41]
	v_and_b32_e32 v58, 0x1f7c0, v49
	s_mov_b64 s[0:1], -1
	v_pk_mul_f32 v[46:47], v[46:47], v[48:49] op_sel_hi:[1,0]
	v_pk_mul_f32 v[44:45], v[44:45], v[48:49] op_sel_hi:[1,0]
	v_pk_mul_f32 v[42:43], v[42:43], v[48:49] op_sel_hi:[1,0]
	v_pk_mul_f32 v[40:41], v[40:41], v[48:49] op_sel_hi:[1,0]
	s_cbranch_vccnz .LBB0_332
	s_and_b64 vcc, exec, s[38:39]
	s_cbranch_vccnz .LBB0_329
	v_mul_f32_e32 v49, 0xbfb8aa3b, v44
	v_exp_f32_e32 v49, v49
	v_mul_f32_e32 v50, 0xbfb8aa3b, v40
	v_mul_f32_e32 v51, 0xbfb8aa3b, v45
	v_exp_f32_e32 v52, v50
	v_exp_f32_e32 v51, v51
	v_add_f32_e32 v49, 1.0, v49
	v_rcp_f32_e32 v50, v49
	v_add_f32_e32 v49, 1.0, v52
	v_rcp_f32_e32 v54, v49
	v_add_f32_e32 v49, 1.0, v51
	v_mul_f32_e32 v53, 0xbfb8aa3b, v42
	v_rcp_f32_e32 v51, v49
	v_mul_f32_e32 v49, 0xbfb8aa3b, v41
	v_mul_f32_e32 v52, 0xbfb8aa3b, v46
	v_exp_f32_e32 v53, v53
	v_mul_f32_e32 v55, 0xbfb8aa3b, v47
	v_mul_f32_e32 v56, 0xbfb8aa3b, v43
	v_exp_f32_e32 v49, v49
	v_exp_f32_e32 v52, v52
	v_exp_f32_e32 v55, v55
	v_exp_f32_e32 v57, v56
	v_add_f32_e32 v53, 1.0, v53
	v_add_f32_e32 v49, 1.0, v49
	v_add_f32_e32 v52, 1.0, v52
	v_rcp_f32_e32 v56, v53
	v_add_f32_e32 v53, 1.0, v55
	v_add_f32_e32 v55, 1.0, v57
	v_rcp_f32_e32 v52, v52
	v_rcp_f32_e32 v53, v53
	v_rcp_f32_e32 v57, v55
	v_rcp_f32_e32 v55, v49
	v_pk_mul_f32 v[50:51], v[44:45], v[50:51]
	v_pk_mul_f32 v[52:53], v[46:47], v[52:53]
	v_pk_mul_f32 v[56:57], v[42:43], v[56:57]
	v_pk_mul_f32 v[54:55], v[40:41], v[54:55]
	s_mov_b64 s[0:1], 0

; __device__ __forceinline__ unsigned cvt_pk_bf16(float lo, float hi) { unsigned r; asm volatile("v_cvt_pk_bf16_f32 %0, %1, %2" : "=v"(r) : "v"(lo), "v"(hi)); return r; }
;     __device__ __forceinline__ void operator()(const f32x4 (&acc)[2][2][4][2], const Unit& u, int wr, int wc, int fr, int fq) const {
;     ...
;                     f32x4 v0 = acc[ai][bj][m][0] * rs, v1 = acc[ai][bj][m][1] * rs;
;                     if (kind <= 1) {
;                         float s = (v0[0] * v0[0] + v0[1] * v0[1]) + (v0[2] * v0[2] + v0[3] * v0[3]) + (v1[0] * v1[0] + v1[1] * v1[1]) + (v1[2] * v1[2] + v1[3] * v1[3]);
;                         s += __shfl_xor(s, 16); s += __shfl_xor(s, 32);
;                         const int head = (u.pn & 3) * 2 + bj;
;                         if (fq == 0) ssq[(size_t)((kind * 8 + head) * 4 + wc) * MT + row] = s;
;                     } else if (kind <= 3) {
;                         const int i0 = (c0 & 127) >> 1;
;                         const f32x4 csa = *(const f32x4*)(cs + (size_t)pos * 64 + i0), csb = *(const f32x4*)(cs + (size_t)pos * 64 + i0 + 2);
;                         const float sc = (kind == 3) ? KSCALE : 1.0f;
;                         f32x4 w0, w1;
;                         w0[0] = (v0[0] * csa[0] - v0[1] * csa[1]) * sc; w0[1] = (v0[1] * csa[0] + v0[0] * csa[1]) * sc;
;                         w0[2] = (v0[2] * csa[2] - v0[3] * csa[3]) * sc; w0[3] = (v0[3] * csa[2] + v0[2] * csa[3]) * sc;
;                         w1[0] = (v1[0] * csb[0] - v1[1] * csb[1]) * sc; w1[1] = (v1[1] * csb[0] + v1[0] * csb[1]) * sc;
;                         w1[2] = (v1[2] * csb[2] - v1[3] * csb[3]) * sc; w1[3] = (v1[3] * csb[2] + v1[2] * csb[3]) * sc;
;                         v0 = w0; v1 = w1;
;                     } else {
; #pragma unroll
;                         for (int j = 0; j < 4; ++j) { v0[j] = v0[j] * __builtin_amdgcn_rcpf(1.0f + __builtin_amdgcn_exp2f(-1.4426950408889634f * v0[j]));
;                                                       v1[j] = v1[j] * __builtin_amdgcn_rcpf(1.0f + __builtin_amdgcn_exp2f(-1.4426950408889634f * v1[j])); }
;                     }
;                     u32x4 w; w.x = cvt_pk_bf16(v0[0], v0[1]); w.y = cvt_pk_bf16(v0[2], v0[3]); w.z = cvt_pk_bf16(v1[0], v1[1]); w.w = cvt_pk_bf16(v1[2], v1[3]);
;                     *(u32x4*)(O + (size_t)row * TOKP + c0) = w;
.LBB0_336:
	v_mov_b64_e32 v[40:41], s[80:81]
	s_movk_i32 s0, 0x2900
	v_mad_i64_i32 v[40:41], s[0:1], v59, s0, v[40:41]
	v_cvt_pk_bf16_f32 v42, v50, v51
	v_cvt_pk_bf16_f32 v43, v52, v53
	v_lshl_add_u64 v[40:41], v[120:121], 1, v[40:41]
	v_mov_b32_e32 v49, v48
	v_cvt_pk_bf16_f32 v44, v54, v55
	v_cvt_pk_bf16_f32 v45, v56, v57
	v_and_b32_e32 v244, -16, v59
	v_lshlrev_b32_e32 v244, 12, v244
	v_mov_b32_e32 v245, 0
	v_lshl_add_u64 v[246:247], v[244:245], 0, v[238:239]
	v_cndmask_b32_e64 v246, v40, v246, s[100:101]
	v_cndmask_b32_e64 v247, v41, v247, s[100:101]
	v_lshl_add_u64 v[248:249], v[246:247], 0, v[242:243]
	global_store_dwordx4 v[246:247], v[42:45], off
	v_pk_mul_f32 v[36:37], v[36:37], v[48:49]
	v_pk_mul_f32 v[32:33], v[32:33], v[48:49]
	v_mov_b32_e32 v42, v48
	v_mov_b32_e32 v43, v48
	v_pk_mul_f32 v[38:39], v[38:39], v[42:43]
	v_pk_mul_f32 v[34:35], v[34:35], v[42:43]
	s_and_b64 vcc, exec, s[40:41]
	s_mov_b64 s[0:1], -1
	s_cbranch_vccnz .LBB0_342
	s_and_b64 vcc, exec, s[38:39]
	s_cbranch_vccnz .LBB0_339
	v_mul_f32_e32 v43, 0xbfb8aa3b, v32
	v_mul_f32_e32 v44, 0xbfb8aa3b, v37
	v_exp_f32_e32 v43, v43
	v_exp_f32_e32 v44, v44
	v_mul_f32_e32 v45, 0xbfb8aa3b, v38
	v_mul_f32_e32 v47, 0xbfb8aa3b, v34
	v_add_f32_e32 v43, 1.0, v43
	v_rcp_f32_e32 v46, v43
	v_add_f32_e32 v43, 1.0, v44
	v_mul_f32_e32 v44, 0xbfb8aa3b, v33
	v_exp_f32_e32 v44, v44
	v_exp_f32_e32 v45, v45
	v_exp_f32_e32 v47, v47
	v_mul_f32_e32 v42, 0xbfb8aa3b, v36
	v_add_f32_e32 v50, 1.0, v44
	v_add_f32_e32 v44, 1.0, v45
	v_add_f32_e32 v45, 1.0, v47
	v_mul_f32_e32 v47, 0xbfb8aa3b, v39
	v_mul_f32_e32 v48, 0xbfb8aa3b, v35
	v_exp_f32_e32 v42, v42
	v_exp_f32_e32 v47, v47
	v_exp_f32_e32 v49, v48
	v_rcp_f32_e32 v48, v45
	v_add_f32_e32 v42, 1.0, v42
	v_add_f32_e32 v45, 1.0, v47
	v_add_f32_e32 v47, 1.0, v49
	v_rcp_f32_e32 v42, v42
	v_rcp_f32_e32 v43, v43
	v_rcp_f32_e32 v44, v44
	v_rcp_f32_e32 v45, v45
	v_rcp_f32_e32 v49, v47
	v_rcp_f32_e32 v47, v50
	v_pk_mul_f32 v[42:43], v[36:37], v[42:43]
	v_pk_mul_f32 v[44:45], v[38:39], v[44:45]
	v_pk_mul_f32 v[48:49], v[34:35], v[48:49]
	v_pk_mul_f32 v[46:47], v[32:33], v[46:47]
	s_mov_b64 s[0:1], 0

;     __device__ __forceinline__ void operator()(const f32x4 (&acc)[2][2][4][2], const Unit& u, int wr, int wc, int fr, int fq) const {
;     ...
;                 const int row = row0 + ai * HALF + m * 16, pos = row & (MS - 1);
;                 const float rs = rstd[row];
; #pragma unroll
;                 for (int bj = 0; bj < 2; ++bj) {
;                     const int c0 = u.pn * BM + bj * HALF + wc * 32 + 8 * fq;
;                     f32x4 v0 = acc[ai][bj][m][0] * rs, v1 = acc[ai][bj][m][1] * rs;
;                     if (kind <= 1) {
;                         float s = (v0[0] * v0[0] + v0[1] * v0[1]) + (v0[2] * v0[2] + v0[3] * v0[3]) + (v1[0] * v1[0] + v1[1] * v1[1]) + (v1[2] * v1[2] + v1[3] * v1[3]);
;                         s += __shfl_xor(s, 16); s += __shfl_xor(s, 32);
;                         const int head = (u.pn & 3) * 2 + bj;
;                         if (fq == 0) ssq[(size_t)((kind * 8 + head) * 4 + wc) * MT + row] = s;
;                     } else if (kind <= 3) {
;                         const int i0 = (c0 & 127) >> 1;
;                         const f32x4 csa = *(const f32x4*)(cs + (size_t)pos * 64 + i0), csb = *(const f32x4*)(cs + (size_t)pos * 64 + i0 + 2);
;                         const float sc = (kind == 3) ? KSCALE : 1.0f;
;                         f32x4 w0, w1;
;                         w0[0] = (v0[0] * csa[0] - v0[1] * csa[1]) * sc; w0[1] = (v0[1] * csa[0] + v0[0] * csa[1]) * sc;
;                         w0[2] = (v0[2] * csa[2] - v0[3] * csa[3]) * sc; w0[3] = (v0[3] * csa[2] + v0[2] * csa[3]) * sc;
;                         w1[0] = (v1[0] * csb[0] - v1[1] * csb[1]) * sc; w1[1] = (v1[1] * csb[0] + v1[0] * csb[1]) * sc;
;                         w1[2] = (v1[2] * csb[2] - v1[3] * csb[3]) * sc; w1[3] = (v1[3] * csb[2] + v1[2] * csb[3]) * sc;
;                         v0 = w0; v1 = w1;
;                     } else {
; #pragma unroll
;                         for (int j = 0; j < 4; ++j) { v0[j] = v0[j] * __builtin_amdgcn_rcpf(1.0f + __builtin_amdgcn_exp2f(-1.4426950408889634f * v0[j]));
;                                                       v1[j] = v1[j] * __builtin_amdgcn_rcpf(1.0f + __builtin_amdgcn_exp2f(-1.4426950408889634f * v1[j])); }
;                     }
;                     u32x4 w; w.x = cvt_pk_bf16(v0[0], v0[1]); w.y = cvt_pk_bf16(v0[2], v0[3]); w.z = cvt_pk_bf16(v1[0], v1[1]); w.w = cvt_pk_bf16(v1[2], v1[3]);
.LBB0_346:
	v_cvt_pk_bf16_f32 v32, v42, v43
	v_cvt_pk_bf16_f32 v33, v44, v45
	v_cvt_pk_bf16_f32 v34, v46, v47
	v_cvt_pk_bf16_f32 v35, v48, v49
	global_store_dwordx4 v[248:249], v[32:35], off
	s_nop 1
	v_mov_b32_e32 v32, v231
	v_add_u32_e32 v43, 0xa0, v142
	v_lshlrev_b32_e32 v33, 6, v43
	s_and_b64 vcc, exec, s[40:41]
	v_and_b32_e32 v42, 0x1fbc0, v33
	s_mov_b64 s[0:1], -1
	v_pk_mul_f32 v[30:31], v[30:31], v[32:33] op_sel_hi:[1,0]
	v_pk_mul_f32 v[28:29], v[28:29], v[32:33] op_sel_hi:[1,0]
	v_pk_mul_f32 v[26:27], v[26:27], v[32:33] op_sel_hi:[1,0]
	v_pk_mul_f32 v[24:25], v[24:25], v[32:33] op_sel_hi:[1,0]
	s_cbranch_vccnz .LBB0_352
	s_and_b64 vcc, exec, s[38:39]
	s_cbranch_vccnz .LBB0_349
	v_mul_f32_e32 v33, 0xbfb8aa3b, v28
	v_exp_f32_e32 v33, v33
	v_mul_f32_e32 v34, 0xbfb8aa3b, v24
	v_mul_f32_e32 v35, 0xbfb8aa3b, v29
	v_exp_f32_e32 v36, v34
	v_exp_f32_e32 v35, v35
	v_add_f32_e32 v33, 1.0, v33
	v_rcp_f32_e32 v34, v33
	v_add_f32_e32 v33, 1.0, v36
	v_rcp_f32_e32 v38, v33
	v_add_f32_e32 v33, 1.0, v35
	v_mul_f32_e32 v37, 0xbfb8aa3b, v26
	v_rcp_f32_e32 v35, v33
	v_mul_f32_e32 v33, 0xbfb8aa3b, v25
	v_mul_f32_e32 v36, 0xbfb8aa3b, v30
	v_exp_f32_e32 v37, v37
	v_mul_f32_e32 v39, 0xbfb8aa3b, v31
	v_mul_f32_e32 v40, 0xbfb8aa3b, v27
	v_exp_f32_e32 v33, v33
	v_exp_f32_e32 v36, v36
	v_exp_f32_e32 v39, v39
	v_exp_f32_e32 v41, v40
	v_add_f32_e32 v37, 1.0, v37
	v_add_f32_e32 v33, 1.0, v33
	v_add_f32_e32 v36, 1.0, v36
	v_rcp_f32_e32 v40, v37
	v_add_f32_e32 v37, 1.0, v39
	v_add_f32_e32 v39, 1.0, v41
	v_rcp_f32_e32 v36, v36
	v_rcp_f32_e32 v37, v37
	v_rcp_f32_e32 v41, v39
	v_rcp_f32_e32 v39, v33
	v_pk_mul_f32 v[34:35], v[28:29], v[34:35]
	v_pk_mul_f32 v[36:37], v[30:31], v[36:37]
	v_pk_mul_f32 v[40:41], v[26:27], v[40:41]
	v_pk_mul_f32 v[38:39], v[24:25], v[38:39]
	s_mov_b64 s[0:1], 0

; __device__ __forceinline__ unsigned cvt_pk_bf16(float lo, float hi) { unsigned r; asm volatile("v_cvt_pk_bf16_f32 %0, %1, %2" : "=v"(r) : "v"(lo), "v"(hi)); return r; }
;     __device__ __forceinline__ void operator()(const f32x4 (&acc)[2][2][4][2], const Unit& u, int wr, int wc, int fr, int fq) const {
;     ...
;                     f32x4 v0 = acc[ai][bj][m][0] * rs, v1 = acc[ai][bj][m][1] * rs;
;                     if (kind <= 1) {
;                         float s = (v0[0] * v0[0] + v0[1] * v0[1]) + (v0[2] * v0[2] + v0[3] * v0[3]) + (v1[0] * v1[0] + v1[1] * v1[1]) + (v1[2] * v1[2] + v1[3] * v1[3]);
;                         s += __shfl_xor(s, 16); s += __shfl_xor(s, 32);
;                         const int head = (u.pn & 3) * 2 + bj;
;                         if (fq == 0) ssq[(size_t)((kind * 8 + head) * 4 + wc) * MT + row] = s;
;                     } else if (kind <= 3) {
;                         const int i0 = (c0 & 127) >> 1;
;                         const f32x4 csa = *(const f32x4*)(cs + (size_t)pos * 64 + i0), csb = *(const f32x4*)(cs + (size_t)pos * 64 + i0 + 2);
;                         const float sc = (kind == 3) ? KSCALE : 1.0f;
;                         f32x4 w0, w1;
;                         w0[0] = (v0[0] * csa[0] - v0[1] * csa[1]) * sc; w0[1] = (v0[1] * csa[0] + v0[0] * csa[1]) * sc;
;                         w0[2] = (v0[2] * csa[2] - v0[3] * csa[3]) * sc; w0[3] = (v0[3] * csa[2] + v0[2] * csa[3]) * sc;
;                         w1[0] = (v1[0] * csb[0] - v1[1] * csb[1]) * sc; w1[1] = (v1[1] * csb[0] + v1[0] * csb[1]) * sc;
;                         w1[2] = (v1[2] * csb[2] - v1[3] * csb[3]) * sc; w1[3] = (v1[3] * csb[2] + v1[2] * csb[3]) * sc;
;                         v0 = w0; v1 = w1;
;                     } else {
; #pragma unroll
;                         for (int j = 0; j < 4; ++j) { v0[j] = v0[j] * __builtin_amdgcn_rcpf(1.0f + __builtin_amdgcn_exp2f(-1.4426950408889634f * v0[j]));
;                                                       v1[j] = v1[j] * __builtin_amdgcn_rcpf(1.0f + __builtin_amdgcn_exp2f(-1.4426950408889634f * v1[j])); }
;                     }
;                     u32x4 w; w.x = cvt_pk_bf16(v0[0], v0[1]); w.y = cvt_pk_bf16(v0[2], v0[3]); w.z = cvt_pk_bf16(v1[0], v1[1]); w.w = cvt_pk_bf16(v1[2], v1[3]);
;                     *(u32x4*)(O + (size_t)row * TOKP + c0) = w;
.LBB0_356:
	v_mov_b64_e32 v[24:25], s[80:81]
	s_movk_i32 s0, 0x2900
	v_mad_i64_i32 v[24:25], s[0:1], v43, s0, v[24:25]
	v_cvt_pk_bf16_f32 v26, v34, v35
	v_cvt_pk_bf16_f32 v27, v36, v37
	v_lshl_add_u64 v[24:25], v[120:121], 1, v[24:25]
	v_mov_b32_e32 v33, v32
	v_cvt_pk_bf16_f32 v28, v38, v39
	v_cvt_pk_bf16_f32 v29, v40, v41
	v_and_b32_e32 v244, -16, v43
	v_lshlrev_b32_e32 v244, 12, v244
	v_mov_b32_e32 v245, 0
	v_lshl_add_u64 v[246:247], v[244:245], 0, v[238:239]
	v_cndmask_b32_e64 v246, v24, v246, s[100:101]
	v_cndmask_b32_e64 v247, v25, v247, s[100:101]
	v_lshl_add_u64 v[248:249], v[246:247], 0, v[242:243]
	global_store_dwordx4 v[246:247], v[26:29], off
	v_pk_mul_f32 v[20:21], v[20:21], v[32:33]
	v_pk_mul_f32 v[16:17], v[16:17], v[32:33]
	v_mov_b32_e32 v26, v32
	v_mov_b32_e32 v27, v32
	v_pk_mul_f32 v[22:23], v[22:23], v[26:27]
	v_pk_mul_f32 v[18:19], v[18:19], v[26:27]
	s_and_b64 vcc, exec, s[40:41]
	s_mov_b64 s[0:1], -1
	s_cbranch_vccnz .LBB0_362
	s_and_b64 vcc, exec, s[38:39]
	s_cbranch_vccnz .LBB0_359
	v_mul_f32_e32 v27, 0xbfb8aa3b, v16
	v_mul_f32_e32 v28, 0xbfb8aa3b, v21
	v_exp_f32_e32 v27, v27
	v_exp_f32_e32 v28, v28
	v_mul_f32_e32 v29, 0xbfb8aa3b, v22
	v_mul_f32_e32 v31, 0xbfb8aa3b, v18
	v_add_f32_e32 v27, 1.0, v27
	v_rcp_f32_e32 v30, v27
	v_add_f32_e32 v27, 1.0, v28
	v_mul_f32_e32 v28, 0xbfb8aa3b, v17
	v_exp_f32_e32 v28, v28
	v_exp_f32_e32 v29, v29
	v_exp_f32_e32 v31, v31
	v_mul_f32_e32 v26, 0xbfb8aa3b, v20
	v_add_f32_e32 v34, 1.0, v28
	v_add_f32_e32 v28, 1.0, v29
	v_add_f32_e32 v29, 1.0, v31
	v_mul_f32_e32 v31, 0xbfb8aa3b, v23
	v_mul_f32_e32 v32, 0xbfb8aa3b, v19
	v_exp_f32_e32 v26, v26
	v_exp_f32_e32 v31, v31
	v_exp_f32_e32 v33, v32
	v_rcp_f32_e32 v32, v29
	v_add_f32_e32 v26, 1.0, v26
	v_add_f32_e32 v29, 1.0, v31
	v_add_f32_e32 v31, 1.0, v33
	v_rcp_f32_e32 v26, v26
	v_rcp_f32_e32 v27, v27
	v_rcp_f32_e32 v28, v28
	v_rcp_f32_e32 v29, v29
	v_rcp_f32_e32 v33, v31
	v_rcp_f32_e32 v31, v34
	v_pk_mul_f32 v[26:27], v[20:21], v[26:27]
	v_pk_mul_f32 v[28:29], v[22:23], v[28:29]
	v_pk_mul_f32 v[32:33], v[18:19], v[32:33]
	v_pk_mul_f32 v[30:31], v[16:17], v[30:31]
	s_mov_b64 s[0:1], 0

;     __device__ __forceinline__ void operator()(const f32x4 (&acc)[2][2][4][2], const Unit& u, int wr, int wc, int fr, int fq) const {
;     ...
;                 const int row = row0 + ai * HALF + m * 16, pos = row & (MS - 1);
;                 const float rs = rstd[row];
; #pragma unroll
;                 for (int bj = 0; bj < 2; ++bj) {
;                     const int c0 = u.pn * BM + bj * HALF + wc * 32 + 8 * fq;
;                     f32x4 v0 = acc[ai][bj][m][0] * rs, v1 = acc[ai][bj][m][1] * rs;
;                     if (kind <= 1) {
;                         float s = (v0[0] * v0[0] + v0[1] * v0[1]) + (v0[2] * v0[2] + v0[3] * v0[3]) + (v1[0] * v1[0] + v1[1] * v1[1]) + (v1[2] * v1[2] + v1[3] * v1[3]);
;                         s += __shfl_xor(s, 16); s += __shfl_xor(s, 32);
;                         const int head = (u.pn & 3) * 2 + bj;
;                         if (fq == 0) ssq[(size_t)((kind * 8 + head) * 4 + wc) * MT + row] = s;
;                     } else if (kind <= 3) {
;                         const int i0 = (c0 & 127) >> 1;
;                         const f32x4 csa = *(const f32x4*)(cs + (size_t)pos * 64 + i0), csb = *(const f32x4*)(cs + (size_t)pos * 64 + i0 + 2);
;                         const float sc = (kind == 3) ? KSCALE : 1.0f;
;                         f32x4 w0, w1;
;                         w0[0] = (v0[0] * csa[0] - v0[1] * csa[1]) * sc; w0[1] = (v0[1] * csa[0] + v0[0] * csa[1]) * sc;
;                         w0[2] = (v0[2] * csa[2] - v0[3] * csa[3]) * sc; w0[3] = (v0[3] * csa[2] + v0[2] * csa[3]) * sc;
;                         w1[0] = (v1[0] * csb[0] - v1[1] * csb[1]) * sc; w1[1] = (v1[1] * csb[0] + v1[0] * csb[1]) * sc;
;                         w1[2] = (v1[2] * csb[2] - v1[3] * csb[3]) * sc; w1[3] = (v1[3] * csb[2] + v1[2] * csb[3]) * sc;
;                         v0 = w0; v1 = w1;
;                     } else {
; #pragma unroll
;                         for (int j = 0; j < 4; ++j) { v0[j] = v0[j] * __builtin_amdgcn_rcpf(1.0f + __builtin_amdgcn_exp2f(-1.4426950408889634f * v0[j]));
;                                                       v1[j] = v1[j] * __builtin_amdgcn_rcpf(1.0f + __builtin_amdgcn_exp2f(-1.4426950408889634f * v1[j])); }
;                     }
;                     u32x4 w; w.x = cvt_pk_bf16(v0[0], v0[1]); w.y = cvt_pk_bf16(v0[2], v0[3]); w.z = cvt_pk_bf16(v1[0], v1[1]); w.w = cvt_pk_bf16(v1[2], v1[3]);
.LBB0_366:
	v_cvt_pk_bf16_f32 v16, v26, v27
	v_cvt_pk_bf16_f32 v17, v28, v29
	v_cvt_pk_bf16_f32 v18, v30, v31
	v_cvt_pk_bf16_f32 v19, v32, v33
	global_store_dwordx4 v[248:249], v[16:19], off
	s_nop 1
	v_mov_b32_e32 v16, v232
	v_add_u32_e32 v27, 0xb0, v142
	v_lshlrev_b32_e32 v17, 6, v27
	s_and_b64 vcc, exec, s[40:41]
	v_and_b32_e32 v26, 0x1ffc0, v17
	s_mov_b64 s[0:1], -1
	v_pk_mul_f32 v[14:15], v[14:15], v[16:17] op_sel_hi:[1,0]
	v_pk_mul_f32 v[12:13], v[12:13], v[16:17] op_sel_hi:[1,0]
	v_pk_mul_f32 v[10:11], v[10:11], v[16:17] op_sel_hi:[1,0]
	v_pk_mul_f32 v[8:9], v[8:9], v[16:17] op_sel_hi:[1,0]
	s_cbranch_vccnz .LBB0_372
	s_and_b64 vcc, exec, s[38:39]
	s_cbranch_vccnz .LBB0_369
	v_mul_f32_e32 v17, 0xbfb8aa3b, v12
	v_exp_f32_e32 v17, v17
	v_mul_f32_e32 v18, 0xbfb8aa3b, v8
	v_mul_f32_e32 v19, 0xbfb8aa3b, v13
	v_exp_f32_e32 v20, v18
	v_exp_f32_e32 v19, v19
	v_add_f32_e32 v17, 1.0, v17
	v_rcp_f32_e32 v18, v17
	v_add_f32_e32 v17, 1.0, v20
	v_rcp_f32_e32 v22, v17
	v_add_f32_e32 v17, 1.0, v19
	v_mul_f32_e32 v21, 0xbfb8aa3b, v10
	v_rcp_f32_e32 v19, v17
	v_mul_f32_e32 v17, 0xbfb8aa3b, v9
	v_mul_f32_e32 v20, 0xbfb8aa3b, v14
	v_exp_f32_e32 v21, v21
	v_mul_f32_e32 v23, 0xbfb8aa3b, v15
	v_mul_f32_e32 v24, 0xbfb8aa3b, v11
	v_exp_f32_e32 v17, v17
	v_exp_f32_e32 v20, v20
	v_exp_f32_e32 v23, v23
	v_exp_f32_e32 v25, v24
	v_add_f32_e32 v21, 1.0, v21
	v_add_f32_e32 v17, 1.0, v17
	v_add_f32_e32 v20, 1.0, v20
	v_rcp_f32_e32 v24, v21
	v_add_f32_e32 v21, 1.0, v23
	v_add_f32_e32 v23, 1.0, v25
	v_rcp_f32_e32 v20, v20
	v_rcp_f32_e32 v21, v21
	v_rcp_f32_e32 v25, v23
	v_rcp_f32_e32 v23, v17
	v_pk_mul_f32 v[18:19], v[12:13], v[18:19]
	v_pk_mul_f32 v[20:21], v[14:15], v[20:21]
	v_pk_mul_f32 v[24:25], v[10:11], v[24:25]
	v_pk_mul_f32 v[22:23], v[8:9], v[22:23]
	s_mov_b64 s[0:1], 0

; __device__ __forceinline__ unsigned cvt_pk_bf16(float lo, float hi) { unsigned r; asm volatile("v_cvt_pk_bf16_f32 %0, %1, %2" : "=v"(r) : "v"(lo), "v"(hi)); return r; }
;     __device__ __forceinline__ void operator()(const f32x4 (&acc)[2][2][4][2], const Unit& u, int wr, int wc, int fr, int fq) const {
;     ...
;                     f32x4 v0 = acc[ai][bj][m][0] * rs, v1 = acc[ai][bj][m][1] * rs;
;                     if (kind <= 1) {
;                         float s = (v0[0] * v0[0] + v0[1] * v0[1]) + (v0[2] * v0[2] + v0[3] * v0[3]) + (v1[0] * v1[0] + v1[1] * v1[1]) + (v1[2] * v1[2] + v1[3] * v1[3]);
;                         s += __shfl_xor(s, 16); s += __shfl_xor(s, 32);
;                         const int head = (u.pn & 3) * 2 + bj;
;                         if (fq == 0) ssq[(size_t)((kind * 8 + head) * 4 + wc) * MT + row] = s;
;                     } else if (kind <= 3) {
;                         const int i0 = (c0 & 127) >> 1;
;                         const f32x4 csa = *(const f32x4*)(cs + (size_t)pos * 64 + i0), csb = *(const f32x4*)(cs + (size_t)pos * 64 + i0 + 2);
;                         const float sc = (kind == 3) ? KSCALE : 1.0f;
;                         f32x4 w0, w1;
;                         w0[0] = (v0[0] * csa[0] - v0[1] * csa[1]) * sc; w0[1] = (v0[1] * csa[0] + v0[0] * csa[1]) * sc;
;                         w0[2] = (v0[2] * csa[2] - v0[3] * csa[3]) * sc; w0[3] = (v0[3] * csa[2] + v0[2] * csa[3]) * sc;
;                         w1[0] = (v1[0] * csb[0] - v1[1] * csb[1]) * sc; w1[1] = (v1[1] * csb[0] + v1[0] * csb[1]) * sc;
;                         w1[2] = (v1[2] * csb[2] - v1[3] * csb[3]) * sc; w1[3] = (v1[3] * csb[2] + v1[2] * csb[3]) * sc;
;                         v0 = w0; v1 = w1;
;                     } else {
; #pragma unroll
;                         for (int j = 0; j < 4; ++j) { v0[j] = v0[j] * __builtin_amdgcn_rcpf(1.0f + __builtin_amdgcn_exp2f(-1.4426950408889634f * v0[j]));
;                                                       v1[j] = v1[j] * __builtin_amdgcn_rcpf(1.0f + __builtin_amdgcn_exp2f(-1.4426950408889634f * v1[j])); }
;                     }
;                     u32x4 w; w.x = cvt_pk_bf16(v0[0], v0[1]); w.y = cvt_pk_bf16(v0[2], v0[3]); w.z = cvt_pk_bf16(v1[0], v1[1]); w.w = cvt_pk_bf16(v1[2], v1[3]);
;                     *(u32x4*)(O + (size_t)row * TOKP + c0) = w;
.LBB0_376:
	v_mov_b64_e32 v[8:9], s[80:81]
	s_movk_i32 s0, 0x2900
	v_mad_i64_i32 v[8:9], s[0:1], v27, s0, v[8:9]
	v_cvt_pk_bf16_f32 v10, v18, v19
	v_cvt_pk_bf16_f32 v11, v20, v21
	v_lshl_add_u64 v[8:9], v[120:121], 1, v[8:9]
	v_mov_b32_e32 v17, v16
	v_cvt_pk_bf16_f32 v12, v22, v23
	v_cvt_pk_bf16_f32 v13, v24, v25
	v_and_b32_e32 v244, -16, v27
	v_lshlrev_b32_e32 v244, 12, v244
	v_mov_b32_e32 v245, 0
	v_lshl_add_u64 v[246:247], v[244:245], 0, v[238:239]
	v_cndmask_b32_e64 v246, v8, v246, s[100:101]
	v_cndmask_b32_e64 v247, v9, v247, s[100:101]
	v_lshl_add_u64 v[248:249], v[246:247], 0, v[242:243]
	global_store_dwordx4 v[246:247], v[10:13], off
	s_and_b64 vcc, exec, s[40:41]
	v_readlane_b32 s40, v250, 32
	v_mov_b32_e32 v10, v16
	v_mov_b32_e32 v11, v16
	v_pk_mul_f32 v[6:7], v[6:7], v[10:11]
	v_pk_mul_f32 v[4:5], v[4:5], v[16:17]
	v_pk_mul_f32 v[2:3], v[2:3], v[10:11]
	v_pk_mul_f32 v[0:1], v[0:1], v[16:17]
	s_mov_b64 s[0:1], -1
	v_readlane_b32 s41, v250, 33
	s_cbranch_vccnz .LBB0_382
	s_and_b64 vcc, exec, s[38:39]
	s_cbranch_vccnz .LBB0_379
	v_mul_f32_e32 v11, 0xbfb8aa3b, v0
	v_mul_f32_e32 v12, 0xbfb8aa3b, v5
	v_exp_f32_e32 v11, v11
	v_exp_f32_e32 v12, v12
	v_mul_f32_e32 v13, 0xbfb8aa3b, v6
	v_mul_f32_e32 v15, 0xbfb8aa3b, v2
	v_add_f32_e32 v11, 1.0, v11
	v_rcp_f32_e32 v14, v11
	v_add_f32_e32 v11, 1.0, v12
	v_mul_f32_e32 v12, 0xbfb8aa3b, v1
	v_exp_f32_e32 v12, v12
	v_exp_f32_e32 v13, v13
	v_exp_f32_e32 v15, v15
	v_mul_f32_e32 v10, 0xbfb8aa3b, v4
	v_add_f32_e32 v18, 1.0, v12
	v_add_f32_e32 v12, 1.0, v13
	v_add_f32_e32 v13, 1.0, v15
	v_mul_f32_e32 v15, 0xbfb8aa3b, v7
	v_mul_f32_e32 v16, 0xbfb8aa3b, v3
	v_exp_f32_e32 v10, v10
	v_exp_f32_e32 v15, v15
	v_exp_f32_e32 v17, v16
	v_rcp_f32_e32 v16, v13
	v_add_f32_e32 v10, 1.0, v10
	v_add_f32_e32 v13, 1.0, v15
	v_add_f32_e32 v15, 1.0, v17
	v_rcp_f32_e32 v10, v10
	v_rcp_f32_e32 v11, v11
	v_rcp_f32_e32 v12, v12
	v_rcp_f32_e32 v13, v13
	v_rcp_f32_e32 v17, v15
	v_rcp_f32_e32 v15, v18
	v_pk_mul_f32 v[10:11], v[4:5], v[10:11]
	v_pk_mul_f32 v[12:13], v[6:7], v[12:13]
	v_pk_mul_f32 v[16:17], v[2:3], v[16:17]
	v_pk_mul_f32 v[14:15], v[0:1], v[14:15]
	s_mov_b64 s[0:1], 0

; __device__ __forceinline__ unsigned cvt_pk_bf16(float lo, float hi) { unsigned r; asm volatile("v_cvt_pk_bf16_f32 %0, %1, %2" : "=v"(r) : "v"(lo), "v"(hi)); return r; }
;     __device__ __forceinline__ void operator()(const f32x4 (&acc)[2][2][4][2], const Unit& u, int wr, int wc, int fr, int fq) const {
;     ...
;                     u32x4 w; w.x = cvt_pk_bf16(v0[0], v0[1]); w.y = cvt_pk_bf16(v0[2], v0[3]); w.z = cvt_pk_bf16(v1[0], v1[1]); w.w = cvt_pk_bf16(v1[2], v1[3]);
;                     *(u32x4*)(O + (size_t)row * TOKP + c0) = w;
.LBB0_386:
	s_andn2_b64 vcc, exec, s[36:37]
	s_mov_b64 s[0:1], -1
	v_cvt_pk_bf16_f32 v0, v10, v11
	v_cvt_pk_bf16_f32 v1, v12, v13
	v_cvt_pk_bf16_f32 v2, v14, v15
	v_cvt_pk_bf16_f32 v3, v16, v17
	global_store_dwordx4 v[248:249], v[0:3], off
	s_cbranch_vccnz .LBB0_219
	s_andn2_b64 vcc, exec, s[42:43]
	s_cbranch_vccnz .LBB0_218
	s_barrier
	s_branch .LBB0_218

; #define LAS __attribute__((address_space(3)))
; __device__ __forceinline__ int lane_id() { return (int)__builtin_amdgcn_mbcnt_hi(~0u, __builtin_amdgcn_mbcnt_lo(~0u, 0u)); }
; __device__ __forceinline__ float fexp2(float x) { return __builtin_amdgcn_exp2f(x); }
; __device__ __forceinline__ void scan_task(const Frame& F, int task) {
;     int lane = lane_id(); asm volatile("" : "+v"(lane));
;     const int c = lane & 15, rq = lane >> 4;
;     const int eh = task & 1, db = (task >> 1) & 7, h = (task >> 4) & 7, b = task >> 7, bhh = b * NH + h;
;     const bf16* TOK = (const bf16*)(F.ws + WS_TOK); const bf16* SWP = (const bf16*)(F.ws + WS_SWP); bf16* ST = (bf16*)(F.ws + WS_ST);
;     const bf16* kg = TOK + (size_t)(b * S + (lane >> 1)) * TOKP + TK_KR + h * HD + db * 16 + (lane & 1) * 8;
;     const bf16* vrow = SWP + (size_t)(SW_VR + h * HD + eh * 64 + c) * SWPP + b * S + rq * 8;
;     bf16* sp = ST + ((size_t)bhh * NCH * HD + eh * 64 + c) * HD + db * 16 + rq * 4;
;     LAS unsigned char* kt = F.lds + RING_OFF + SC_OFF + F.wave * SC_WAVE_BYTES;
;     LAS unsigned char* kw = kt + (lane >> 1) * SC_PITCH + (lane & 1) * 16;
;     const LAS unsigned char* kr = kt + (rq * 8) * SC_PITCH + c * 2;
;     f32x4 st[4];
; #pragma unroll
;     for (int eb = 0; eb < 4; ++eb) st[eb] = (f32x4){0.f, 0.f, 0.f, 0.f};
;     const float lg = pg8::lg2gamma(h), cd = fexp2(64.f * lg);
;     float dec[16];
; #pragma unroll
;     for (int i = 0; i < 16; ++i) dec[i] = fexp2((float)(63 - ((i >> 3) * 32 + rq * 8 + (i & 7))) * lg);
;     ScanOps o0, o1, o2;
;     scan_load(o0, kg, vrow, 0); scan_load(o1, kg, vrow, 1);
.LBB0_504:
	s_lshr_b32 s0, s8, 4
	s_and_b32 s16, s0, 7
	s_lshl_b32 s0, s2, 1
	s_and_b32 s4, s0, 0xe0
	s_lshl_b32 s0, s16, 8
	v_mov_b32_e32 v184, s0
	s_ashr_i32 s0, s8, 7
	s_lshl_b32 s13, s0, 3
	s_lshl_b32 s0, s0, 11
	v_ashrrev_i32_e32 v6, 1, v0
	v_add_u32_e32 v92, s0, v6
	v_lshrrev_b32_e32 v242, 5, v0
	v_lshlrev_b32_e32 v242, 16, v242
	v_bfe_u32 v243, v0, 1, 4
	v_lshl_add_u32 v242, v243, 4, v242
	v_and_b32_e32 v243, 1, v0
	v_lshl_add_u32 v242, v243, 8, v242
	v_lshl_add_u32 v242, s0, 12, v242
	v_lshl_add_u32 v242, s16, 12, v242
	v_add_u32_e32 v242, 0x8000, v242
	v_mov_b32_e32 v243, s8
	v_bfe_u32 v244, v243, 2, 2
	v_lshl_add_u32 v242, v244, 10, v242
	v_bfe_u32 v244, v243, 1, 1
	v_lshl_add_u32 v242, v244, 9, v242
	v_mov_b32_e32 v243, 0
	v_mov_b64_e32 v[2:3], s[62:63]
	s_movk_i32 s7, 0x2900
	v_mad_i64_i32 v[2:3], s[14:15], v92, s7, v[2:3]
	s_lshl_b32 s14, s8, 6
	s_lshl_b32 s1, s9, 7
	s_and_b32 s14, s14, 64
	v_and_b32_e32 v136, 15, v0
	s_or_b32 s1, s14, s1
	s_lshl_b32 s12, s8, 3
	v_or_b32_e32 v4, s1, v136
	s_waitcnt lgkmcnt(0)
	v_ashrrev_i32_e32 v1, 4, v0
	s_and_b32 s12, s12, 0x70
	v_mul_u32_u24_e32 v4, 0x4080, v4
	v_lshlrev_b32_e32 v0, 4, v0
	s_movk_i32 s15, 0x120
	s_lshl_b32 s96, s9, 8
	v_lshlrev_b32_e32 v84, 1, v4
	v_mov_b32_e32 v85, v185
	s_ashr_i32 s1, s0, 31
	v_lshlrev_b32_e32 v86, 3, v1
	v_lshlrev_b32_e32 v138, 2, v1
	v_and_b32_e32 v80, 16, v0
	v_mul_lo_u32 v7, v1, s15
	v_lshl_add_u64 v[0:1], v[2:3], 0, s[96:97]
	s_lshl_b32 s96, s12, 1
	v_lshl_add_u64 v[4:5], s[62:63], 0, v[84:85]
	v_ashrrev_i32_e32 v87, 31, v86
	v_lshl_add_u64 v[0:1], v[0:1], 0, s[96:97]
	v_mov_b32_e32 v81, v185
	s_lshl_b64 s[0:1], s[0:1], 1
	v_lshl_add_u64 v[16:17], v[0:1], 0, v[80:81]
	v_lshl_add_u64 v[16:17], s[62:63], 0, v[242:243]
	v_lshl_add_u64 v[0:1], v[4:5], 0, s[0:1]
	v_lshlrev_b64 v[88:89], 1, v[86:87]
	v_lshl_add_u64 v[18:19], v[0:1], 0, v[88:89]
	v_sub_u32_e32 v1, 63, v86
	v_cvt_f32_i32_e32 v1, v1
	v_readlane_b32 s6, v253, 48
	s_mov_b64 s[18:19], 0x1e840000
	s_waitcnt vmcnt(0)
	v_lshl_add_u64 v[44:45], v[18:19], 0, s[18:19]
	v_mov_b32_e32 v0, s6
	v_mad_u64_u32 v[90:91], s[18:19], v6, 36, v[0:1]
	v_mul_f32_e32 v0, v82, v1
	v_sub_u32_e32 v1, 62, v86
	v_cvt_f32_i32_e32 v1, v1
	v_sub_u32_e32 v2, 61, v86
	v_cvt_f32_i32_e32 v2, v2
	v_exp_f32_e32 v140, v0
	v_mul_f32_e32 v0, v82, v1
	v_sub_u32_e32 v1, 60, v86
	v_cvt_f32_i32_e32 v1, v1
	v_exp_f32_e32 v142, v0
	v_mul_f32_e32 v0, v82, v2
	s_mov_b32 s15, 0xdfff800
	v_exp_f32_e32 v141, v0
	v_mul_f32_e32 v0, v82, v1
	v_add_co_u32_e32 v24, vcc, s15, v16
	v_exp_f32_e32 v143, v0
	v_sub_u32_e32 v0, 58, v86
	v_addc_co_u32_e32 v25, vcc, 0, v17, vcc
	s_mov_b32 s15, 0xe01f800
	v_cvt_f32_i32_e32 v91, v0
	v_add_co_u32_e32 v0, vcc, s15, v16
	s_mov_b32 s15, 0x1e840000
	s_nop 0
	v_addc_co_u32_e32 v1, vcc, 0, v17, vcc
	v_add_co_u32_e32 v4, vcc, s15, v18
	s_mov_b32 s15, 0x1e8c1000
	s_nop 0
	v_addc_co_u32_e32 v5, vcc, 0, v19, vcc
	v_add_co_u32_e32 v60, vcc, s15, v18
	s_mov_b32 s15, 0x1e942000
	s_nop 0
	v_addc_co_u32_e32 v61, vcc, 0, v19, vcc
	v_add_co_u32_e32 v68, vcc, s15, v18
	s_mov_b32 s15, 0x1e9c3000
	s_nop 0
	v_addc_co_u32_e32 v69, vcc, 0, v19, vcc
	v_add_co_u32_e32 v76, vcc, s15, v18
	v_sub_u32_e32 v2, 59, v86
	s_nop 0
	v_addc_co_u32_e32 v77, vcc, 0, v19, vcc
	s_mov_b32 s15, 0xe03f800
	v_cvt_f32_i32_e32 v2, v2
	v_add_co_u32_e32 v18, vcc, s15, v16
	s_mov_b32 s15, 0xe05f800
	s_nop 0
	v_addc_co_u32_e32 v19, vcc, 0, v17, vcc
	v_add_co_u32_e32 v20, vcc, s15, v16
	v_add_u32_e32 v81, s6, v7
	s_nop 0
	v_addc_co_u32_e32 v21, vcc, 0, v17, vcc
	v_mul_f32_e32 v87, v82, v2
	global_load_dwordx4 v[0:3], v[0:1], off offset:2048
	s_nop 0
	global_load_dwordx4 v[4:7], v[4:5], off
	s_nop 0
	global_load_dwordx4 v[8:11], v[60:61], off
	s_waitcnt lgkmcnt(0)
; __device__ __forceinline__ float fexp2(float x) { return __builtin_amdgcn_exp2f(x); }
; __device__ __forceinline__ void scan_load(ScanOps& o, const bf16* kg, const bf16* vrow, int n) {
; #pragma unroll
;     for (int i = 0; i < 2; ++i) o.kp[i] = ld_u4(kg + (size_t)(n * CH + i * 32) * TOKP);
; #pragma unroll
;     for (int eb = 0; eb < 4; ++eb)
; #pragma unroll
;         for (int ks = 0; ks < 2; ++ks) o.va[eb][ks] = ld_b8(vrow + (size_t)eb * 16 * SWPP + n * CH + ks * 32);
; }
; __device__ __forceinline__ void scan_task(const Frame& F, int task) {
;     ...
;     const float lg = pg8::lg2gamma(h), cd = fexp2(64.f * lg);
;     float dec[16];
; #pragma unroll
;     for (int i = 0; i < 16; ++i) dec[i] = fexp2((float)(63 - ((i >> 3) * 32 + rq * 8 + (i & 7))) * lg);
;     ScanOps o0, o1, o2;
;     scan_load(o0, kg, vrow, 0); scan_load(o1, kg, vrow, 1);
	global_load_dwordx4 v[12:15], v[60:61], off offset:64
	global_load_dwordx4 v[28:31], v[68:69], off
	global_load_dwordx4 v[32:35], v[68:69], off offset:64
	global_load_dwordx4 v[48:51], v[76:77], off
	global_load_dwordx4 v[52:55], v[76:77], off offset:64
	s_nop 0
	global_load_dwordx4 v[16:19], v[18:19], off offset:2048
	s_nop 0
	global_load_dwordx4 v[20:23], v[20:21], off offset:2048
	s_nop 0
	global_load_dwordx4 v[40:43], v[44:45], off offset:64
	global_load_dwordx4 v[36:39], v[44:45], off offset:128
	s_nop 0
	global_load_dwordx4 v[24:27], v[24:25], off offset:2048
	s_nop 0
	global_load_dwordx4 v[44:47], v[44:45], off offset:192
	s_nop 0
	global_load_dwordx4 v[56:59], v[60:61], off offset:128
	s_nop 0
	global_load_dwordx4 v[60:63], v[60:61], off offset:192
	s_nop 0
	global_load_dwordx4 v[64:67], v[68:69], off offset:128
	s_nop 0
	global_load_dwordx4 v[68:71], v[68:69], off offset:192
	s_nop 0
	global_load_dwordx4 v[72:75], v[76:77], off offset:128
	s_nop 0
	global_load_dwordx4 v[76:79], v[76:77], off offset:192
	v_exp_f32_e32 v144, v87
	v_mul_f32_e32 v87, v82, v91
	v_sub_u32_e32 v91, 57, v86
	v_cvt_f32_i32_e32 v91, v91
	v_sub_u32_e32 v94, 56, v86
	v_cvt_f32_i32_e32 v94, v94
	v_exp_f32_e32 v146, v87
	v_mul_f32_e32 v87, v82, v91
	v_sub_u32_e32 v91, 31, v86
	v_cvt_f32_i32_e32 v91, v91
	v_exp_f32_e32 v145, v87
	v_mul_f32_e32 v87, v82, v94
	v_sub_u32_e32 v94, 30, v86
	v_cvt_f32_i32_e32 v94, v94
	v_exp_f32_e32 v147, v87
	v_mul_f32_e32 v87, v82, v91
	v_sub_u32_e32 v91, 29, v86
	v_cvt_f32_i32_e32 v91, v91
	v_exp_f32_e32 v148, v87
	v_mul_f32_e32 v87, v82, v94
	v_sub_u32_e32 v94, 28, v86
	v_cvt_f32_i32_e32 v94, v94
	v_exp_f32_e32 v150, v87
	v_mul_f32_e32 v87, v82, v91
	v_sub_u32_e32 v91, 27, v86
	v_cvt_f32_i32_e32 v91, v91
	v_exp_f32_e32 v149, v87
	v_mul_f32_e32 v87, v82, v94
	v_sub_u32_e32 v94, 26, v86
	v_cvt_f32_i32_e32 v94, v94
	v_exp_f32_e32 v151, v87
	v_mul_f32_e32 v87, v82, v91
	v_sub_u32_e32 v91, 25, v86
	v_sub_u32_e32 v86, 24, v86
	v_cvt_f32_i32_e32 v91, v91
	v_cvt_f32_i32_e32 v86, v86
	v_exp_f32_e32 v152, v87
	v_mul_f32_e32 v87, v82, v94
	v_mul_f32_e32 v83, 0x42800000, v82
	v_exp_f32_e32 v154, v87
	v_mul_f32_e32 v87, v82, v91
	v_mul_f32_e32 v82, v82, v86
	v_exp_f32_e32 v156, v83
	v_exp_f32_e32 v155, v82
	v_lshl_add_u64 v[82:83], s[0:1], 0, v[88:89]
	s_or_b32 s0, s13, s16
	s_ashr_i32 s1, s0, 31
	s_and_b32 s5, s3, 64
	s_lshl_b64 s[0:1], s[0:1], 12
	s_or_b32 s0, s0, s5
	v_exp_f32_e32 v153, v87
	v_lshl_add_u64 v[160:161], v[82:83], 0, v[84:85]
	v_mov_b32_e32 v82, s0
	v_mov_b32_e32 v83, s1
	v_lshlrev_b64 v[82:83], 8, v[82:83]
	v_ashrrev_i32_e32 v139, 31, v138
	v_lshlrev_b32_e32 v93, 1, v136
	v_lshl_or_b32 v82, s4, 4, v82
	v_mad_i64_i32 v[164:165], s[0:1], v92, s7, v[184:185]
	v_mov_b32_e32 v88, 0
	s_mov_b32 s15, 0
	v_mov_b32_e32 v158, v156
	v_mov_b32_e32 v159, v156
	v_and_b32_e32 v240, 8, v138
	v_and_b32_e32 v241, 4, v138
	v_lshlrev_b32_e32 v240, 5, v240
	v_lshl_or_b32 v240, v241, 1, v240
	v_lshl_or_b32 v240, v136, 4, v240
	v_mov_b32_e32 v241, 0
	v_lshl_add_u64 v[162:163], v[82:83], 0, v[240:241]
	v_or3_b32 v164, v164, s4, v80
	v_mov_b32_e32 v164, v242
	v_mov_b32_e32 v165, 0
	v_add_u32_e32 v137, v90, v80
	v_add_u32_e32 v168, v81, v93
	v_mov_b32_e32 v89, v88
	v_mov_b32_e32 v90, v88
	v_mov_b32_e32 v91, v88
	v_mov_b32_e32 v92, v88
	v_mov_b32_e32 v93, v88
	v_mov_b32_e32 v94, v88
	v_mov_b32_e32 v95, v88
	v_mov_b32_e32 v84, v88
	v_mov_b32_e32 v85, v88
	v_mov_b32_e32 v86, v88
	v_mov_b32_e32 v87, v88
	v_mov_b32_e32 v80, v88
	v_mov_b32_e32 v81, v88
	v_mov_b32_e32 v82, v88
	v_mov_b32_e32 v83, v88
	s_branch .LBB0_507

; #define LAS __attribute__((address_space(3)))
; #define LDS_WAIT() asm volatile("s_waitcnt lgkmcnt(0)" ::: "memory")
; __device__ __forceinline__ unsigned pk2(float lo, float hi) { return f2bf(lo) | (f2bf(hi) << 16); }
; __device__ __forceinline__ void scan_load(ScanOps& o, const bf16* kg, const bf16* vrow, int n) {
; #pragma unroll
;     for (int i = 0; i < 2; ++i) o.kp[i] = ld_u4(kg + (size_t)(n * CH + i * 32) * TOKP);
; #pragma unroll
;     for (int eb = 0; eb < 4; ++eb)
; #pragma unroll
;         for (int ks = 0; ks < 2; ++ks) o.va[eb][ks] = ld_b8(vrow + (size_t)eb * 16 * SWPP + n * CH + ks * 32);
; }
; __device__ __forceinline__ void scan_step(f32x4 (&st)[4], const ScanOps& o, const float (&dec)[16], LAS unsigned char* kw, const LAS unsigned char* kr, bf16* sp, int n, float cd) {
; #pragma unroll
;     for (int eb = 0; eb < 4; ++eb) { u32x2 w; w.x = pk2(st[eb][0], st[eb][1]); w.y = pk2(st[eb][2], st[eb][3]); st_u2(sp + (size_t)n * HD * HD + eb * 16 * HD, w); }
; #pragma unroll
;     for (int i = 0; i < 2; ++i)
; #pragma unroll
;         for (int d = 0; d < 4; ++d) *(LAS unsigned*)(kw + i * 32 * SC_PITCH + d * 4) = o.kp[i][d];
;     LDS_WAIT(); asm volatile("" ::: "memory");
;     bf16x8 ka[2];
; #pragma unroll
;     for (int ks = 0; ks < 2; ++ks) { u32x4 w;
; #pragma unroll
;         for (int j = 0; j < 4; ++j) { const unsigned e0 = *(const LAS unsigned short*)(kr + (ks * 32 + 2 * j) * SC_PITCH), e1 = *(const LAS unsigned short*)(kr + (ks * 32 + 2 * j + 1) * SC_PITCH);
;             w[j] = pk2(bf_lo(e0) * dec[ks * 8 + 2 * j], bf_lo(e1) * dec[ks * 8 + 2 * j + 1]); }
.LBB0_506:
	s_mov_b64 s[0:1], 0x180
	v_lshl_add_u64 v[160:161], v[160:161], 0, s[0:1]
	s_mov_b64 s[0:1], 0x18000
	s_add_i32 s4, s15, 3
	v_lshl_add_u64 v[162:163], v[162:163], 0, s[0:1]
	s_mov_b64 s[0:1], 0xc0000
	v_lshl_add_u64 v[164:165], v[164:165], 0, s[0:1]
	s_cmp_lt_u32 s15, 28
	s_mov_b32 s15, s4
	s_cbranch_scc0 .LBB0_482
.LBB0_507:
	s_cmp_lt_u32 s15, 29
	s_cselect_b64 s[0:1], -1, 0
	s_cmp_gt_u32 s15, 28
	s_cbranch_scc1 .LBB0_509
	v_lshl_add_u64 v[96:97], s[62:63], 0, v[164:165]
	v_add_co_u32_e32 v98, vcc, 0xe07f800, v96
	s_waitcnt vmcnt(5)
	v_lshl_add_u64 v[128:129], s[62:63], 0, v[160:161]
	v_addc_co_u32_e32 v99, vcc, 0, v97, vcc
	v_add_co_u32_e32 v100, vcc, 0xe09f800, v96
	s_nop 1
	v_addc_co_u32_e32 v101, vcc, 0, v97, vcc
	v_add_co_u32_e32 v108, vcc, 0x1e840000, v128
	global_load_dwordx4 v[96:99], v[98:99], off offset:2048
	s_nop 0
	global_load_dwordx4 v[100:103], v[100:101], off offset:2048
	v_addc_co_u32_e32 v109, vcc, 0, v129, vcc
	v_add_co_u32_e32 v116, vcc, 0x1e8c1000, v128
	global_load_dwordx4 v[104:107], v[108:109], off offset:256
	s_nop 0
	global_load_dwordx4 v[108:111], v[108:109], off offset:320
	v_addc_co_u32_e32 v117, vcc, 0, v129, vcc
	v_add_co_u32_e32 v124, vcc, 0x1e942000, v128
	global_load_dwordx4 v[112:115], v[116:117], off offset:256
	s_nop 0
	global_load_dwordx4 v[116:119], v[116:117], off offset:320
	v_addc_co_u32_e32 v125, vcc, 0, v129, vcc
	s_waitcnt vmcnt(10)
	v_add_co_u32_e32 v132, vcc, 0x1e9c3000, v128
	global_load_dwordx4 v[120:123], v[124:125], off offset:256
	s_nop 0
	global_load_dwordx4 v[124:127], v[124:125], off offset:320
	v_addc_co_u32_e32 v133, vcc, 0, v129, vcc
	global_load_dwordx4 v[128:131], v[132:133], off offset:256
	s_nop 0
	global_load_dwordx4 v[132:135], v[132:133], off offset:320
.LBB0_509:
	s_nop 4
	v_cvt_pk_bf16_f32 v170, v88, v89
	s_nop 4
	v_lshl_add_u64 v[166:167], s[62:63], 0, v[162:163]
	v_cvt_pk_bf16_f32 v171, v90, v91
	s_mov_b32 s4, 0x22c01000
	s_nop 0
	v_add_co_u32_e32 v172, vcc, s4, v166
	s_nop 1
	v_addc_co_u32_e32 v173, vcc, 0, v167, vcc
	s_nop 1
	global_store_dwordx2 v[172:173], v[170:171], off offset:-4096
	v_cvt_pk_bf16_f32 v170, v92, v93
	s_nop 4
	v_cvt_pk_bf16_f32 v171, v94, v95
	s_nop 4
	global_store_dwordx2 v[172:173], v[170:171], off
	v_cvt_pk_bf16_f32 v170, v84, v85
	s_nop 4
	v_cvt_pk_bf16_f32 v171, v86, v87
	s_mov_b32 s4, 0x22c03000
	s_nop 0
	v_add_co_u32_e32 v172, vcc, s4, v166
	s_nop 1
	v_addc_co_u32_e32 v173, vcc, 0, v167, vcc
	s_nop 1
	global_store_dwordx2 v[172:173], v[170:171], off offset:-4096
	v_cvt_pk_bf16_f32 v170, v80, v81
	s_nop 4
	v_cvt_pk_bf16_f32 v171, v82, v83
	global_store_dwordx2 v[172:173], v[170:171], off
	v_add_u32_e32 v169, 0x480, v137
	v_add_u32_e32 v170, 0x488, v137
	s_waitcnt vmcnt(11)
	ds_write2_b32 v137, v24, v25 offset1:1
	ds_write2_b32 v137, v26, v27 offset0:2 offset1:3
	ds_write2_b32 v169, v0, v1 offset1:1
	ds_write2_b32 v170, v2, v3 offset1:1
	s_waitcnt lgkmcnt(0)
	ds_read_u16 v157, v168 offset:72
	ds_read_u16 v171, v168 offset:108
	ds_read_u16 v172, v168
	ds_read_u16 v176, v168 offset:144
	ds_read_u16 v177, v168 offset:216
	ds_read_u16 v178, v168 offset:252
	ds_read_u16 v179, v168 offset:180
	ds_read_u16 v174, v168 offset:36
	s_waitcnt lgkmcnt(7)
	v_lshlrev_b32_e32 v173, 16, v157
	s_waitcnt lgkmcnt(5)
	v_lshlrev_b32_e32 v172, 16, v172
	v_pk_mul_f32 v[172:173], v[140:141], v[172:173]
	v_lshlrev_b32_e32 v175, 16, v171
	v_and_b32_sdwa v157, v173, v213 dst_sel:DWORD dst_unused:UNUSED_PAD src0_sel:WORD_1 src1_sel:DWORD
	v_and_b32_sdwa v171, v172, v213 dst_sel:DWORD dst_unused:UNUSED_PAD src0_sel:WORD_1 src1_sel:DWORD
	v_add3_u32 v157, v173, v157, s76
	v_add3_u32 v171, v172, v171, s76
	s_waitcnt lgkmcnt(3)
	v_lshlrev_b32_e32 v173, 16, v177
	v_lshlrev_b32_e32 v172, 16, v176
	s_waitcnt lgkmcnt(0)
	v_lshlrev_b32_e32 v174, 16, v174
	v_pk_mul_f32 v[172:173], v[144:145], v[172:173]
	v_lshlrev_b32_e32 v177, 16, v178
	v_lshlrev_b32_e32 v176, 16, v179
	v_pk_mul_f32 v[174:175], v[142:143], v[174:175]
	v_pk_mul_f32 v[176:177], v[146:147], v[176:177]
	v_and_b32_sdwa v178, v173, v213 dst_sel:DWORD dst_unused:UNUSED_PAD src0_sel:WORD_1 src1_sel:DWORD
	v_and_b32_sdwa v179, v172, v213 dst_sel:DWORD dst_unused:UNUSED_PAD src0_sel:WORD_1 src1_sel:DWORD
	v_add3_u32 v182, v173, v178, s76
	v_add3_u32 v172, v172, v179, s76
	v_bfe_u32 v173, v176, 16, 1
	v_bfe_u32 v178, v175, 16, 1
	v_bfe_u32 v179, v174, 16, 1
	v_bfe_u32 v180, v177, 16, 1
	v_lshrrev_b32_e32 v171, 16, v171
	v_lshrrev_b32_e32 v157, 16, v157
	v_lshrrev_b32_e32 v172, 16, v172
	v_add3_u32 v183, v177, v180, s76
	v_add3_u32 v177, v174, v179, s76
	v_add3_u32 v175, v175, v178, s76
	v_add3_u32 v173, v176, v173, s76
	v_and_or_b32 v174, v173, s75, v172
	v_and_or_b32 v173, v175, s75, v157
	v_and_or_b32 v172, v177, s75, v171
	ds_read_u16 v157, v168 offset:1152
	ds_read_u16 v171, v168 offset:1224
	ds_read_u16 v175, v168 offset:1260
	ds_read_u16 v180, v168 offset:1296
	ds_read_u16 v181, v168 offset:1368
	ds_read_u16 v184, v168 offset:1404
	ds_read_u16 v194, v168 offset:1332
	ds_read_u16 v178, v168 offset:1188
	s_waitcnt lgkmcnt(6)
; #define LAS __attribute__((address_space(3)))
; #define LDS_WAIT() asm volatile("s_waitcnt lgkmcnt(0)" ::: "memory")
; __device__ __forceinline__ unsigned pk2(float lo, float hi) { return f2bf(lo) | (f2bf(hi) << 16); }
; __device__ __forceinline__ f32x4 mfma16(bf16x8 a, bf16x8 b, f32x4 c) { return __builtin_amdgcn_mfma_f32_16x16x32_bf16(a, b, c, 0, 0, 0); }
; __device__ __forceinline__ void scan_step(f32x4 (&st)[4], const ScanOps& o, const float (&dec)[16], LAS unsigned char* kw, const LAS unsigned char* kr, bf16* sp, int n, float cd) {
;     ...
;     for (int ks = 0; ks < 2; ++ks) { u32x4 w;
; #pragma unroll
;         for (int j = 0; j < 4; ++j) { const unsigned e0 = *(const LAS unsigned short*)(kr + (ks * 32 + 2 * j) * SC_PITCH), e1 = *(const LAS unsigned short*)(kr + (ks * 32 + 2 * j + 1) * SC_PITCH);
;             w[j] = pk2(bf_lo(e0) * dec[ks * 8 + 2 * j], bf_lo(e1) * dec[ks * 8 + 2 * j + 1]); }
;         ka[ks] = __builtin_bit_cast(bf16x8, w); }
;     LDS_WAIT(); asm volatile("" ::: "memory");
; #pragma unroll
;     for (int eb = 0; eb < 4; ++eb) { st[eb] *= cd;
; #pragma unroll
;         for (int ks = 0; ks < 2; ++ks) st[eb] = mfma16(ka[ks], o.va[eb][ks], st[eb]); }
; __device__ __forceinline__ void scan_task(const Frame& F, int task) {
;     ...
;     for (int n = 0; n < NCH - 1; n += 3) {
;         if (n + 2 < NCH - 1) scan_load(o2, kg, vrow, n + 2);
;         scan_step(st, o0, dec, kw, kr, sp, n, cd);
;         if (n + 1 < NCH - 1) { if (n + 3 < NCH - 1) scan_load(o0, kg, vrow, n + 3); scan_step(st, o1, dec, kw, kr, sp, n + 1, cd); }
;         if (n + 2 < NCH - 1) { if (n + 4 < NCH - 1) scan_load(o1, kg, vrow, n + 4); scan_step(st, o2, dec, kw, kr, sp, n + 2, cd); }
	v_lshlrev_b32_e32 v177, 16, v171
	v_lshlrev_b32_e32 v176, 16, v157
	v_pk_mul_f32 v[176:177], v[148:149], v[176:177]
	s_waitcnt lgkmcnt(5)
	v_lshlrev_b32_e32 v179, 16, v175
	v_and_b32_sdwa v157, v177, v213 dst_sel:DWORD dst_unused:UNUSED_PAD src0_sel:WORD_1 src1_sel:DWORD
	v_and_b32_sdwa v171, v176, v213 dst_sel:DWORD dst_unused:UNUSED_PAD src0_sel:WORD_1 src1_sel:DWORD
	v_add3_u32 v157, v177, v157, s76
	v_add3_u32 v171, v176, v171, s76
	s_waitcnt lgkmcnt(3)
	v_lshlrev_b32_e32 v177, 16, v181
	v_lshlrev_b32_e32 v176, 16, v180
	v_pk_mul_f32 v[176:177], v[152:153], v[176:177]
	s_waitcnt lgkmcnt(2)
	v_lshlrev_b32_e32 v181, 16, v184
	s_waitcnt lgkmcnt(1)
	v_lshlrev_b32_e32 v180, 16, v194
	s_waitcnt lgkmcnt(0)
	v_lshlrev_b32_e32 v178, 16, v178
	v_pk_mul_f32 v[180:181], v[154:155], v[180:181]
	v_and_b32_sdwa v175, v177, v213 dst_sel:DWORD dst_unused:UNUSED_PAD src0_sel:WORD_1 src1_sel:DWORD
	v_and_b32_sdwa v184, v176, v213 dst_sel:DWORD dst_unused:UNUSED_PAD src0_sel:WORD_1 src1_sel:DWORD
	v_pk_mul_f32 v[178:179], v[150:151], v[178:179]
	v_add3_u32 v194, v177, v175, s76
	v_add3_u32 v175, v176, v184, s76
	v_bfe_u32 v176, v180, 16, 1
	v_lshrrev_b32_e32 v175, 16, v175
	v_bfe_u32 v184, v178, 16, 1
	v_add3_u32 v176, v180, v176, s76
	v_add3_u32 v184, v178, v184, s76
	v_and_or_b32 v178, v176, s75, v175
	v_perm_b32 v175, v183, v182, s71
	v_bfe_u32 v177, v179, 16, 1
	v_lshrrev_b32_e32 v157, 16, v157
	v_bfe_u32 v195, v181, 16, 1
	v_add3_u32 v177, v179, v177, s76
	v_lshrrev_b32_e32 v171, 16, v171
	v_add3_u32 v181, v181, v195, s76
	v_and_or_b32 v177, v177, s75, v157
	v_mov_b32_e32 v157, v156
	v_and_or_b32 v176, v184, s75, v171
	v_pk_mul_f32 v[90:91], v[156:157], v[90:91]
	v_pk_mul_f32 v[88:89], v[158:159], v[88:89]
	v_perm_b32 v179, v181, v194, s71
	v_pk_mul_f32 v[94:95], v[156:157], v[94:95]
	v_pk_mul_f32 v[92:93], v[158:159], v[92:93]
	v_pk_mul_f32 v[86:87], v[156:157], v[86:87]
	v_pk_mul_f32 v[84:85], v[158:159], v[84:85]
	v_pk_mul_f32 v[82:83], v[156:157], v[82:83]
	v_pk_mul_f32 v[80:81], v[158:159], v[80:81]
	v_mfma_f32_16x16x32_bf16 v[88:91], v[172:175], v[4:7], v[88:91]
	s_waitcnt lgkmcnt(0)
	s_cmp_eq_u32 s15, 30
	v_mfma_f32_16x16x32_bf16 v[92:95], v[172:175], v[8:11], v[92:95]
	v_mfma_f32_16x16x32_bf16 v[84:87], v[172:175], v[28:31], v[84:87]
	s_waitcnt vmcnt(9)
	v_mfma_f32_16x16x32_bf16 v[80:83], v[172:175], v[48:51], v[80:83]
	v_mfma_f32_16x16x32_bf16 v[88:91], v[176:179], v[40:43], v[88:91]
	v_mfma_f32_16x16x32_bf16 v[92:95], v[176:179], v[12:15], v[92:95]
	v_mfma_f32_16x16x32_bf16 v[84:87], v[176:179], v[32:35], v[84:87]
	s_waitcnt vmcnt(8)
	v_mfma_f32_16x16x32_bf16 v[80:83], v[176:179], v[52:55], v[80:83]
	s_cbranch_scc1 .LBB0_513
	s_cmp_gt_u32 s15, 27
	s_cbranch_scc1 .LBB0_512
	v_lshl_add_u64 v[0:1], s[62:63], 0, v[164:165]
	v_add_co_u32_e32 v2, vcc, 0xe0bf800, v0
	v_lshl_add_u64 v[48:49], s[62:63], 0, v[160:161]
	s_nop 0
	v_addc_co_u32_e32 v3, vcc, 0, v1, vcc
	v_add_co_u32_e32 v0, vcc, 0xe0df800, v0
	s_nop 1
	v_addc_co_u32_e32 v1, vcc, 0, v1, vcc
	v_add_co_u32_e32 v8, vcc, 0x1e840000, v48
	global_load_dwordx4 v[24:27], v[2:3], off offset:2048
	s_nop 0
	global_load_dwordx4 v[0:3], v[0:1], off offset:2048
	v_addc_co_u32_e32 v9, vcc, 0, v49, vcc
	v_add_co_u32_e32 v12, vcc, 0x1e8c1000, v48
	global_load_dwordx4 v[4:7], v[8:9], off offset:384
	global_load_dwordx4 v[40:43], v[8:9], off offset:448
	v_addc_co_u32_e32 v13, vcc, 0, v49, vcc
	v_add_co_u32_e32 v32, vcc, 0x1e942000, v48
	global_load_dwordx4 v[8:11], v[12:13], off offset:384
	s_nop 0
	global_load_dwordx4 v[12:15], v[12:13], off offset:448
	v_addc_co_u32_e32 v33, vcc, 0, v49, vcc
	v_add_co_u32_e32 v52, vcc, 0x1e9c3000, v48
	global_load_dwordx4 v[28:31], v[32:33], off offset:384
	s_nop 0
	global_load_dwordx4 v[32:35], v[32:33], off offset:448
	v_addc_co_u32_e32 v53, vcc, 0, v49, vcc
	global_load_dwordx4 v[48:51], v[52:53], off offset:384
	s_nop 0
	global_load_dwordx4 v[52:55], v[52:53], off offset:448

; __device__ __forceinline__ void scan_load(ScanOps& o, const bf16* kg, const bf16* vrow, int n) {
; #pragma unroll
;     for (int i = 0; i < 2; ++i) o.kp[i] = ld_u4(kg + (size_t)(n * CH + i * 32) * TOKP);
; #pragma unroll
;     for (int eb = 0; eb < 4; ++eb)
; #pragma unroll
;         for (int ks = 0; ks < 2; ++ks) o.va[eb][ks] = ld_b8(vrow + (size_t)eb * 16 * SWPP + n * CH + ks * 32);
; }
; __device__ __forceinline__ void scan_task(const Frame& F, int task) {
;     ...
;     for (int n = 0; n < NCH - 1; n += 3) {
;         if (n + 2 < NCH - 1) scan_load(o2, kg, vrow, n + 2);
;         scan_step(st, o0, dec, kw, kr, sp, n, cd);
;         if (n + 1 < NCH - 1) { if (n + 3 < NCH - 1) scan_load(o0, kg, vrow, n + 3); scan_step(st, o1, dec, kw, kr, sp, n + 1, cd); }
;         if (n + 2 < NCH - 1) { if (n + 4 < NCH - 1) scan_load(o1, kg, vrow, n + 4); scan_step(st, o2, dec, kw, kr, sp, n + 2, cd); }
.LBB0_513:
	s_andn2_b64 vcc, exec, s[0:1]
	s_cbranch_vccnz .LBB0_506
	s_cmp_gt_u32 s15, 26
	s_cbranch_scc1 .LBB0_505
	v_lshl_add_u64 v[16:17], s[62:63], 0, v[164:165]
	v_add_co_u32_e32 v18, vcc, 0xe0ff800, v16
	s_waitcnt vmcnt(5)
	v_lshl_add_u64 v[72:73], s[62:63], 0, v[160:161]
	v_addc_co_u32_e32 v19, vcc, 0, v17, vcc
	v_add_co_u32_e32 v20, vcc, 0xe11f800, v16
	s_nop 1
	v_addc_co_u32_e32 v21, vcc, 0, v17, vcc
	v_add_co_u32_e32 v44, vcc, 0x1e840000, v72
	global_load_dwordx4 v[16:19], v[18:19], off offset:2048
	s_nop 0
	global_load_dwordx4 v[20:23], v[20:21], off offset:2048
	v_addc_co_u32_e32 v45, vcc, 0, v73, vcc
	v_add_co_u32_e32 v60, vcc, 0x1e8c1000, v72
	global_load_dwordx4 v[36:39], v[44:45], off offset:512
	s_nop 0
	global_load_dwordx4 v[44:47], v[44:45], off offset:576
	v_addc_co_u32_e32 v61, vcc, 0, v73, vcc
	v_add_co_u32_e32 v68, vcc, 0x1e942000, v72
	global_load_dwordx4 v[56:59], v[60:61], off offset:512
	s_nop 0
	global_load_dwordx4 v[60:63], v[60:61], off offset:576
	v_addc_co_u32_e32 v69, vcc, 0, v73, vcc
	s_waitcnt vmcnt(10)
	v_add_co_u32_e32 v76, vcc, 0x1e9c3000, v72
	global_load_dwordx4 v[64:67], v[68:69], off offset:512
	s_nop 0
	global_load_dwordx4 v[68:71], v[68:69], off offset:576
	v_addc_co_u32_e32 v77, vcc, 0, v73, vcc
	global_load_dwordx4 v[72:75], v[76:77], off offset:512
	s_nop 0
	global_load_dwordx4 v[76:79], v[76:77], off offset:576
	s_branch .LBB0_505

; __device__ __forceinline__ f32x4 mfma16(bf16x8 a, bf16x8 b, f32x4 c) { return __builtin_amdgcn_mfma_f32_16x16x32_bf16(a, b, c, 0, 0, 0); }
; __device__ __forceinline__ void ret_task(const Frame& F, int l, int task) {
;     ...
;     bf16x8 Qf[2][4], Kf[2][2][4];
; #pragma unroll
;     for (int qb = 0; qb < 2; ++qb)
; #pragma unroll
;         for (int ks = 0; ks < 4; ++ks) Qf[qb][ks] = ld_b8(TOK + (size_t)(tq0 + qb * 16 + c) * TOKP + TK_QR + h * HD + ks * 32 + rq * 8);
; #pragma unroll
;     for (int g = 0; g < 2; ++g)
; #pragma unroll
;         for (int ab = 0; ab < 2; ++ab) { const int key = 32 * g + (c >> 2) * 8 + 4 * ab + (c & 3);
; #pragma unroll
;             for (int ks = 0; ks < 4; ++ks) Kf[g][ab][ks] = ld_b8(TOK + (size_t)(tc0 + key) * TOKP + TK_KR + h * HD + rq * 8 + ks * 32); }
;     f32x4 acc[2][8];
; #pragma unroll
;     for (int qb = 0; qb < 2; ++qb)
; #pragma unroll
;         for (int eb = 0; eb < 8; ++eb) acc[qb][eb] = (f32x4){0.f, 0.f, 0.f, 0.f};
;     const bf16* sp = ST + (((size_t)bhh * NCH + n) * HD + c) * HD + rq * 8;
; #pragma unroll
;     for (int eb = 0; eb < 8; ++eb)
; #pragma unroll
;         for (int ks = 0; ks < 4; ++ks) { const bf16x8 sf = ld_b8(sp + eb * 16 * HD + ks * 32);
; #pragma unroll
;             for (int qb = 0; qb < 2; ++qb) acc[qb][eb] = mfma16(sf, Qf[qb][ks], acc[qb][eb]); }
.LBB0_655:
	s_bfe_u32 s1, s8, 0x50001
	s_ashr_i32 s0, s8, 9
	s_lshl_b32 s4, s0, 3
	s_lshl_b32 s0, s0, 11
	s_lshl_b32 s5, s1, 6
	v_and_b32_e32 v180, 15, v118
	s_or_b32 s0, s5, s0
	v_readlane_b32 s5, v251, 32
	v_ashrrev_i32_e32 v205, 4, v118
	s_or_b32 s4, s4, s9
	v_or_b32_e32 v209, s5, v180
	v_or_b32_e32 v196, s0, v209
	v_lshlrev_b32_e32 v202, 3, v205
	v_mov_b64_e32 v[160:161], s[80:81]
	s_movk_i32 s7, 0x2900
	s_ashr_i32 s5, s4, 31
	v_ashrrev_i32_e32 v203, 31, v202
	v_mad_i64_i32 v[198:199], s[12:13], v196, s7, v[160:161]
	s_lshl_b32 s96, s9, 8
	s_lshl_b64 s[4:5], s[4:5], 12
	s_lshl_b32 s1, s1, 7
	s_waitcnt lgkmcnt(0)
	v_lshl_add_u64 v[0:1], v[198:199], 0, s[96:97]
	v_lshlrev_b64 v[176:177], 1, v[202:203]
	s_or_b32 s1, s4, s1
	v_lshl_add_u64 v[8:9], v[0:1], 0, v[176:177]
	v_mov_b32_e32 v0, s1
	v_mov_b32_e32 v1, s5
	v_readlane_b32 s4, v253, 46
	v_lshlrev_b64 v[0:1], 8, v[0:1]
	v_readlane_b32 s5, v253, 47
	v_or_b32_e32 v194, 16, v196
	s_movk_i32 s6, 0x1000
	v_lshl_add_u64 v[0:1], s[4:5], 0, v[0:1]
	v_mad_i64_i32 v[200:201], s[4:5], v194, s7, v[160:161]
	v_add_co_u32_e32 v4, vcc, s6, v8
	s_mov_b64 s[4:5], 0x1000
	v_lshlrev_b32_e32 v2, 4, v180
	v_lshl_or_b32 v2, v205, 8, v2
	v_mov_b32_e32 v3, 0
	v_lshl_add_u64 v[36:37], v[0:1], 0, v[2:3]
	v_addc_co_u32_e32 v5, vcc, 0, v9, vcc
	v_lshl_add_u64 v[8:9], v[8:9], 0, s[4:5]
	global_load_dwordx4 v[0:3], v[36:37], off
	global_load_dwordx4 v[46:49], v[36:37], off offset:1024
	v_and_b32_e32 v242, -16, v196
	v_lshlrev_b32_e32 v242, 12, v242
	v_lshl_add_u32 v242, v180, 4, v242
	v_lshl_add_u32 v242, v205, 8, v242
	s_lshl_b32 s100, s9, 12
	v_add_u32_e32 v242, s100, v242
	v_add_u32_e32 v242, 0xe000000, v242
	v_mov_b32_e32 v243, 0
	v_mov_b32_e32 v238, s62
	v_mov_b32_e32 v239, s63
	v_lshl_add_u64 v[238:239], v[238:239], 0, v[242:243]
	v_mov_b32_e32 v242, 0x10000
	v_lshl_add_u64 v[240:241], v[238:239], 0, v[242:243]
	global_load_dwordx4 v[20:23], v[238:239], off
	global_load_dwordx4 v[52:55], v[238:239], off offset:1024
	v_lshl_add_u64 v[4:5], v[200:201], 0, s[96:97]
	v_lshl_add_u64 v[12:13], v[4:5], 0, v[176:177]
	v_add_co_u32_e32 v4, vcc, s6, v12
	v_lshl_add_u64 v[80:81], v[12:13], 0, s[4:5]
	s_nop 0
	v_addc_co_u32_e32 v5, vcc, 0, v13, vcc
	global_load_dwordx4 v[24:27], v[240:241], off
	global_load_dwordx4 v[60:63], v[238:239], off offset:2048
	global_load_dwordx4 v[56:59], v[240:241], off offset:1024
	global_load_dwordx4 v[64:67], v[240:241], off offset:2048
	s_movk_i32 s1, 0x2000
	v_add_co_u32_e32 v10, vcc, s1, v36
	s_movk_i32 s1, 0x4000
	s_nop 0
	v_addc_co_u32_e32 v11, vcc, 0, v37, vcc
	s_waitcnt lgkmcnt(0)
	global_load_dwordx4 v[14:17], v[10:11], off offset:-4096
	global_load_dwordx4 v[72:75], v[238:239], off offset:3072
	s_waitcnt vmcnt(19)
	v_add_co_u32_e32 v50, vcc, s1, v36
	global_load_dwordx4 v[28:31], v[10:11], off
	s_nop 0
	v_addc_co_u32_e32 v51, vcc, 0, v37, vcc
	v_add_co_u32_e32 v84, vcc, s6, v36
	global_load_dwordx4 v[38:41], v[50:51], off offset:-4096
	global_load_dwordx4 v[112:115], v[50:51], off offset:2048
	v_addc_co_u32_e32 v85, vcc, 0, v37, vcc
	s_movk_i32 s1, 0x3000
	v_lshlrev_b32_e32 v119, 1, v118
	v_and_b32_e32 v118, 3, v118
	s_mov_b64 s[10:11], 0x1800
	s_lshl_b32 s9, s9, 7
	v_or_b32_e32 v228, 16, v209
	v_mov_b32_e32 v210, v202
	v_mov_b32_e32 v195, v202
	s_waitcnt vmcnt(10)
	v_mfma_f32_16x16x32_bf16 v[4:7], v[0:3], v[20:23], 0
	global_load_dwordx4 v[80:83], v[240:241], off offset:3072
	s_waitcnt vmcnt(9)
	v_mfma_f32_16x16x32_bf16 v[0:3], v[0:3], v[24:27], 0
	v_mfma_f32_16x16x32_bf16 v[4:7], v[46:49], v[52:55], v[4:7]
	s_waitcnt vmcnt(7)
	v_mfma_f32_16x16x32_bf16 v[0:3], v[46:49], v[56:59], v[0:3]
	global_load_dwordx4 v[46:49], v[84:85], off offset:1024
	s_waitcnt vmcnt(6)
	v_mfma_f32_16x16x32_bf16 v[32:35], v[14:17], v[20:23], 0
	v_mfma_f32_16x16x32_bf16 v[14:17], v[14:17], v[24:27], 0
	s_waitcnt vmcnt(3)
	v_mfma_f32_16x16x32_bf16 v[68:71], v[38:41], v[20:23], 0
	s_waitcnt vmcnt(0)
	v_mfma_f32_16x16x32_bf16 v[12:15], v[46:49], v[56:59], v[14:17]
	s_nop 3
	global_load_dwordx4 v[16:19], v[10:11], off offset:1024
	v_mfma_f32_16x16x32_bf16 v[42:45], v[28:31], v[20:23], 0
	v_mfma_f32_16x16x32_bf16 v[28:31], v[28:31], v[24:27], 0
	v_mfma_f32_16x16x32_bf16 v[32:35], v[46:49], v[52:55], v[32:35]
	global_load_dwordx4 v[46:49], v[36:37], off offset:2048
	s_waitcnt vmcnt(1)
	v_mfma_f32_16x16x32_bf16 v[42:45], v[16:19], v[52:55], v[42:45]
	v_mfma_f32_16x16x32_bf16 v[16:19], v[16:19], v[56:59], v[28:31]
	s_nop 2
	global_load_dwordx4 v[28:31], v[84:85], off offset:2048
	s_waitcnt vmcnt(0)
	v_mfma_f32_16x16x32_bf16 v[76:79], v[28:31], v[64:67], v[12:15]
	s_nop 2
	global_load_dwordx4 v[12:15], v[36:37], off offset:3072
	v_mfma_f32_16x16x32_bf16 v[4:7], v[46:49], v[60:63], v[4:7]
	v_mfma_f32_16x16x32_bf16 v[0:3], v[46:49], v[64:67], v[0:3]
	v_mfma_f32_16x16x32_bf16 v[46:49], v[28:31], v[60:63], v[32:35]
	s_nop 2
	global_load_dwordx4 v[32:35], v[10:11], off offset:2048
	s_waitcnt vmcnt(1)
	v_mfma_f32_16x16x32_bf16 v[28:31], v[12:15], v[80:83], v[0:3]
	s_nop 2
	global_load_dwordx4 v[0:3], v[10:11], off offset:3072
	s_waitcnt vmcnt(1)
	v_mfma_f32_16x16x32_bf16 v[42:45], v[32:35], v[60:63], v[42:45]
	v_mfma_f32_16x16x32_bf16 v[16:19], v[32:35], v[64:67], v[16:19]
	v_mfma_f32_16x16x32_bf16 v[32:35], v[12:15], v[72:75], v[4:7]
	s_nop 2
	global_load_dwordx4 v[4:7], v[84:85], off offset:3072
	v_add_co_u32_e32 v84, vcc, s1, v36
	s_movk_i32 s1, 0x6000
	s_nop 0
	v_addc_co_u32_e32 v85, vcc, 0, v37, vcc
	s_waitcnt vmcnt(0)
; __device__ __forceinline__ f32x4 mfma16(bf16x8 a, bf16x8 b, f32x4 c) { return __builtin_amdgcn_mfma_f32_16x16x32_bf16(a, b, c, 0, 0, 0); }
; __device__ __forceinline__ void ret_task(const Frame& F, int l, int task) {
;     ...
;     bf16x8 Qf[2][4], Kf[2][2][4];
; #pragma unroll
;     for (int qb = 0; qb < 2; ++qb)
; #pragma unroll
;         for (int ks = 0; ks < 4; ++ks) Qf[qb][ks] = ld_b8(TOK + (size_t)(tq0 + qb * 16 + c) * TOKP + TK_QR + h * HD + ks * 32 + rq * 8);
; #pragma unroll
;     for (int g = 0; g < 2; ++g)
; #pragma unroll
;         for (int ab = 0; ab < 2; ++ab) { const int key = 32 * g + (c >> 2) * 8 + 4 * ab + (c & 3);
; #pragma unroll
;             for (int ks = 0; ks < 4; ++ks) Kf[g][ab][ks] = ld_b8(TOK + (size_t)(tc0 + key) * TOKP + TK_KR + h * HD + rq * 8 + ks * 32); }
;     f32x4 acc[2][8];
; #pragma unroll
;     for (int qb = 0; qb < 2; ++qb)
; #pragma unroll
;         for (int eb = 0; eb < 8; ++eb) acc[qb][eb] = (f32x4){0.f, 0.f, 0.f, 0.f};
;     const bf16* sp = ST + (((size_t)bhh * NCH + n) * HD + c) * HD + rq * 8;
; #pragma unroll
;     for (int eb = 0; eb < 8; ++eb)
; #pragma unroll
;         for (int ks = 0; ks < 4; ++ks) { const bf16x8 sf = ld_b8(sp + eb * 16 * HD + ks * 32);
; #pragma unroll
;             for (int qb = 0; qb < 2; ++qb) acc[qb][eb] = mfma16(sf, Qf[qb][ks], acc[qb][eb]); }
	v_mfma_f32_16x16x32_bf16 v[12:15], v[4:7], v[72:75], v[46:49]
	s_nop 2
	global_load_dwordx4 v[46:49], v[84:85], off offset:1024
	v_add_co_u32_e32 v116, vcc, s1, v36
	v_mfma_f32_16x16x32_bf16 v[8:11], v[4:7], v[80:83], v[76:79]
	s_nop 0
	v_addc_co_u32_e32 v117, vcc, 0, v37, vcc
	s_movk_i32 s1, 0x5000
	v_mfma_f32_16x16x32_bf16 v[4:7], v[0:3], v[72:75], v[42:45]
	global_load_dwordx4 v[76:79], v[84:85], off offset:3072
	global_load_dwordx4 v[92:95], v[116:117], off
	global_load_dwordx4 v[88:91], v[116:117], off offset:1024
	global_load_dwordx4 v[42:45], v[84:85], off offset:2048
	v_mfma_f32_16x16x32_bf16 v[0:3], v[0:3], v[80:83], v[16:19]
	global_load_dwordx4 v[108:111], v[116:117], off offset:-4096
	v_mfma_f32_16x16x32_bf16 v[16:19], v[38:41], v[24:27], 0
	s_waitcnt vmcnt(5)
	v_mfma_f32_16x16x32_bf16 v[38:41], v[46:49], v[52:55], v[68:71]
	s_nop 2
	global_load_dwordx4 v[68:71], v[50:51], off offset:1024
	global_load_dwordx4 v[84:87], v[50:51], off
	v_mfma_f32_16x16x32_bf16 v[16:19], v[46:49], v[56:59], v[16:19]
	s_waitcnt vmcnt(3)
	v_mfma_f32_16x16x32_bf16 v[38:41], v[42:45], v[60:63], v[38:41]
	v_mfma_f32_16x16x32_bf16 v[42:45], v[42:45], v[64:67], v[16:19]
	v_mfma_f32_16x16x32_bf16 v[16:19], v[76:79], v[72:75], v[38:41]
	s_nop 5
	v_add_co_u32_e32 v38, vcc, s1, v36
	v_mfma_f32_16x16x32_bf16 v[40:43], v[76:79], v[80:83], v[42:45]
	s_nop 0
	v_addc_co_u32_e32 v39, vcc, 0, v37, vcc
	global_load_dwordx4 v[96:99], v[38:39], off offset:3072
	global_load_dwordx4 v[104:107], v[38:39], off offset:1024
	global_load_dwordx4 v[100:103], v[38:39], off offset:2048
	s_waitcnt vmcnt(3)
	v_mfma_f32_16x16x32_bf16 v[44:47], v[84:87], v[20:23], 0
	global_load_dwordx4 v[48:51], v[50:51], off offset:3072
	s_movk_i32 s1, 0x7000
	v_mfma_f32_16x16x32_bf16 v[76:79], v[84:87], v[24:27], 0
	v_mfma_f32_16x16x32_bf16 v[44:47], v[68:71], v[52:55], v[44:47]
	v_mfma_f32_16x16x32_bf16 v[68:71], v[68:71], v[56:59], v[76:79]
	s_nop 5
	global_load_dwordx4 v[76:79], v[116:117], off offset:2048
	global_load_dwordx4 v[84:87], v[116:117], off offset:3072
	v_add_co_u32_e32 v116, vcc, s1, v36
	v_mfma_f32_16x16x32_bf16 v[44:47], v[112:115], v[60:63], v[44:47]
	s_nop 0
	v_addc_co_u32_e32 v117, vcc, 0, v37, vcc
	global_load_dwordx4 v[36:39], v[116:117], off offset:1024
	v_mfma_f32_16x16x32_bf16 v[112:115], v[112:115], v[64:67], v[68:71]
	s_ashr_i32 s1, s0, 31
	s_nop 1
	global_load_dwordx4 v[68:71], v[116:117], off
	s_waitcnt vmcnt(4)
	v_mfma_f32_16x16x32_bf16 v[44:47], v[48:51], v[72:75], v[44:47]
	v_mfma_f32_16x16x32_bf16 v[48:51], v[48:51], v[80:83], v[112:115]
	s_nop 2
	v_and_b32_e32 v112, 24, v119
	v_mfma_f32_16x16x32_bf16 v[120:123], v[108:111], v[20:23], 0
	v_or3_b32 v162, v118, v112, s0
	v_and_b32_e32 v242, -16, v162
	v_lshlrev_b32_e32 v242, 12, v242
	v_and_b32_e32 v243, 15, v162
	v_lshl_add_u32 v242, v243, 4, v242
	v_lshl_add_u32 v242, v205, 8, v242
	s_lshl_b32 s100, s9, 5
	s_add_i32 s100, s100, 0x8000
	v_add_u32_e32 v242, s100, v242
	v_add_u32_e32 v242, 0xe000000, v242
	v_mov_b32_e32 v243, 0
	v_mov_b32_e32 v244, s62
	v_mov_b32_e32 v245, s63
	v_lshl_add_u64 v[244:245], v[244:245], 0, v[242:243]
	v_mov_b32_e32 v242, 0x20000
	v_lshl_add_u64 v[246:247], v[244:245], 0, v[242:243]
	v_mad_i64_i32 v[118:119], s[4:5], v162, s7, v[160:161]
	v_mfma_f32_16x16x32_bf16 v[124:127], v[108:111], v[24:27], 0
	global_load_dwordx4 v[112:115], v[116:117], off offset:2048
	v_lshl_add_u64 v[118:119], v[118:119], 0, s[96:97]
	v_lshl_add_u64 v[128:129], v[118:119], 0, v[176:177]
	v_mfma_f32_16x16x32_bf16 v[120:123], v[104:107], v[52:55], v[120:123]
	v_add_co_u32_e32 v108, vcc, s6, v128
	v_mfma_f32_16x16x32_bf16 v[104:107], v[104:107], v[56:59], v[124:127]
	s_nop 0
	v_addc_co_u32_e32 v109, vcc, 0, v129, vcc
	v_lshl_add_u64 v[128:129], v[128:129], 0, s[10:11]
	v_or_b32_e32 v124, 4, v162
	v_mad_i64_i32 v[124:125], s[4:5], v124, s7, v[160:161]
	v_lshl_add_u64 v[124:125], v[124:125], 0, s[96:97]
	global_load_dwordx4 v[108:111], v[244:245], off
	v_lshl_add_u64 v[130:131], v[124:125], 0, v[176:177]
	global_load_dwordx4 v[124:127], v[244:245], off offset:1024
	v_mfma_f32_16x16x32_bf16 v[120:123], v[100:103], v[60:63], v[120:123]
	global_load_dwordx4 v[116:119], v[116:117], off offset:3072
	v_mfma_f32_16x16x32_bf16 v[100:103], v[100:103], v[64:67], v[104:107]
	s_nop 2
	v_add_co_u32_e32 v104, vcc, s6, v130
	v_mfma_f32_16x16x32_bf16 v[144:147], v[96:99], v[72:75], v[120:123]
	s_nop 0
	v_addc_co_u32_e32 v105, vcc, 0, v131, vcc
	v_or_b32_e32 v106, s9, v180
	global_load_dwordx4 v[120:123], v[244:245], off offset:64
	v_mfma_f32_16x16x32_bf16 v[148:151], v[96:99], v[80:83], v[100:103]
	global_load_dwordx4 v[168:171], v[244:245], off offset:2048
	global_load_dwordx4 v[96:99], v[244:245], off offset:3072
	v_mul_u32_u24_e32 v106, 0x4080, v106
	v_lshlrev_b32_e32 v184, 1, v106
	v_mfma_f32_16x16x32_bf16 v[100:103], v[92:95], v[20:23], 0
	v_or_b32_e32 v104, 32, v162
	v_lshl_add_u64 v[106:107], s[64:65], 0, v[184:185]
	v_mad_i64_i32 v[104:105], s[4:5], v104, s7, v[160:161]
	v_mfma_f32_16x16x32_bf16 v[92:95], v[92:95], v[24:27], 0
	v_lshl_add_u64 v[106:107], s[0:1], 1, v[106:107]
	v_lshl_add_u64 v[178:179], v[106:107], 0, v[176:177]
	s_mov_b32 s4, 0x23c7000
	v_mfma_f32_16x16x32_bf16 v[100:103], v[88:91], v[52:55], v[100:103]
	v_add_co_u32_e32 v106, vcc, s4, v178
	v_lshl_add_u64 v[128:129], v[130:131], 0, s[10:11]
	v_mfma_f32_16x16x32_bf16 v[88:91], v[88:91], v[56:59], v[92:95]
	v_addc_co_u32_e32 v107, vcc, 0, v179, vcc
	s_waitcnt vmcnt(10)
	v_mfma_f32_16x16x32_bf16 v[92:95], v[76:79], v[60:63], v[100:103]
	v_mfma_f32_16x16x32_bf16 v[100:103], v[76:79], v[64:67], v[88:91]
	global_load_dwordx4 v[76:79], v[106:107], off
	global_load_dwordx4 v[172:175], v[244:245], off offset:1088
	s_nop 1
	v_lshl_add_u64 v[88:89], v[104:105], 0, s[96:97]
	s_waitcnt vmcnt(11)
; __device__ __forceinline__ float fexp2(float x) { return __builtin_amdgcn_exp2f(x); }
; __device__ __forceinline__ void ret_task(const Frame& F, int l, int task) {
;     ...
;     for (int g = 0; g < 2; ++g)
; #pragma unroll
;         for (int ab = 0; ab < 2; ++ab) { const int key = 32 * g + (c >> 2) * 8 + 4 * ab + (c & 3);
; #pragma unroll
;             for (int ks = 0; ks < 4; ++ks) Kf[g][ab][ks] = ld_b8(TOK + (size_t)(tc0 + key) * TOKP + TK_KR + h * HD + rq * 8 + ks * 32); }
;     f32x4 acc[2][8];
; #pragma unroll
;     for (int qb = 0; qb < 2; ++qb)
; #pragma unroll
;         for (int eb = 0; eb < 8; ++eb) acc[qb][eb] = (f32x4){0.f, 0.f, 0.f, 0.f};
;     const bf16* sp = ST + (((size_t)bhh * NCH + n) * HD + c) * HD + rq * 8;
; #pragma unroll
;     for (int eb = 0; eb < 8; ++eb)
; #pragma unroll
;         for (int ks = 0; ks < 4; ++ks) { const bf16x8 sf = ld_b8(sp + eb * 16 * HD + ks * 32);
; #pragma unroll
;             for (int qb = 0; qb < 2; ++qb) acc[qb][eb] = mfma16(sf, Qf[qb][ks], acc[qb][eb]); }
;     bf16x8 Vf[8];
; #pragma unroll
;     for (int eb = 0; eb < 8; ++eb) Vf[eb] = ld_b8(SWP + (size_t)(SW_VR + h * HD + eb * 16 + c) * SWPP + tc0 + 8 * rq);
; #pragma unroll
;     for (int qb = 0; qb < 2; ++qb) { const float f = fexp2((float)(qb2 * 32 + qb * 16 + c + 1) * lg);
; #pragma unroll
;         for (int eb = 0; eb < 8; ++eb) acc[qb][eb] *= f; }
;     f32x4 g4[8]; u32x2 gwq[2][8];
; #pragma unroll
;     for (int g = 0; g < 2; ++g) {
;         if (g <= qb2) {
;             f32x4 sa[2][2];
; #pragma unroll
;             for (int qb = 0; qb < 2; ++qb)
; #pragma unroll
;                 for (int ab = 0; ab < 2; ++ab) sa[qb][ab] = (f32x4){0.f, 0.f, 0.f, 0.f};
; #pragma unroll
;             for (int ab = 0; ab < 2; ++ab)
; #pragma unroll
;                 for (int ks = 0; ks < 4; ++ks)
; #pragma unroll
;                     for (int qb = 0; qb < 2; ++qb) sa[qb][ab] = mfma16(Kf[g][ab][ks], Qf[qb][ks], sa[qb][ab]);
;             bf16x8 Pf[2];
; #pragma unroll
;             for (int qb = 0; qb < 2; ++qb) {
;                 const int i = qb2 * 32 + qb * 16 + c;
; #pragma unroll
;                 for (int ab = 0; ab < 2; ++ab)
; #pragma unroll
;                     for (int e = 0; e < 4; ++e) { const int diff = i - (32 * g + 8 * rq + 4 * ab + e);
;                         sa[qb][ab][e] = diff >= 0 ? sa[qb][ab][e] * fexp2((float)diff * lg) : 0.f; }
	v_mfma_f32_16x16x32_bf16 v[152:155], v[84:87], v[72:75], v[92:95]
	v_lshl_add_u64 v[104:105], v[88:89], 0, v[176:177]
	global_load_dwordx4 v[88:91], v[244:245], off offset:3136
	v_lshl_add_u64 v[106:107], v[104:105], 0, s[10:11]
	v_mfma_f32_16x16x32_bf16 v[156:159], v[84:87], v[80:83], v[100:103]
	global_load_dwordx4 v[84:87], v[244:245], off offset:2112
	v_add_co_u32_e32 v104, vcc, s6, v104
	s_waitcnt vmcnt(11)
	v_mfma_f32_16x16x32_bf16 v[92:95], v[68:71], v[20:23], 0
	v_addc_co_u32_e32 v105, vcc, 0, v105, vcc
	global_load_dwordx4 v[132:135], v[246:247], off offset:1024
	global_load_dwordx4 v[128:131], v[246:247], off offset:2048
	v_mfma_f32_16x16x32_bf16 v[100:103], v[68:71], v[24:27], 0
	v_or_b32_e32 v68, 36, v162
	v_mad_i64_i32 v[68:69], s[4:5], v68, s7, v[160:161]
	v_mfma_f32_16x16x32_bf16 v[92:95], v[36:39], v[52:55], v[92:95]
	s_mov_b32 s4, 0x2040000
	v_add_co_u32_e32 v70, vcc, s4, v178
	v_mfma_f32_16x16x32_bf16 v[36:39], v[36:39], v[56:59], v[100:103]
	s_nop 0
	v_addc_co_u32_e32 v71, vcc, 0, v179, vcc
	s_mov_b32 s4, 0x20c1000
	s_waitcnt vmcnt(12)
	v_mfma_f32_16x16x32_bf16 v[36:39], v[112:115], v[64:67], v[36:39]
	global_load_dwordx4 v[140:143], v[246:247], off
	global_load_dwordx4 v[136:139], v[246:247], off offset:3072
	v_lshl_add_u64 v[68:69], v[68:69], 0, s[96:97]
	v_lshl_add_u64 v[68:69], v[68:69], 0, v[176:177]
	v_mfma_f32_16x16x32_bf16 v[100:103], v[112:115], v[60:63], v[92:95]
	s_nop 2
	global_load_dwordx4 v[92:95], v[70:71], off
	v_add_co_u32_e32 v70, vcc, s4, v178
	s_mov_b32 s4, 0x2142000
	s_nop 0
	v_addc_co_u32_e32 v71, vcc, 0, v179, vcc
	v_add_co_u32_e32 v104, vcc, s4, v178
	s_waitcnt vmcnt(12)
	v_mfma_f32_16x16x32_bf16 v[164:167], v[116:119], v[80:83], v[36:39]
	v_addc_co_u32_e32 v105, vcc, 0, v179, vcc
	s_mov_b32 s4, 0x21c3000
	v_mfma_f32_16x16x32_bf16 v[36:39], v[108:111], v[20:23], 0
	v_mfma_f32_16x16x32_bf16 v[108:111], v[108:111], v[24:27], 0
	v_mfma_f32_16x16x32_bf16 v[160:163], v[116:119], v[72:75], v[100:103]
	s_nop 2
	global_load_dwordx4 v[100:103], v[70:71], off
	s_nop 0
	global_load_dwordx4 v[104:107], v[104:105], off
	v_add_co_u32_e32 v70, vcc, s4, v178
	s_mov_b32 s4, 0x2244000
	s_nop 0
	v_addc_co_u32_e32 v71, vcc, 0, v179, vcc
	v_add_co_u32_e32 v116, vcc, s4, v178
	v_readlane_b32 s4, v251, 33
	s_nop 0
	v_addc_co_u32_e32 v117, vcc, 0, v179, vcc
	v_mfma_f32_16x16x32_bf16 v[36:39], v[124:127], v[52:55], v[36:39]
	global_load_dwordx4 v[112:115], v[70:71], off
	s_nop 0
	global_load_dwordx4 v[116:119], v[116:117], off
	v_add_u32_e32 v70, s4, v180
	v_cvt_f32_ubyte0_e32 v71, v70
	v_mfma_f32_16x16x32_bf16 v[108:111], v[124:127], v[56:59], v[108:111]
	v_add_u32_e32 v70, 16, v70
	v_cvt_f32_ubyte0_e32 v70, v70
	v_or_b32_e32 v126, 2, v202
	v_mul_f32_e32 v71, v197, v71
	v_mul_f32_e32 v70, v197, v70
	s_waitcnt vmcnt(14)
	v_mfma_f32_16x16x32_bf16 v[36:39], v[168:171], v[60:63], v[36:39]
	v_exp_f32_e32 v204, v71
	v_exp_f32_e32 v206, v70
	v_or_b32_e32 v127, 3, v202
	v_mfma_f32_16x16x32_bf16 v[108:111], v[168:171], v[64:67], v[108:111]
	v_sub_u32_e32 v169, v209, v202
	v_sub_u32_e32 v170, v209, v126
	v_cvt_f32_u32_e32 v70, v169
	v_cvt_f32_u32_e32 v71, v170
	s_waitcnt vmcnt(13)
	v_mfma_f32_16x16x32_bf16 v[36:39], v[96:99], v[72:75], v[36:39]
	v_or_b32_e32 v168, 1, v202
	v_mul_f32_e32 v70, v197, v70
	v_mul_f32_e32 v71, v197, v71
	v_exp_f32_e32 v70, v70
	v_exp_f32_e32 v71, v71
	v_mfma_f32_16x16x32_bf16 v[96:99], v[96:99], v[80:83], v[108:111]
	s_nop 1
	v_mov_b32_e32 v124, v36
	v_mov_b32_e32 v125, v38
	v_pk_mul_f32 v[70:71], v[70:71], v[124:125]
	v_mfma_f32_16x16x32_bf16 v[108:111], v[120:123], v[20:23], 0
	v_cmp_lt_i32_e32 vcc, -1, v170
	v_sub_u32_e32 v125, v209, v127
	v_cvt_f32_u32_e32 v38, v125
	v_mfma_f32_16x16x32_bf16 v[120:123], v[120:123], v[24:27], 0
	v_cndmask_b32_e32 v124, 0, v71, vcc
	v_sub_u32_e32 v71, v209, v168
	v_cvt_f32_u32_e32 v36, v71
	s_waitcnt vmcnt(11)
	v_mfma_f32_16x16x32_bf16 v[108:111], v[172:175], v[52:55], v[108:111]
	v_cmp_lt_i32_e32 vcc, -1, v169
	v_pk_mul_f32 v[14:15], v[204:205], v[14:15] op_sel_hi:[0,1]
	v_mul_f32_e32 v36, v197, v36
	v_mfma_f32_16x16x32_bf16 v[120:123], v[172:175], v[56:59], v[120:123]
	v_mul_f32_e64 v12, v204, v12
	v_mul_f32_e64 v13, v204, v13
	s_mov_b32 s4, 0x22c5000
	v_pk_mul_f32 v[6:7], v[204:205], v[6:7] op_sel_hi:[0,1]
	s_waitcnt vmcnt(9)
; __device__ __forceinline__ f32x4 mfma16(bf16x8 a, bf16x8 b, f32x4 c) { return __builtin_amdgcn_mfma_f32_16x16x32_bf16(a, b, c, 0, 0, 0); }
; __device__ __forceinline__ float fexp2(float x) { return __builtin_amdgcn_exp2f(x); }
; __device__ __forceinline__ void ret_task(const Frame& F, int l, int task) {
;     ...
;     for (int qb = 0; qb < 2; ++qb) { const float f = fexp2((float)(qb2 * 32 + qb * 16 + c + 1) * lg);
; #pragma unroll
;         for (int eb = 0; eb < 8; ++eb) acc[qb][eb] *= f; }
;     f32x4 g4[8]; u32x2 gwq[2][8];
; #pragma unroll
;     for (int g = 0; g < 2; ++g) {
;         if (g <= qb2) {
;             f32x4 sa[2][2];
; #pragma unroll
;             for (int qb = 0; qb < 2; ++qb)
; #pragma unroll
;                 for (int ab = 0; ab < 2; ++ab) sa[qb][ab] = (f32x4){0.f, 0.f, 0.f, 0.f};
; #pragma unroll
;             for (int ab = 0; ab < 2; ++ab)
; #pragma unroll
;                 for (int ks = 0; ks < 4; ++ks)
; #pragma unroll
;                     for (int qb = 0; qb < 2; ++qb) sa[qb][ab] = mfma16(Kf[g][ab][ks], Qf[qb][ks], sa[qb][ab]);
;             bf16x8 Pf[2];
; #pragma unroll
;             for (int qb = 0; qb < 2; ++qb) {
;                 const int i = qb2 * 32 + qb * 16 + c;
; #pragma unroll
;                 for (int ab = 0; ab < 2; ++ab)
; #pragma unroll
;                     for (int e = 0; e < 4; ++e) { const int diff = i - (32 * g + 8 * rq + 4 * ab + e);
;                         sa[qb][ab][e] = diff >= 0 ? sa[qb][ab][e] * fexp2((float)diff * lg) : 0.f; }
;                 Pf[qb] = pack8(sa[qb][0], sa[qb][1]);
;             }
; #pragma unroll
;             for (int eb = 0; eb < 8; ++eb)
; #pragma unroll
;                 for (int qb = 0; qb < 2; ++qb) acc[qb][eb] = mfma16(Vf[eb], Pf[qb], acc[qb][eb]);
	v_mfma_f32_16x16x32_bf16 v[108:111], v[84:87], v[60:63], v[108:111]
	v_mul_f32_e64 v4, v204, v4
	v_mul_f32_e64 v5, v204, v5
	v_pk_mul_f32 v[30:31], v[206:207], v[30:31] op_sel_hi:[0,1]
	v_pk_mul_f32 v[28:29], v[206:207], v[28:29] op_sel_hi:[0,1]
	v_mfma_f32_16x16x32_bf16 v[84:87], v[84:87], v[64:67], v[120:123]
	v_mul_f32_e64 v2, v206, v2
	v_mul_f32_e64 v3, v206, v3
	v_pk_mul_f32 v[0:1], v[206:207], v[0:1] op_sel_hi:[0,1]
	v_pk_mul_f32 v[34:35], v[204:205], v[34:35] op_sel_hi:[0,1]
	v_exp_f32_e32 v120, v36
	v_mul_f32_e32 v36, v197, v38
	v_exp_f32_e32 v121, v36
	v_mov_b32_e32 v38, v37
	v_cndmask_b32_e32 v122, 0, v70, vcc
	v_cmp_lt_i32_e32 vcc, -1, v71
	v_pk_mul_f32 v[36:37], v[120:121], v[38:39]
	v_mfma_f32_16x16x32_bf16 v[108:111], v[88:91], v[72:75], v[108:111]
	v_sub_u32_e32 v39, v228, v126
	v_cvt_f32_u32_e32 v70, v39
	v_sub_u32_e32 v120, v228, v127
	v_mfma_f32_16x16x32_bf16 v[84:87], v[88:91], v[80:83], v[84:87]
	v_cndmask_b32_e32 v88, 0, v36, vcc
	v_cmp_lt_i32_e32 vcc, -1, v125
	v_sub_u32_e32 v91, v228, v168
	v_sub_u32_e32 v89, v228, v202
	v_cndmask_b32_e32 v90, 0, v37, vcc
	v_cvt_f32_u32_e32 v37, v91
	v_cvt_f32_u32_e32 v36, v89
	v_mov_b32_e32 v71, v98
	v_cmp_lt_i32_e32 vcc, -1, v39
	v_mul_f32_e32 v37, v197, v37
	v_mul_f32_e32 v36, v197, v36
	v_exp_f32_e32 v38, v37
	v_mul_f32_e32 v37, v197, v70
	v_exp_f32_e32 v36, v36
	v_exp_f32_e32 v37, v37
	v_mov_b32_e32 v70, v96
	v_cvt_f32_u32_e32 v96, v120
	v_mov_b32_e32 v98, v97
	v_pk_mul_f32 v[36:37], v[36:37], v[70:71]
	v_or_b32_e32 v123, 5, v202
	v_cndmask_b32_e32 v121, 0, v37, vcc
	v_mul_f32_e32 v37, v197, v96
	v_exp_f32_e32 v39, v37
	v_cmp_lt_i32_e32 vcc, -1, v89
	v_or_b32_e32 v97, 6, v202
	v_sub_u32_e32 v125, v209, v123
	v_cndmask_b32_e32 v89, 0, v36, vcc
	v_pk_mul_f32 v[36:37], v[38:39], v[98:99]
	v_cmp_lt_i32_e32 vcc, -1, v91
	v_or_b32_e32 v98, 4, v202
	v_sub_u32_e32 v99, v209, v98
	v_cndmask_b32_e32 v91, 0, v36, vcc
	v_cmp_lt_i32_e32 vcc, -1, v120
	v_sub_u32_e32 v39, v209, v97
	v_cvt_f32_u32_e32 v36, v99
	v_cndmask_b32_e32 v96, 0, v37, vcc
	v_cvt_f32_u32_e32 v37, v125
	v_cvt_f32_u32_e32 v70, v39
	v_or_b32_e32 v120, 7, v202
	v_mul_f32_e32 v36, v197, v36
	v_mul_f32_e32 v37, v197, v37
	v_exp_f32_e32 v38, v37
	v_mul_f32_e32 v37, v197, v70
	v_exp_f32_e32 v36, v36
	v_sub_u32_e32 v126, v209, v120
	v_exp_f32_e32 v37, v37
	v_mov_b32_e32 v70, v108
	v_cvt_f32_u32_e32 v108, v126
	v_mov_b32_e32 v71, v110
	v_pk_mul_f32 v[36:37], v[36:37], v[70:71]
	v_cmp_lt_i32_e32 vcc, -1, v39
	v_mov_b32_e32 v110, v109
	v_sub_u32_e32 v98, v228, v98
	v_cndmask_b32_e32 v127, 0, v37, vcc
	v_mul_f32_e32 v37, v197, v108
	v_exp_f32_e32 v39, v37
	v_cmp_lt_i32_e32 vcc, -1, v99
	v_mov_b32_e32 v71, v86
	v_mov_b32_e32 v86, v85
	v_cndmask_b32_e32 v99, 0, v36, vcc
	v_pk_mul_f32 v[36:37], v[38:39], v[110:111]
	v_cmp_lt_i32_e32 vcc, -1, v125
	v_sub_u32_e32 v39, v228, v97
	v_sub_u32_e32 v97, v228, v123
	v_cndmask_b32_e32 v108, 0, v36, vcc
	v_cmp_lt_i32_e32 vcc, -1, v126
	v_cvt_f32_u32_e32 v36, v98
	v_cvt_f32_u32_e32 v70, v39
	v_cndmask_b32_e32 v109, 0, v37, vcc
	v_cvt_f32_u32_e32 v37, v97
	v_mul_f32_e32 v36, v197, v36
	v_exp_f32_e32 v36, v36
	v_sub_u32_e32 v110, v228, v120
	v_mul_f32_e32 v37, v197, v37
	v_exp_f32_e32 v38, v37
	v_mul_f32_e32 v37, v197, v70
	v_exp_f32_e32 v37, v37
	v_mov_b32_e32 v70, v84
	v_cvt_f32_u32_e32 v84, v110
	v_cmp_lt_i32_e32 vcc, -1, v39
	v_pk_mul_f32 v[36:37], v[36:37], v[70:71]
	s_nop 0
	v_cndmask_b32_e32 v70, 0, v37, vcc
	v_mul_f32_e32 v37, v197, v84
	v_exp_f32_e32 v39, v37
	v_cmp_lt_i32_e32 vcc, -1, v98
	s_nop 1
	v_cndmask_b32_e32 v71, 0, v36, vcc
	v_pk_mul_f32 v[36:37], v[38:39], v[86:87]
	v_bfe_u32 v38, v90, 16, 1
	v_bfe_u32 v39, v88, 16, 1
	v_add3_u32 v39, v88, v39, s76
	v_add3_u32 v38, v90, v38, s76
	s_nop 1
	v_bfe_u32 v88, v122, 16, 1
	v_bfe_u32 v90, v124, 16, 1
	v_cmp_lt_i32_e32 vcc, -1, v97
	v_add3_u32 v90, v124, v90, s76
	v_add3_u32 v88, v122, v88, s76
	s_nop 1
	v_cndmask_b32_e32 v36, 0, v36, vcc
	v_cmp_lt_i32_e32 vcc, -1, v110
	s_nop 2
	v_lshrrev_b32_e32 v88, 16, v88
	v_lshrrev_b32_e32 v90, 16, v90
	v_cndmask_b32_e32 v37, 0, v37, vcc
	v_and_or_b32 v231, v38, s75, v90
	v_and_or_b32 v230, v39, s75, v88
	v_cvt_pk_bf16_f32 v233, v127, v109
	v_cvt_pk_bf16_f32 v232, v99, v108
	v_bfe_u32 v84, v96, 16, 1
	v_bfe_u32 v38, v37, 16, 1
	v_add3_u32 v84, v96, v84, s76
	s_waitcnt vmcnt(3)
	v_mfma_f32_16x16x32_bf16 v[96:99], v[100:103], v[230:233], v[12:15]
	v_bfe_u32 v39, v36, 16, 1
	v_bfe_u32 v85, v91, 16, 1
	v_add3_u32 v37, v37, v38, s76
	v_add_co_u32_e32 v12, vcc, s4, v178
	v_bfe_u32 v38, v89, 16, 1
	s_nop 0
	v_addc_co_u32_e32 v13, vcc, 0, v179, vcc
	s_mov_b32 s4, 0x2346000
	v_add3_u32 v85, v91, v85, s76
	v_add3_u32 v36, v36, v39, s76
	v_bfe_u32 v39, v121, 16, 1
	v_add3_u32 v38, v89, v38, s76
	s_waitcnt vmcnt(2)
; __device__ __forceinline__ f32x4 mfma16(bf16x8 a, bf16x8 b, f32x4 c) { return __builtin_amdgcn_mfma_f32_16x16x32_bf16(a, b, c, 0, 0, 0); }
; __device__ __forceinline__ void ret_task(const Frame& F, int l, int task) {
;     ...
;     for (int g = 0; g < 2; ++g)
; #pragma unroll
;         for (int ab = 0; ab < 2; ++ab) { const int key = 32 * g + (c >> 2) * 8 + 4 * ab + (c & 3);
; #pragma unroll
;             for (int ks = 0; ks < 4; ++ks) Kf[g][ab][ks] = ld_b8(TOK + (size_t)(tc0 + key) * TOKP + TK_KR + h * HD + rq * 8 + ks * 32); }
;     ...
; #pragma unroll
;             for (int eb = 0; eb < 8; ++eb)
; #pragma unroll
;                 for (int qb = 0; qb < 2; ++qb) acc[qb][eb] = mfma16(Vf[eb], Pf[qb], acc[qb][eb]);
;         }
;         if (g == 0) {
;             if (qb2) {
; #pragma unroll
;                 for (int eb = 0; eb < 8; ++eb) Vf[eb] = ld_b8(SWP + (size_t)(SW_VR + h * HD + eb * 16 + c) * SWPP + tc0 + 32 + 8 * rq);
;             }
; #pragma unroll
;             for (int eb = 0; eb < 8; ++eb) { const int e0 = h * HD + eb * 16 + rq * 4;
; #pragma unroll
;                 for (int qb = 0; qb < 2; ++qb) gwq[qb][eb] = ld_u2(TOK + (size_t)(tq0 + qb * 16 + c) * TOKP + TK_GR + e0); }
	v_mfma_f32_16x16x32_bf16 v[88:91], v[104:107], v[230:233], v[4:7]
	v_add3_u32 v39, v121, v39, s76
	global_load_dwordx4 v[120:123], v[12:13], off
	v_bfe_u32 v86, v71, 16, 1
	v_add_co_u32_e32 v4, vcc, s4, v178
	v_bfe_u32 v87, v70, 16, 1
	s_nop 0
	v_addc_co_u32_e32 v5, vcc, 0, v179, vcc
	global_load_dwordx4 v[124:127], v[4:5], off
	v_add_co_u32_e32 v6, vcc, s6, v68
	v_lshl_add_u64 v[4:5], v[68:69], 0, s[10:11]
	s_nop 0
	v_addc_co_u32_e32 v7, vcc, 0, v69, vcc
	global_load_dwordx4 v[172:175], v[246:247], off offset:1088
	global_load_dwordx4 v[168:171], v[246:247], off offset:2112
	global_load_dwordx4 v[180:183], v[246:247], off offset:64
	global_load_dwordx4 v[176:179], v[246:247], off offset:3136
	v_add3_u32 v70, v70, v87, s76
	v_add3_u32 v71, v71, v86, s76
	v_lshrrev_b32_e32 v38, 16, v38
	v_lshrrev_b32_e32 v39, 16, v39
	v_lshrrev_b32_e32 v71, 16, v71
	v_lshrrev_b32_e32 v70, 16, v70
	v_and_or_b32 v237, v37, s75, v70
	v_and_or_b32 v236, v36, s75, v71
	v_and_or_b32 v235, v84, s75, v39
	v_and_or_b32 v234, v85, s75, v38
	v_readlane_b32 s4, v251, 34
	v_pk_mul_f32 v[32:33], v[204:205], v[32:33] op_sel_hi:[0,1]
	v_mfma_f32_16x16x32_bf16 v[36:39], v[92:95], v[234:237], v[28:31]
	v_mul_f32_e64 v10, v206, v10
	v_mul_f32_e64 v11, v206, v11
	v_pk_mul_f32 v[8:9], v[206:207], v[8:9] op_sel_hi:[0,1]
	v_pk_mul_f32 v[6:7], v[206:207], v[150:151] op_sel_hi:[0,1]
	v_mfma_f32_16x16x32_bf16 v[28:31], v[104:107], v[234:237], v[0:3]
	v_mul_f32_e64 v4, v206, v148
	v_mul_f32_e64 v5, v206, v149
	v_readlane_b32 s5, v251, 35
	s_andn2_b64 vcc, exec, s[4:5]
	v_pk_mul_f32 v[2:3], v[204:205], v[18:19] op_sel_hi:[0,1]
	v_pk_mul_f32 v[0:1], v[204:205], v[16:17] op_sel_hi:[0,1]
	v_mfma_f32_16x16x32_bf16 v[108:111], v[92:95], v[230:233], v[32:35]
	s_waitcnt vmcnt(7)
	v_mfma_f32_16x16x32_bf16 v[84:87], v[112:115], v[230:233], v[0:3]
	s_nop 2
	v_mul_f32_e64 v2, v206, v42
	v_mul_f32_e64 v3, v206, v43
	v_pk_mul_f32 v[0:1], v[206:207], v[40:41] op_sel_hi:[0,1]
	v_mfma_f32_16x16x32_bf16 v[32:35], v[100:103], v[234:237], v[8:11]
	v_mul_f32_e64 v42, v204, v162
	v_mul_f32_e64 v43, v204, v163
	v_pk_mul_f32 v[40:41], v[204:205], v[160:161] op_sel_hi:[0,1]
	v_mfma_f32_16x16x32_bf16 v[16:19], v[112:115], v[234:237], v[0:3]
	s_nop 2
	v_mul_f32_e64 v2, v204, v46
	v_mul_f32_e64 v3, v204, v47
	v_pk_mul_f32 v[0:1], v[204:205], v[44:45] op_sel_hi:[0,1]
	s_waitcnt vmcnt(5)
	v_mfma_f32_16x16x32_bf16 v[8:11], v[120:123], v[234:237], v[4:7]
	v_mfma_f32_16x16x32_bf16 v[68:71], v[116:119], v[230:233], v[0:3]
	s_nop 2
	v_mul_f32_e64 v2, v206, v50
	v_mul_f32_e64 v3, v206, v51
	v_pk_mul_f32 v[0:1], v[206:207], v[48:49] op_sel_hi:[0,1]
	v_mfma_f32_16x16x32_bf16 v[40:43], v[76:79], v[230:233], v[40:43]
	s_nop 0
	v_mfma_f32_16x16x32_bf16 v[12:15], v[116:119], v[234:237], v[0:3]
	s_nop 2
	v_mul_f32_e64 v2, v204, v146
	v_mul_f32_e64 v3, v204, v147
	v_pk_mul_f32 v[0:1], v[204:205], v[144:145] op_sel_hi:[0,1]
	v_pk_mul_f32 v[146:147], v[206:207], v[166:167] op_sel_hi:[0,1]
	v_pk_mul_f32 v[144:145], v[206:207], v[164:165] op_sel_hi:[0,1]
	v_mfma_f32_16x16x32_bf16 v[48:51], v[120:123], v[230:233], v[0:3]
	s_nop 2
	v_mul_f32_e64 v2, v204, v154
	v_mul_f32_e64 v3, v204, v155
	v_pk_mul_f32 v[0:1], v[204:205], v[152:153] op_sel_hi:[0,1]
	s_waitcnt vmcnt(4)
	s_nop 0
	v_mfma_f32_16x16x32_bf16 v[44:47], v[124:127], v[230:233], v[0:3]
	s_nop 2
	v_mul_f32_e64 v2, v206, v158
	v_mul_f32_e64 v3, v206, v159
	v_pk_mul_f32 v[0:1], v[206:207], v[156:157] op_sel_hi:[0,1]
	s_nop 1
	v_mfma_f32_16x16x32_bf16 v[4:7], v[124:127], v[234:237], v[0:3]
	s_nop 2
	v_cndmask_b32_e64 v0, 0, 1, s[4:5]
	v_cmp_ne_u32_e64 s[34:35], 1, v0
	v_mfma_f32_16x16x32_bf16 v[0:3], v[76:79], v[234:237], v[144:147]
	s_cbranch_vccnz .LBB0_657
	s_lshl_b64 s[0:1], s[0:1], 1
	s_add_u32 s0, s64, s0
	s_addc_u32 s1, s65, s1
	v_lshl_add_u64 v[76:77], s[0:1], 0, v[184:185]
	v_lshl_add_u64 v[76:77], v[202:203], 1, v[76:77]
	v_add_co_u32_e32 v78, vcc, 0x2040000, v76
	s_nop 1
	v_addc_co_u32_e32 v79, vcc, 0, v77, vcc
	v_add_co_u32_e32 v100, vcc, 0x20c1000, v76
	s_nop 1
	v_addc_co_u32_e32 v101, vcc, 0, v77, vcc
	global_load_dwordx4 v[92:95], v[78:79], off offset:64
	s_nop 0
	global_load_dwordx4 v[100:103], v[100:101], off offset:64
	v_add_co_u32_e32 v78, vcc, 0x2142000, v76
	s_nop 1
	v_addc_co_u32_e32 v79, vcc, 0, v77, vcc
	v_add_co_u32_e32 v112, vcc, 0x21c3000, v76
	s_nop 1
	v_addc_co_u32_e32 v113, vcc, 0, v77, vcc
	global_load_dwordx4 v[104:107], v[78:79], off offset:64
	s_nop 0
	global_load_dwordx4 v[112:115], v[112:113], off offset:64
	v_add_co_u32_e32 v78, vcc, 0x2244000, v76
	s_nop 1
	v_addc_co_u32_e32 v79, vcc, 0, v77, vcc
	v_add_co_u32_e32 v120, vcc, 0x22c5000, v76
	s_nop 1
	v_addc_co_u32_e32 v121, vcc, 0, v77, vcc
	global_load_dwordx4 v[116:119], v[78:79], off offset:64
	s_nop 0
	global_load_dwordx4 v[120:123], v[120:121], off offset:64
	v_add_co_u32_e32 v78, vcc, 0x2346000, v76
	s_nop 1
	v_addc_co_u32_e32 v79, vcc, 0, v77, vcc
	v_add_co_u32_e32 v76, vcc, 0x23c7000, v76
	s_nop 1
	v_addc_co_u32_e32 v77, vcc, 0, v77, vcc
	global_load_dwordx4 v[124:127], v[78:79], off offset:64
	s_nop 0
	global_load_dwordx4 v[76:79], v[76:77], off offset:64
